# experts 10-17 fp8 conversion moved from the Hyena barrier hook into the mLSTM chunk loop (per-wave half-items), hook stores without nt
# speedup vs baseline: 1.0053x; 1.0053x over previous
.LBB0_698:
	s_cmp_gt_u32 s72, 4
	s_cbranch_scc1 .Lmlh_top_nowait
	s_waitcnt vmcnt(0)
.Lmlh_top_nowait:
	s_cmp_gt_u32 s72, 3
	s_mov_b64 s[48:49], -1
	ds_write_b128 v120, v[8:11]
	ds_write_b128 v120, v[12:15] offset:33792
	ds_write_b128 v122, v[16:19]
	ds_write_b128 v122, v[20:23] offset:33792
	ds_write_b128 v124, v[24:27]
	ds_write_b128 v124, v[28:31] offset:33792
	ds_write_b128 v126, v[32:35]
	ds_write_b128 v126, v[36:39] offset:33792
	ds_write_b128 v150, v[40:43]
	ds_write_b16 v151, v40
	ds_write_b16_d16_hi v151, v40 offset:144
	ds_write_b16 v151, v41 offset:288
	ds_write_b16_d16_hi v151, v41 offset:432
	ds_write_b16 v151, v42 offset:576
	ds_write_b16_d16_hi v151, v42 offset:720
	ds_write_b16 v151, v43 offset:864
	ds_write_b16_d16_hi v151, v43 offset:1008
	s_cbranch_scc0 .LBB0_700
	s_add_i32 s1, s95, 1
	s_add_i32 s11, s72, -4
	s_and_b64 s[48:49], s[52:53], exec
	s_cselect_b32 s1, s11, s1
	s_lshl_b32 s1, s1, 6
	s_add_i32 s73, s1, s94
	s_mov_b64 s[48:49], 0

.LBB0_734:
	s_cmp_lg_u32 s11, 5
	s_cbranch_scc1 .Lmlh_init_done
	v_writelane_b32 v254, s12, 0
	v_writelane_b32 v254, s13, 1
	v_writelane_b32 v254, s14, 2
	v_writelane_b32 v254, s15, 3
	v_writelane_b32 v254, s16, 4
	v_writelane_b32 v254, s17, 5
	v_writelane_b32 v254, s18, 6
	v_writelane_b32 v254, s19, 7
	v_readlane_b32 s12, v255, 2
	v_readlane_b32 s14, v255, 12
	v_readlane_b32 s15, v255, 13
	s_lshr_b32 s12, s12, 6
	s_mul_i32 s16, s12, 0x500
	s_add_i32 s16, s16, 0x23300
	s_lshl_b32 s13, s2, 3
	s_add_i32 s12, s12, s13
	s_and_b32 s13, s12, 0x7f
	s_bitcmp1_b32 s13, 2
	s_movk_i32 s17, 0xf0
	s_cselect_b32 s17, 0x100, s17
	s_add_u32 s18, s14, s17
	s_addc_u32 s19, s15, 0
	s_load_dwordx2 s[18:19], s[18:19], 0x0
	s_load_dwordx2 s[14:15], s[14:15], 0x110
	s_lshr_b32 s17, s13, 3
	s_lshl_b32 s17, s17, 9
	s_and_b32 s98, s13, 3
	s_lshl_b32 s98, s98, 7
	s_or_b32 s17, s17, s98
	s_lshr_b32 s98, s12, 7
	s_lshl_b32 s99, s98, 19
	s_or_b32 s17, s17, s99
	s_lshl_b32 s99, s13, 16
	s_lshl_b32 s98, s98, 6
	s_or_b32 s99, s99, s98
	s_waitcnt lgkmcnt(0)
	s_add_u32 s18, s18, s17
	s_addc_u32 s19, s19, 0
	v_writelane_b32 v249, s18, 0
	v_writelane_b32 v249, s19, 1
	s_lshr_b32 s17, s12, 6
	s_and_b32 s13, s12, 0x3f
	s_lshl_b32 s98, s17, 19
	s_lshl_b32 s18, s13, 7
	s_or_b32 s98, s98, s18
	s_add_u32 s14, s14, s98
	s_addc_u32 s15, s15, 0
	v_writelane_b32 v249, s14, 2
	v_writelane_b32 v249, s15, 3
	s_lshl_b32 s13, s13, 16
	s_lshl_b32 s17, s17, 6
	s_or_b32 s13, s13, s17
	v_readlane_b32 s14, v255, 8
	v_readlane_b32 s15, v255, 9
	s_add_u32 s18, s14, 0x4e00000
	s_addc_u32 s19, s15, 0
	s_add_u32 s18, s18, s99
	s_addc_u32 s19, s19, 0
	v_writelane_b32 v249, s18, 4
	v_writelane_b32 v249, s19, 5
	s_add_u32 s18, s14, 0x24e00000
	s_addc_u32 s19, s15, 0
	s_add_u32 s18, s18, s13
	s_addc_u32 s19, s19, 0
	v_writelane_b32 v249, s18, 6
	v_writelane_b32 v249, s19, 7
	v_mbcnt_lo_u32_b32 v230, -1, 0
	v_mbcnt_hi_u32_b32 v230, -1, v230
	v_lshrrev_b32_e32 v231, 3, v230
	v_and_b32_e32 v248, 7, v230
	v_lshlrev_b32_e32 v250, 16, v231
	v_lshl_or_b32 v250, v248, 4, v250
	v_mul_u32_u24_e32 v251, 0xa0, v248
	v_lshl_add_u32 v251, v231, 3, v251
	v_add_u32_e32 v251, s16, v251
	v_lshrrev_b32_e32 v231, 2, v230
	v_and_b32_e32 v248, 3, v230
	v_mul_u32_u24_e32 v252, 0x50, v231
	v_lshl_add_u32 v252, v248, 4, v252
	v_add_u32_e32 v252, s16, v252
	v_lshrrev_b32_e32 v253, 1, v231
	v_and_b32_e32 v231, 1, v231
	v_lshl_add_u32 v253, v253, 2, v231
	v_lshlrev_b32_e32 v253, 11, v253
	v_lshl_or_b32 v253, v248, 4, v253
	v_readlane_b32 s12, v254, 0
	v_readlane_b32 s13, v254, 1
	v_readlane_b32 s14, v254, 2
	v_readlane_b32 s15, v254, 3
	v_readlane_b32 s16, v254, 4
	v_readlane_b32 s17, v254, 5
	v_readlane_b32 s18, v254, 6
	v_readlane_b32 s19, v254, 7
.Lmlh_init_done:
	s_add_i32 s32, s11, -6
	s_cmp_lt_u32 s32, 24
	s_cbranch_scc0 .Lmlh_pack_done
	s_mul_hi_u32 s98, s32, 0x55555556
	s_mul_i32 s98, s98, 3
	s_sub_i32 s99, s32, s98
	s_mov_b32 s98, 0x42000000
	s_cmp_eq_u32 s99, 2
	s_cselect_b32 s98, 0x42800000, s98
	s_mov_b32 s99, s98
	v_pk_mul_f32 v[198:199], v[198:199], s[98:99]
	v_pk_mul_f32 v[200:201], v[200:201], s[98:99]
	v_pk_mul_f32 v[202:203], v[202:203], s[98:99]
	v_pk_mul_f32 v[204:205], v[204:205], s[98:99]
	v_pk_mul_f32 v[206:207], v[206:207], s[98:99]
	v_pk_mul_f32 v[208:209], v[208:209], s[98:99]
	v_pk_mul_f32 v[210:211], v[210:211], s[98:99]
	v_pk_mul_f32 v[212:213], v[212:213], s[98:99]
	v_pk_mul_f32 v[214:215], v[214:215], s[98:99]
	v_pk_mul_f32 v[216:217], v[216:217], s[98:99]
	v_pk_mul_f32 v[218:219], v[218:219], s[98:99]
	v_pk_mul_f32 v[220:221], v[220:221], s[98:99]
	v_pk_mul_f32 v[222:223], v[222:223], s[98:99]
	v_pk_mul_f32 v[224:225], v[224:225], s[98:99]
	v_pk_mul_f32 v[226:227], v[226:227], s[98:99]
	v_pk_mul_f32 v[228:229], v[228:229], s[98:99]
	v_cvt_pk_fp8_f32 v232, v198, v202
	v_cvt_pk_fp8_f32 v233, v214, v218
	v_cvt_pk_fp8_f32 v232, v206, v210 op_sel:[0,0,1]
	v_cvt_pk_fp8_f32 v233, v222, v226 op_sel:[0,0,1]
	v_cvt_pk_fp8_f32 v234, v199, v203
	v_cvt_pk_fp8_f32 v235, v215, v219
	v_cvt_pk_fp8_f32 v234, v207, v211 op_sel:[0,0,1]
	v_cvt_pk_fp8_f32 v235, v223, v227 op_sel:[0,0,1]
	v_cvt_pk_fp8_f32 v236, v200, v204
	v_cvt_pk_fp8_f32 v237, v216, v220
	v_cvt_pk_fp8_f32 v236, v208, v212 op_sel:[0,0,1]
	v_cvt_pk_fp8_f32 v237, v224, v228 op_sel:[0,0,1]
	v_cvt_pk_fp8_f32 v238, v201, v205
	v_cvt_pk_fp8_f32 v239, v217, v221
	v_cvt_pk_fp8_f32 v238, v209, v213 op_sel:[0,0,1]
	v_cvt_pk_fp8_f32 v239, v225, v229 op_sel:[0,0,1]
.Lmlh_pack_done:
	s_add_i32 s32, s11, -5
	s_cmp_lt_u32 s32, 24
	s_cbranch_scc0 .Lmlh_req_done
	s_mul_hi_u32 s98, s32, 0x55555556
	s_mul_i32 s99, s98, 3
	s_sub_i32 s99, s32, s99
	s_add_i32 s98, s98, 10
	s_lshl_b32 s98, s98, 24
	s_cmp_eq_u32 s99, 2
	s_cbranch_scc1 .Lmlh_req_dn
	v_readlane_b32 s100, v249, 0
	v_readlane_b32 s101, v249, 1
	s_lshl_b32 s99, s99, 23
	s_add_i32 s98, s98, s99
	s_branch .Lmlh_req_cm
.Lmlh_req_dn:
	v_readlane_b32 s100, v249, 2
	v_readlane_b32 s101, v249, 3
.Lmlh_req_cm:
	s_add_u32 s100, s100, s98
	s_addc_u32 s101, s101, 0
	global_load_dwordx4 v[198:201], v250, s[100:101] nt
	s_add_u32 s100, s100, 0x2000
	s_addc_u32 s101, s101, 0
	global_load_dwordx4 v[202:205], v250, s[100:101] nt
	s_add_u32 s100, s100, 0x2000
	s_addc_u32 s101, s101, 0
	global_load_dwordx4 v[206:209], v250, s[100:101] nt
	s_add_u32 s100, s100, 0x2000
	s_addc_u32 s101, s101, 0
	global_load_dwordx4 v[210:213], v250, s[100:101] nt
	s_add_u32 s100, s100, 0x2000
	s_addc_u32 s101, s101, 0
	global_load_dwordx4 v[214:217], v250, s[100:101] nt
	s_add_u32 s100, s100, 0x2000
	s_addc_u32 s101, s101, 0
	global_load_dwordx4 v[218:221], v250, s[100:101] nt
	s_add_u32 s100, s100, 0x2000
	s_addc_u32 s101, s101, 0
	global_load_dwordx4 v[222:225], v250, s[100:101] nt
	s_add_u32 s100, s100, 0x2000
	s_addc_u32 s101, s101, 0
	global_load_dwordx4 v[226:229], v250, s[100:101] nt
.Lmlh_req_done:
	v_mov_b32_e32 v84, s1
	ds_read_b32 v192, v84 offset:1280
	v_add_u32_e32 v131, s1, v158
	s_or_b64 s[50:51], s[92:93], s[50:51]
	s_and_b64 vcc, exec, s[50:51]
	s_waitcnt lgkmcnt(0)
	v_pk_mul_f32 v[94:95], v[62:63], v[192:193] op_sel_hi:[1,0]
	v_pk_mul_f32 v[92:93], v[60:61], v[192:193] op_sel_hi:[1,0]
	v_pk_mul_f32 v[90:91], v[70:71], v[192:193] op_sel_hi:[1,0]
	v_pk_mul_f32 v[88:89], v[68:69], v[192:193] op_sel_hi:[1,0]
	v_pk_mul_f32 v[86:87], v[74:75], v[192:193] op_sel_hi:[1,0]
	v_pk_mul_f32 v[84:85], v[72:73], v[192:193] op_sel_hi:[1,0]
	v_pk_mul_f32 v[62:63], v[46:47], v[192:193] op_sel_hi:[1,0]
	v_pk_mul_f32 v[60:61], v[44:45], v[192:193] op_sel_hi:[1,0]
	v_pk_mul_f32 v[70:71], v[54:55], v[192:193] op_sel_hi:[1,0]
	v_pk_mul_f32 v[68:69], v[52:53], v[192:193] op_sel_hi:[1,0]
	v_pk_mul_f32 v[74:75], v[58:59], v[192:193] op_sel_hi:[1,0]
	v_pk_mul_f32 v[72:73], v[56:57], v[192:193] op_sel_hi:[1,0]
	v_pk_mul_f32 v[100:101], v[64:65], v[192:193] op_sel_hi:[1,0]
	ds_read_b128 v[44:47], v131 offset:768
	ds_read_b128 v[52:55], v131 offset:784
	ds_read_b64_tr_b16 v[56:57], v174 offset:35904
	ds_read_b64_tr_b16 v[58:59], v174 offset:33792
	ds_read_b64_tr_b16 v[64:65], v174 offset:33824
	v_pk_mul_f32 v[96:97], v[48:49], v[192:193] op_sel_hi:[1,0]
	v_pk_mul_f32 v[48:49], v[80:81], v[192:193] op_sel_hi:[1,0]
	v_pk_mul_f32 v[80:81], v[76:77], v[192:193] op_sel_hi:[1,0]
	s_waitcnt lgkmcnt(1)
	v_lshlrev_b32_e32 v76, 16, v59
	v_pk_mul_f32 v[102:103], v[66:67], v[192:193] op_sel_hi:[1,0]
	v_lshlrev_b32_e32 v67, 16, v56
	v_and_b32_e32 v56, 0xffff0000, v56
	v_mul_f32_e32 v77, v46, v76
	v_lshlrev_b32_e32 v76, 16, v57
	v_and_b32_e32 v57, 0xffff0000, v57
	v_pk_mul_f32 v[98:99], v[50:51], v[192:193] op_sel_hi:[1,0]
	v_pk_mul_f32 v[50:51], v[82:83], v[192:193] op_sel_hi:[1,0]
	v_pk_mul_f32 v[82:83], v[78:79], v[192:193] op_sel_hi:[1,0]
	v_mul_f32_e32 v56, v53, v56
	v_mul_f32_e32 v79, v54, v76
	v_mul_f32_e32 v57, v55, v57
	v_mul_f32_e32 v67, v52, v67
	v_cvt_pk_bf16_f32 v78, v67, v56
	v_cvt_pk_bf16_f32 v79, v79, v57
	ds_read_b64_tr_b16 v[56:57], v174 offset:35936
	v_lshlrev_b32_e32 v66, 16, v58
	v_and_b32_e32 v58, 0xffff0000, v58
	v_mul_f32_e32 v58, v45, v58
	v_mul_f32_e32 v66, v44, v66
	v_cvt_pk_bf16_f32 v76, v66, v58
	s_waitcnt lgkmcnt(1)
	v_lshlrev_b32_e32 v58, 16, v64
	v_mul_f32_e32 v44, v44, v58
	s_waitcnt lgkmcnt(0)
	v_lshlrev_b32_e32 v58, 16, v56
	v_and_b32_e32 v56, 0xffff0000, v56
	v_mul_f32_e32 v53, v53, v56
	v_lshlrev_b32_e32 v56, 16, v65
	v_mul_f32_e32 v46, v46, v56
	v_lshlrev_b32_e32 v56, 16, v57
	v_and_b32_e32 v59, 0xffff0000, v59
	v_mul_f32_e32 v54, v54, v56
	v_and_b32_e32 v56, 0xffff0000, v65
	v_mul_f32_e32 v59, v47, v59
	v_mul_f32_e32 v47, v47, v56
	v_and_b32_e32 v56, 0xffff0000, v57
	v_mul_f32_e32 v52, v52, v58
	v_and_b32_e32 v58, 0xffff0000, v64
	v_mul_f32_e32 v55, v55, v56
	v_cvt_pk_bf16_f32 v77, v77, v59
	v_mul_f32_e32 v45, v45, v58
	v_cvt_pk_bf16_f32 v194, v52, v53
	v_cvt_pk_bf16_f32 v195, v54, v55
	ds_read_b128 v[52:55], v175
	ds_read_b128 v[56:59], v175 offset:2304
	ds_read_b128 v[64:67], v175 offset:4608
	v_cvt_pk_bf16_f32 v192, v44, v45
	v_cvt_pk_bf16_f32 v193, v46, v47
	s_waitcnt lgkmcnt(2)
	v_mfma_f32_16x16x32_bf16 v[44:47], v[76:79], v[52:55], v[96:99]
	v_mfma_f32_16x16x32_bf16 v[60:63], v[192:195], v[52:55], v[60:63]
	s_waitcnt lgkmcnt(1)
	v_mfma_f32_16x16x32_bf16 v[52:55], v[76:79], v[56:59], v[92:95]
	v_mfma_f32_16x16x32_bf16 v[68:71], v[192:195], v[56:59], v[68:71]
	s_waitcnt lgkmcnt(0)
	v_mfma_f32_16x16x32_bf16 v[56:59], v[76:79], v[64:67], v[88:91]
	s_nop 2
	ds_read_b128 v[88:91], v175 offset:6912
	v_mfma_f32_16x16x32_bf16 v[72:75], v[192:195], v[64:67], v[72:75]
	s_waitcnt lgkmcnt(0)
	v_mfma_f32_16x16x32_bf16 v[64:67], v[76:79], v[88:91], v[84:87]
	s_nop 2
	ds_read_b128 v[84:87], v175 offset:9216
	s_waitcnt lgkmcnt(0)
	v_mfma_f32_16x16x32_bf16 v[76:79], v[76:79], v[84:87], v[48:51]
	v_mfma_f32_16x16x32_bf16 v[84:87], v[192:195], v[84:87], v[80:83]
	s_nop 1
	ds_read_b128 v[48:51], v131 offset:896
	ds_read_b128 v[92:95], v131 offset:912
	ds_read_b64_tr_b16 v[80:81], v174 offset:50688
	ds_read_b64_tr_b16 v[82:83], v174 offset:52800
	s_waitcnt lgkmcnt(1)
	v_lshlrev_b32_e32 v96, 16, v80
	s_waitcnt lgkmcnt(0)
	v_lshlrev_b32_e32 v97, 16, v82
	v_and_b32_e32 v80, 0xffff0000, v80
	v_and_b32_e32 v82, 0xffff0000, v82
	v_lshlrev_b32_e32 v98, 16, v81
	v_lshlrev_b32_e32 v99, 16, v83
	v_and_b32_e32 v81, 0xffff0000, v81
	v_and_b32_e32 v83, 0xffff0000, v83
	v_mul_f32_e32 v96, v48, v96
	v_mul_f32_e32 v97, v92, v97
	v_mul_f32_e32 v80, v49, v80
	v_mul_f32_e32 v82, v93, v82
	v_mul_f32_e32 v98, v50, v98
	v_mul_f32_e32 v99, v94, v99
	v_mul_f32_e32 v81, v51, v81
	v_mul_f32_e32 v83, v95, v83
	v_cvt_pk_bf16_f32 v80, v96, v80
	v_cvt_pk_bf16_f32 v81, v98, v81
	v_cvt_pk_bf16_f32 v82, v97, v82
	v_cvt_pk_bf16_f32 v83, v99, v83
	ds_read_b64_tr_b16 v[96:97], v174 offset:50720
	ds_read_b64_tr_b16 v[98:99], v174 offset:52832
	v_mfma_f32_16x16x32_bf16 v[88:91], v[192:195], v[88:91], v[100:103]
	s_waitcnt lgkmcnt(1)
	s_nop 1
	v_lshlrev_b32_e32 v100, 16, v96
	v_mul_f32_e32 v48, v48, v100
	s_waitcnt lgkmcnt(0)
	v_lshlrev_b32_e32 v100, 16, v98
	v_mul_f32_e32 v100, v92, v100
	v_and_b32_e32 v92, 0xffff0000, v96
	v_mul_f32_e32 v49, v49, v92
	v_and_b32_e32 v92, 0xffff0000, v98
	v_mul_f32_e32 v96, v93, v92
	v_lshlrev_b32_e32 v92, 16, v97
	v_mul_f32_e32 v50, v50, v92
	v_lshlrev_b32_e32 v92, 16, v99
	v_mul_f32_e32 v98, v94, v92
	v_and_b32_e32 v92, 0xffff0000, v97
	v_mul_f32_e32 v51, v51, v92
	v_and_b32_e32 v92, 0xffff0000, v99
	v_mul_f32_e32 v95, v95, v92
	v_cvt_pk_bf16_f32 v94, v100, v96
	v_cvt_pk_bf16_f32 v95, v98, v95
	ds_read_b128 v[96:99], v175 offset:64
	v_cvt_pk_bf16_f32 v92, v48, v49
	v_cvt_pk_bf16_f32 v93, v50, v51
	s_waitcnt lgkmcnt(0)
	v_mfma_f32_16x16x32_bf16 v[48:51], v[80:83], v[96:99], v[44:47]
	v_mfma_f32_16x16x32_bf16 v[44:47], v[92:95], v[96:99], v[60:63]
	ds_read_b128 v[96:99], v175 offset:2368
	s_waitcnt lgkmcnt(0)
	v_mfma_f32_16x16x32_bf16 v[60:63], v[80:83], v[96:99], v[52:55]
	v_mfma_f32_16x16x32_bf16 v[52:55], v[92:95], v[96:99], v[68:71]
	ds_read_b128 v[96:99], v175 offset:4672
	s_waitcnt lgkmcnt(0)
	v_mfma_f32_16x16x32_bf16 v[68:71], v[80:83], v[96:99], v[56:59]
	v_mfma_f32_16x16x32_bf16 v[56:59], v[92:95], v[96:99], v[72:75]
	ds_read_b128 v[96:99], v175 offset:6976
	s_waitcnt lgkmcnt(0)
	v_mfma_f32_16x16x32_bf16 v[72:75], v[80:83], v[96:99], v[64:67]
	v_mfma_f32_16x16x32_bf16 v[64:67], v[92:95], v[96:99], v[88:91]
	s_nop 2
	ds_read_b128 v[88:91], v175 offset:9280
	s_waitcnt lgkmcnt(0)
	v_mfma_f32_16x16x32_bf16 v[80:83], v[80:83], v[88:91], v[76:79]
	s_barrier
	v_mfma_f32_16x16x32_bf16 v[76:79], v[92:95], v[88:91], v[84:87]
	s_cbranch_vccnz .LBB0_740
	s_and_b64 vcc, exec, s[48:49]
	s_cbranch_vccnz .Lmlh_nowait
	s_waitcnt vmcnt(0)
.Lmlh_nowait:
	s_nop 0
	v_lshlrev_b32_e32 v84, 16, v186
	s_and_b64 vcc, exec, s[54:55]
	v_lshlrev_b32_e32 v85, 16, v187
	s_cbranch_vccnz .LBB0_737
	ds_bpermute_b32 v84, v178, v84
	ds_bpermute_b32 v85, v178, v85

.LBB0_740:
	s_add_i32 s32, s11, -6
	s_cmp_lt_u32 s32, 24
	s_cbranch_scc0 .Lmlh_st_done
	s_mul_hi_u32 s98, s32, 0x55555556
	s_mul_i32 s99, s98, 3
	s_sub_i32 s99, s32, s99
	s_add_i32 s98, s98, 10
	s_cmp_eq_u32 s99, 2
	s_cbranch_scc1 .Lmlh_st_dn
	v_readlane_b32 s100, v249, 4
	v_readlane_b32 s101, v249, 5
	s_lshl_b32 s98, s98, 23
	s_lshl_b32 s99, s99, 10
	s_add_i32 s98, s98, s99
	s_branch .Lmlh_st_cm
.Lmlh_st_dn:
	v_readlane_b32 s100, v249, 6
	v_readlane_b32 s101, v249, 7
	s_lshl_b32 s98, s98, 22
.Lmlh_st_cm:
	s_add_u32 s100, s100, s98
	s_addc_u32 s101, s101, 0
	ds_write_b64 v251, v[232:233]
	ds_write_b64 v251, v[234:235] offset:80
	ds_read_b128 v[240:243], v252
	s_waitcnt lgkmcnt(0)
	global_store_dwordx4 v253, v[240:243], s[100:101]
	ds_write_b64 v251, v[236:237]
	ds_write_b64 v251, v[238:239] offset:80
	ds_read_b128 v[244:247], v252
	s_add_u32 s100, s100, 0x1000
	s_addc_u32 s101, s101, 0
	s_waitcnt lgkmcnt(0)
	global_store_dwordx4 v253, v[244:247], s[100:101]

.LBB0_742:
	s_abs_i32 s7, s3
	v_cvt_f32_u32_e32 v0, s7
	v_readlane_b32 s86, v255, 12
	v_readlane_b32 s87, v255, 13
	s_sub_i32 s8, 0, s7
	v_rcp_iflag_f32_e32 v0, v0
	s_mov_b64 s[0:1], s[86:87]
	s_mov_b32 s6, 0
	s_sub_i32 s4, 0x29ff, s2
	v_mul_f32_e32 v0, 0x4f7ffffe, v0
	v_cvt_u32_f32_e32 v0, v0
	v_readlane_b32 s92, v255, 2
	v_readfirstlane_b32 s9, v0
	s_mul_i32 s8, s8, s9
	s_mul_hi_u32 s8, s9, s8
	v_mbcnt_lo_u32_b32 v1, -1, s6
	s_xor_b32 s6, s4, s3
	s_abs_i32 s4, s4
	s_add_i32 s9, s9, s8
	s_mul_hi_u32 s8, s4, s9
	s_mul_i32 s9, s8, s7
	s_sub_i32 s4, s4, s9
	s_ashr_i32 s6, s6, 31
	s_add_i32 s9, s8, 1
	s_sub_i32 s10, s4, s7
	s_cmp_ge_u32 s4, s7
	s_cselect_b32 s8, s9, s8
	s_cselect_b32 s4, s10, s4
	s_add_i32 s9, s8, 1
	s_cmp_ge_u32 s4, s7
	s_cselect_b32 s4, s9, s8
	s_xor_b32 s4, s4, s6
	s_sub_i32 s59, s4, s6
	s_min_i32 s4, s59, 0
	s_mul_i32 s4, s4, s3
	s_add_i32 s4, s4, s2
	s_mul_hi_i32 s6, s4, 0x2aaaaaab
	s_lshr_b32 s7, s6, 31
	s_ashr_i32 s6, s6, 7
	s_add_i32 s7, s6, s7
	s_add_i32 s6, s7, 18
	s_mulk_i32 s7, 0x300
	v_mbcnt_hi_u32_b32 v1, -1, v1
	s_sub_i32 s12, s4, s7
	s_mov_b32 s5, 0
	v_or_b32_e32 v192, s92, v1
	s_mov_b64 s[14:15], s[86:87]
	s_cmpk_gt_i32 s12, 0x1ff
	s_cbranch_scc0 .LBB0_744
	s_load_dwordx2 s[8:9], s[14:15], 0x110
	s_ashr_i32 s7, s6, 31
	s_lshl_b64 s[10:11], s[6:7], 24
	s_waitcnt lgkmcnt(0)
	s_add_u32 s8, s8, s10
	s_addc_u32 s9, s9, s11
	s_lshl_b32 s4, s12, 3
	s_and_b32 s4, s4, 0x7fffffc0
	s_addk_i32 s4, 0xf000
	s_mov_b32 s7, 8
	s_cbranch_execz .LBB0_745
	s_branch .LBB0_746

.LBB0_746:
	s_lshl_b64 s[4:5], s[4:5], 13
	s_add_u32 s4, s8, s4
	s_addc_u32 s5, s9, s5
	s_lshl_b32 s6, s12, s7
	s_and_b32 s6, s6, 0x700
	s_lshl_b32 s6, s6, 2
	s_add_u32 s4, s4, s6
	s_addc_u32 s5, s5, 0
	s_cmp_lt_i32 s59, 0
	v_lshlrev_b32_e32 v0, 2, v192
	v_and_b32_e32 v180, 0xfc, v0
	s_cselect_b64 s[6:7], -1, 0
	v_cndmask_b32_e64 v0, v180, 0, s[6:7]
	s_and_b64 s[6:7], s[6:7], exec
	v_ashrrev_i32_e32 v6, 3, v192
	s_cselect_b32 s6, 0, 0x800
	v_and_b32_e32 v181, -8, v6
	v_lshlrev_b32_e32 v0, 2, v0
	v_mov_b32_e32 v1, 0
	v_lshl_add_u64 v[0:1], s[4:5], 0, v[0:1]
	v_mad_i64_i32 v[2:3], s[4:5], s6, v181, 0
	v_or_b32_e32 v182, 1, v181
	v_lshl_add_u64 v[2:3], v[2:3], 2, v[0:1]
	v_mad_i64_i32 v[4:5], s[4:5], s6, v182, 0
	v_or_b32_e32 v183, 2, v181
	v_lshl_add_u64 v[4:5], v[4:5], 2, v[0:1]
	global_load_dwordx4 v[48:51], v[2:3], off nt
	global_load_dwordx4 v[52:55], v[4:5], off nt
	v_mad_i64_i32 v[2:3], s[4:5], s6, v183, 0
	v_or_b32_e32 v184, 3, v181
	v_lshl_add_u64 v[2:3], v[2:3], 2, v[0:1]
	v_mad_i64_i32 v[4:5], s[4:5], s6, v184, 0
	v_or_b32_e32 v185, 4, v181
	v_lshl_add_u64 v[4:5], v[4:5], 2, v[0:1]
	global_load_dwordx4 v[64:67], v[2:3], off nt
	global_load_dwordx4 v[68:71], v[4:5], off nt
	v_mad_i64_i32 v[2:3], s[4:5], s6, v185, 0
	s_waitcnt vmcnt(0)
	v_or_b32_e32 v186, 5, v181
	v_lshl_add_u64 v[2:3], v[2:3], 2, v[0:1]
	v_mad_i64_i32 v[4:5], s[4:5], s6, v186, 0
	v_or_b32_e32 v187, 6, v181
	v_lshl_add_u64 v[4:5], v[4:5], 2, v[0:1]
	global_load_dwordx4 v[40:43], v[2:3], off nt
	global_load_dwordx4 v[44:47], v[4:5], off nt
	v_mad_i64_i32 v[2:3], s[4:5], s6, v187, 0
	v_or_b32_e32 v188, 7, v6
	v_lshl_add_u64 v[2:3], v[2:3], 2, v[0:1]
	v_mad_i64_i32 v[4:5], s[4:5], s6, v188, 0
	v_lshl_add_u64 v[0:1], v[4:5], 2, v[0:1]
	global_load_dwordx4 v[56:59], v[2:3], off nt
	global_load_dwordx4 v[60:63], v[0:1], off nt
	s_min_i32 s4, s59, 1
	s_mul_i32 s4, s4, s3
	s_add_i32 s5, s4, s2
	s_mul_hi_i32 s4, s5, 0x2aaaaaab
	s_lshr_b32 s6, s4, 31
	s_ashr_i32 s4, s4, 7
	s_add_i32 s6, s4, s6
	s_add_i32 s4, s6, 18
	s_mulk_i32 s6, 0x300
	s_sub_i32 s12, s5, s6
	v_readlane_b32 s88, v255, 6
	v_readlane_b32 s90, v255, 3
	s_cmpk_gt_i32 s12, 0x1ff
	s_mov_b32 s7, 0
	v_readlane_b32 s89, v255, 7
	v_readlane_b32 s85, v255, 5
	v_readlane_b32 s91, v255, 4
	s_cbranch_scc0 .LBB0_748
	s_load_dwordx2 s[8:9], s[14:15], 0x110
	s_ashr_i32 s5, s4, 31
	s_lshl_b64 s[10:11], s[4:5], 24
	s_waitcnt lgkmcnt(0)
	s_add_u32 s8, s8, s10
	s_addc_u32 s9, s9, s11
	s_lshl_b32 s5, s12, 3
	s_and_b32 s5, s5, 0x7fffffc0
	s_add_i32 s6, s5, 0xfffff000
	s_load_dwordx2 s[16:17], s[0:1], 0x138
	s_mov_b32 s0, 8
	s_cbranch_execz .LBB0_749
	s_branch .LBB0_750

.LBB0_805:
	s_or_b64 exec, exec, s[0:1]
	v_lshlrev_b32_e32 v0, 2, v122
	v_and_b32_e32 v0, -8, v0
	v_lshlrev_b32_e32 v1, 3, v123
	v_add3_u32 v2, v219, v0, v1
	v_mov_b32_e32 v0, v104
	v_mov_b32_e32 v1, v96
	v_mov_b32_e32 v96, v105
	ds_write2_b64 v2, v[0:1], v[96:97] offset1:1
	v_mov_b32_e32 v0, v102
	v_mov_b32_e32 v1, v110
	v_mov_b32_e32 v110, v103
	ds_write2_b64 v2, v[0:1], v[110:111] offset0:2 offset1:3
	v_mov_b32_e32 v0, v106
	v_mov_b32_e32 v1, v112
	v_mov_b32_e32 v112, v107
	ds_write2_b64 v2, v[0:1], v[112:113] offset0:4 offset1:5
	v_mov_b32_e32 v0, v108
	v_mov_b32_e32 v1, v114
	v_mov_b32_e32 v114, v109
	ds_write2_b64 v2, v[0:1], v[114:115] offset0:6 offset1:7
	s_waitcnt lgkmcnt(0)
	s_barrier
	ds_read_b64 v[112:113], v222
	ds_read_b64 v[110:111], v223 offset:2048
	ds_read_b64 v[108:109], v224 offset:4096
	ds_read_b64 v[106:107], v225 offset:6144
	ds_read_b64 v[104:105], v226 offset:8192
	ds_read_b64 v[102:103], v227 offset:10240
	ds_read_b64 v[100:101], v228 offset:12288
	ds_read_b64 v[98:99], v229 offset:14336
	s_waitcnt lgkmcnt(6)
	v_pk_add_f32 v[96:97], v[110:111], 0 op_sel_hi:[1,0]
	s_waitcnt lgkmcnt(5)
	v_pk_add_f32 v[120:121], v[108:109], 0 op_sel_hi:[1,0]
	s_waitcnt lgkmcnt(2)
	v_pk_add_f32 v[114:115], v[102:103], 0 op_sel_hi:[1,0]
	s_waitcnt lgkmcnt(1)
	v_pk_add_f32 v[122:123], v[100:101], 0 op_sel_hi:[1,0]
	v_pk_add_f32 v[116:117], v[96:97], v[114:115]
	v_pk_add_f32 v[96:97], v[96:97], v[114:115] neg_lo:[0,1] neg_hi:[0,1]
	v_pk_fma_f32 v[114:115], v[102:103], s[28:29], v[110:111] op_sel:[1,0,0] op_sel_hi:[0,1,1]
	s_mov_b32 s8, s34
	s_mov_b32 s9, s30
	v_pk_add_f32 v[124:125], v[120:121], v[122:123]
	v_pk_add_f32 v[120:121], v[120:121], v[122:123] neg_lo:[0,1] neg_hi:[0,1]
	v_pk_fma_f32 v[122:123], v[100:101], s[28:29], v[108:109] op_sel:[1,0,0] op_sel_hi:[0,1,1]
	v_pk_add_f32 v[128:129], v[106:107], 0 op_sel_hi:[1,0]
	s_waitcnt lgkmcnt(0)
	v_pk_add_f32 v[130:131], v[98:99], 0 op_sel_hi:[1,0]
	v_pk_mul_f32 v[136:137], v[114:115], s[8:9] op_sel_hi:[0,1]
	s_mov_b32 s0, s35
	s_mov_b32 s1, s34
	s_mov_b32 s6, s37
	s_mov_b32 s7, s36
	v_pk_add_f32 v[132:133], v[128:129], v[130:131]
	v_pk_add_f32 v[128:129], v[128:129], v[130:131] neg_lo:[0,1] neg_hi:[0,1]
	v_pk_fma_f32 v[130:131], v[98:99], s[28:29], v[106:107] op_sel:[1,0,0] op_sel_hi:[0,1,1]
	v_pk_fma_f32 v[114:115], v[114:115], s[0:1], v[136:137] op_sel:[1,0,0]
	v_pk_mul_f32 v[136:137], v[122:123], s[6:7] op_sel_hi:[0,1]
	s_mov_b32 s12, s37
	s_mov_b32 s4, s35
	s_mov_b32 s5, s38
	v_pk_fma_f32 v[122:123], v[122:123], s[12:13], v[136:137] op_sel:[1,0,0] op_sel_hi:[1,0,1]
	v_pk_mul_f32 v[136:137], v[130:131], s[4:5] op_sel_hi:[0,1]
	v_pk_fma_f32 v[130:131], v[130:131], s[34:35], v[136:137] op_sel:[1,0,0]
	v_pk_mul_f32 v[136:137], v[96:97], s[6:7] op_sel_hi:[0,1]
	s_mov_b32 s19, s26
	v_pk_fma_f32 v[118:119], v[102:103], s[26:27], v[110:111] op_sel:[1,0,0] op_sel_hi:[0,1,1]
	v_pk_fma_f32 v[96:97], v[96:97], s[12:13], v[136:137] op_sel:[1,0,0] op_sel_hi:[1,0,1]
	v_pk_mul_f32 v[136:137], v[120:121], s[18:19] op_sel_hi:[0,1]
	s_mov_b32 s50, s27
	s_mov_b32 s51, s18
	v_pk_add_f32 v[4:5], v[112:113], 0 op_sel_hi:[1,0]
	v_pk_add_f32 v[6:7], v[104:105], 0 op_sel_hi:[1,0]
	v_pk_fma_f32 v[134:135], v[98:99], s[26:27], v[106:107] op_sel:[1,0,0] op_sel_hi:[0,1,1]
	v_pk_fma_f32 v[120:121], v[120:121], s[50:51], v[136:137] op_sel:[1,0,0]
	v_pk_mul_f32 v[136:137], v[118:119], s[4:5] op_sel_hi:[0,1]
	s_mov_b32 s39, s35
	v_pk_add_f32 v[80:81], v[4:5], v[6:7]
	v_pk_fma_f32 v[118:119], v[118:119], s[34:35], v[136:137] op_sel:[1,0,0]
	v_pk_mul_f32 v[136:137], v[134:135], s[38:39] op_sel_hi:[0,1]
	s_mov_b32 s31, s38
	v_pk_add_f32 v[4:5], v[4:5], v[6:7] neg_lo:[0,1] neg_hi:[0,1]
	v_pk_fma_f32 v[6:7], v[104:105], s[28:29], v[112:113] op_sel:[1,0,0] op_sel_hi:[0,1,1]
	v_pk_fma_f32 v[126:127], v[100:101], s[26:27], v[108:109] op_sel:[1,0,0] op_sel_hi:[0,1,1]
	v_mul_f32_e32 v86, 0xbf3504f3, v128
	v_pk_fma_f32 v[134:135], v[134:135], s[30:31], v[136:137] op_sel:[1,0,0]
	v_pk_add_f32 v[136:137], v[80:81], v[124:125]
	v_pk_add_f32 v[80:81], v[80:81], v[124:125] neg_lo:[0,1] neg_hi:[0,1]
	v_pk_add_f32 v[124:125], v[116:117], v[132:133]
	v_pk_add_f32 v[116:117], v[116:117], v[132:133] neg_lo:[0,1] neg_hi:[0,1]
	v_pk_fma_f32 v[128:129], v[128:129], s[6:7], v[86:87] op_sel:[1,0,0] op_sel_hi:[1,1,0]
	v_mul_f32_e32 v86, 0xbf3504f3, v126
	v_pk_add_f32 v[132:133], v[136:137], v[124:125]
	v_pk_add_f32 v[124:125], v[136:137], v[124:125] neg_lo:[0,1] neg_hi:[0,1]
	v_pk_fma_f32 v[136:137], v[116:117], s[28:29], v[80:81] op_sel:[1,0,0] op_sel_hi:[0,1,1]
	v_pk_fma_f32 v[80:81], v[116:117], s[26:27], v[80:81] op_sel:[1,0,0] op_sel_hi:[0,1,1]
	v_pk_add_f32 v[116:117], v[6:7], v[122:123]
	v_pk_add_f32 v[6:7], v[6:7], v[122:123] neg_lo:[0,1] neg_hi:[0,1]
	v_pk_add_f32 v[122:123], v[114:115], v[130:131]
	v_pk_add_f32 v[114:115], v[114:115], v[130:131] neg_lo:[0,1] neg_hi:[0,1]
	v_pk_fma_f32 v[82:83], v[104:105], s[26:27], v[112:113] op_sel:[1,0,0] op_sel_hi:[0,1,1]
	v_pk_fma_f32 v[126:127], v[126:127], s[6:7], v[86:87] op_sel:[1,0,0] op_sel_hi:[1,1,0]
	v_pk_add_f32 v[130:131], v[116:117], v[122:123]
	v_pk_add_f32 v[116:117], v[116:117], v[122:123] neg_lo:[0,1] neg_hi:[0,1]
	v_pk_fma_f32 v[122:123], v[114:115], s[28:29], v[6:7] op_sel:[1,0,0] op_sel_hi:[0,1,1]
	v_pk_fma_f32 v[6:7], v[114:115], s[26:27], v[6:7] op_sel:[1,0,0] op_sel_hi:[0,1,1]
	v_pk_add_f32 v[114:115], v[4:5], v[120:121]
	v_pk_add_f32 v[4:5], v[4:5], v[120:121] neg_lo:[0,1] neg_hi:[0,1]
	v_pk_add_f32 v[120:121], v[96:97], v[128:129]
	v_pk_add_f32 v[96:97], v[96:97], v[128:129] neg_lo:[0,1] neg_hi:[0,1]
	v_mov_b32_e32 v160, v215
	v_mov_b32_e32 v3, v220
	v_mov_b32_e32 v1, v221
	v_mov_b32_e32 v2, v217
	v_mov_b32_e32 v0, v218
	v_pk_add_f32 v[128:129], v[114:115], v[120:121]
	v_pk_add_f32 v[114:115], v[114:115], v[120:121] neg_lo:[0,1] neg_hi:[0,1]
	v_pk_fma_f32 v[120:121], v[96:97], s[28:29], v[4:5] op_sel:[1,0,0] op_sel_hi:[0,1,1]
	v_pk_fma_f32 v[4:5], v[96:97], s[26:27], v[4:5] op_sel:[1,0,0] op_sel_hi:[0,1,1]
	v_pk_add_f32 v[96:97], v[82:83], v[126:127]
	v_pk_add_f32 v[82:83], v[82:83], v[126:127] neg_lo:[0,1] neg_hi:[0,1]
	v_pk_add_f32 v[126:127], v[118:119], v[134:135]
	v_pk_add_f32 v[118:119], v[118:119], v[134:135] neg_lo:[0,1] neg_hi:[0,1]
	v_pk_add_f32 v[134:135], v[96:97], v[126:127]
	v_pk_add_f32 v[96:97], v[96:97], v[126:127] neg_lo:[0,1] neg_hi:[0,1]
	v_pk_fma_f32 v[126:127], v[118:119], s[28:29], v[82:83] op_sel:[1,0,0] op_sel_hi:[0,1,1]
	v_pk_fma_f32 v[82:83], v[118:119], s[26:27], v[82:83] op_sel:[1,0,0] op_sel_hi:[0,1,1]
	v_pk_mul_f32 v[118:119], v[2:3], s[28:29]
	v_mov_b32_e32 v86, v3
	v_pk_mul_f32 v[138:139], v[2:3], v[2:3] op_sel_hi:[1,0]
	v_pk_mul_f32 v[158:159], v[2:3], v[130:131] op_sel_hi:[1,0]
	v_pk_fma_f32 v[138:139], v[86:87], v[118:119], v[138:139] op_sel:[0,1,0] op_sel_hi:[0,0,1]
	v_pk_mul_f32 v[142:143], v[138:139], s[28:29]
	v_pk_mul_f32 v[144:145], v[138:139], v[138:139] op_sel_hi:[1,0]
	v_pk_mul_f32 v[140:141], v[2:3], v[138:139] op_sel_hi:[1,0]
	v_pk_fma_f32 v[144:145], v[138:139], v[142:143], v[144:145] op_sel:[1,1,0] op_sel_hi:[1,0,1]
	v_pk_fma_f32 v[140:141], v[138:139], v[118:119], v[140:141] op_sel:[1,1,0] op_sel_hi:[1,0,1]
	v_pk_mul_f32 v[146:147], v[2:3], v[144:145] op_sel_hi:[1,0]
	v_pk_mul_f32 v[150:151], v[140:141], s[28:29]
	v_pk_fma_f32 v[146:147], v[144:145], v[118:119], v[146:147] op_sel:[1,1,0] op_sel_hi:[1,0,1]
	v_pk_fma_f32 v[118:119], v[130:131], v[118:119], v[158:159] op_sel:[1,1,0] op_sel_hi:[1,0,1]
	v_pk_mul_f32 v[130:131], v[138:139], v[128:129] op_sel_hi:[1,0]
	v_pk_mul_f32 v[148:149], v[138:139], v[144:145] op_sel_hi:[1,0]
	v_pk_fma_f32 v[128:129], v[128:129], v[142:143], v[130:131] op_sel:[1,1,0] op_sel_hi:[1,0,1]
	v_pk_mul_f32 v[130:131], v[134:135], v[140:141] op_sel_hi:[0,1]
	v_pk_mul_f32 v[154:155], v[144:145], s[28:29]
	v_pk_fma_f32 v[130:131], v[134:135], v[150:151], v[130:131] op_sel:[1,1,0] op_sel_hi:[1,0,1]
	v_pk_mul_f32 v[134:135], v[136:137], v[144:145] op_sel_hi:[0,1]
	v_pk_fma_f32 v[148:149], v[144:145], v[142:143], v[148:149] op_sel:[1,1,0] op_sel_hi:[1,0,1]
	v_pk_mul_f32 v[152:153], v[140:141], v[144:145] op_sel_hi:[1,0]
	v_pk_fma_f32 v[134:135], v[136:137], v[154:155], v[134:135] op_sel:[1,1,0] op_sel_hi:[1,0,1]
	v_pk_mul_f32 v[136:137], v[146:147], s[28:29]
	v_pk_mul_f32 v[142:143], v[122:123], v[146:147] op_sel_hi:[0,1]
	v_pk_fma_f32 v[152:153], v[144:145], v[150:151], v[152:153] op_sel:[1,1,0] op_sel_hi:[1,0,1]
	v_pk_mul_f32 v[156:157], v[144:145], v[144:145] op_sel_hi:[1,0]
	v_pk_fma_f32 v[122:123], v[122:123], v[136:137], v[142:143] op_sel:[1,1,0] op_sel_hi:[1,0,1]
	v_pk_mul_f32 v[136:137], v[148:149], s[28:29]
	v_pk_mul_f32 v[142:143], v[120:121], v[148:149] op_sel_hi:[0,1]
	v_pk_fma_f32 v[156:157], v[144:145], v[154:155], v[156:157] op_sel:[1,1,0] op_sel_hi:[1,0,1]
	v_pk_fma_f32 v[120:121], v[120:121], v[136:137], v[142:143] op_sel:[1,1,0] op_sel_hi:[1,0,1]
	v_pk_mul_f32 v[136:137], v[152:153], s[28:29]
	v_pk_mul_f32 v[142:143], v[126:127], v[152:153] op_sel_hi:[0,1]
	v_pk_fma_f32 v[126:127], v[126:127], v[136:137], v[142:143] op_sel:[1,1,0] op_sel_hi:[1,0,1]
	v_pk_mul_f32 v[136:137], v[156:157], s[28:29]
	v_pk_mul_f32 v[2:3], v[2:3], v[156:157] op_sel_hi:[0,1]
	v_pk_mul_f32 v[142:143], v[124:125], v[156:157] op_sel_hi:[0,1]
	v_pk_fma_f32 v[2:3], v[86:87], v[136:137], v[2:3] op_sel:[0,1,0] op_sel_hi:[0,0,1]
	v_pk_fma_f32 v[124:125], v[124:125], v[136:137], v[142:143] op_sel:[1,1,0] op_sel_hi:[1,0,1]
	v_pk_mul_f32 v[142:143], v[2:3], s[28:29]
	v_pk_mul_f32 v[2:3], v[116:117], v[2:3] op_sel_hi:[0,1]
	v_pk_fma_f32 v[2:3], v[116:117], v[142:143], v[2:3] op_sel:[1,1,0] op_sel_hi:[1,0,1]
	v_pk_mul_f32 v[116:117], v[138:139], v[156:157] op_sel_hi:[0,1]
	v_pk_fma_f32 v[116:117], v[138:139], v[136:137], v[116:117] op_sel:[1,1,0] op_sel_hi:[1,0,1]
	v_ashrrev_i32_e32 v86, 4, v160
	v_pk_mul_f32 v[138:139], v[116:117], s[28:29]
	v_pk_mul_f32 v[116:117], v[114:115], v[116:117] op_sel_hi:[0,1]
	v_pk_fma_f32 v[114:115], v[114:115], v[138:139], v[116:117] op_sel:[1,1,0] op_sel_hi:[1,0,1]
	v_pk_mul_f32 v[116:117], v[140:141], v[156:157] op_sel_hi:[0,1]
	v_pk_fma_f32 v[116:117], v[140:141], v[136:137], v[116:117] op_sel:[1,1,0] op_sel_hi:[1,0,1]
	s_add_i32 s56, s62, -2
	v_pk_mul_f32 v[138:139], v[116:117], s[28:29]
	v_pk_mul_f32 v[116:117], v[96:97], v[116:117] op_sel_hi:[0,1]
	v_pk_fma_f32 v[96:97], v[96:97], v[138:139], v[116:117] op_sel:[1,1,0] op_sel_hi:[1,0,1]
	v_pk_mul_f32 v[116:117], v[144:145], v[156:157] op_sel_hi:[0,1]
	v_pk_fma_f32 v[116:117], v[144:145], v[136:137], v[116:117] op_sel:[1,1,0] op_sel_hi:[1,0,1]
	v_add_u32_e32 v236, v196, v197
	v_pk_mul_f32 v[138:139], v[116:117], s[28:29]
	v_pk_mul_f32 v[116:117], v[80:81], v[116:117] op_sel_hi:[0,1]
	v_pk_fma_f32 v[80:81], v[80:81], v[138:139], v[116:117] op_sel:[1,1,0] op_sel_hi:[1,0,1]
	v_pk_mul_f32 v[116:117], v[156:157], v[146:147] op_sel_hi:[1,0]
	v_add_u32_e32 v237, v196, v198
	v_pk_fma_f32 v[116:117], v[146:147], v[136:137], v[116:117] op_sel:[1,1,0] op_sel_hi:[1,0,1]
	s_nop 0
	v_pk_mul_f32 v[138:139], v[116:117], s[28:29]
	v_pk_mul_f32 v[116:117], v[6:7], v[116:117] op_sel_hi:[0,1]
	v_pk_fma_f32 v[6:7], v[6:7], v[138:139], v[116:117] op_sel:[1,1,0] op_sel_hi:[1,0,1]
	v_pk_mul_f32 v[116:117], v[156:157], v[148:149] op_sel_hi:[1,0]
	s_nop 0
	v_pk_fma_f32 v[116:117], v[148:149], v[136:137], v[116:117] op_sel:[1,1,0] op_sel_hi:[1,0,1]
	s_nop 0
	v_pk_mul_f32 v[138:139], v[116:117], s[28:29]
	v_pk_mul_f32 v[116:117], v[4:5], v[116:117] op_sel_hi:[0,1]
	v_pk_fma_f32 v[4:5], v[4:5], v[138:139], v[116:117] op_sel:[1,1,0] op_sel_hi:[1,0,1]
	v_pk_mul_f32 v[116:117], v[156:157], v[152:153] op_sel_hi:[1,0]
	s_nop 0
	v_pk_fma_f32 v[116:117], v[152:153], v[136:137], v[116:117] op_sel:[1,1,0] op_sel_hi:[1,0,1]
	s_nop 0
	v_pk_mul_f32 v[136:137], v[116:117], s[28:29]
	v_pk_mul_f32 v[116:117], v[82:83], v[116:117] op_sel_hi:[0,1]
	v_pk_fma_f32 v[82:83], v[82:83], v[136:137], v[116:117] op_sel:[1,1,0] op_sel_hi:[1,0,1]
	v_lshlrev_b32_e32 v116, 3, v160
	v_add_u32_e32 v158, v219, v116
	v_lshl_add_u32 v117, v86, 3, v158
	ds_write_b64 v117, v[132:133]
	v_add_u32_e32 v117, 0x100, v160
	v_ashrrev_i32_e32 v117, 4, v117
	v_lshl_add_u32 v117, v117, 3, v158
	ds_write_b64 v117, v[118:119] offset:2048
	v_add_u32_e32 v117, 0x200, v160
	v_ashrrev_i32_e32 v117, 4, v117
	v_lshl_add_u32 v117, v117, 3, v158
	ds_write_b64 v117, v[128:129] offset:4096
	v_add_u32_e32 v117, 0x300, v160
	v_ashrrev_i32_e32 v117, 4, v117
	v_lshl_add_u32 v117, v117, 3, v158
	ds_write_b64 v117, v[130:131] offset:6144
	v_add_u32_e32 v117, 0x400, v160
	v_ashrrev_i32_e32 v117, 4, v117
	v_lshl_add_u32 v117, v117, 3, v158
	ds_write_b64 v117, v[134:135] offset:8192
	v_add_u32_e32 v117, 0x500, v160
	v_ashrrev_i32_e32 v117, 4, v117
	v_lshl_add_u32 v117, v117, 3, v158
	ds_write_b64 v117, v[122:123] offset:10240
	v_add_u32_e32 v117, 0x600, v160
	v_ashrrev_i32_e32 v117, 4, v117
	v_lshl_add_u32 v117, v117, 3, v158
	ds_write_b64 v117, v[120:121] offset:12288
	v_add_u32_e32 v117, 0x700, v160
	v_ashrrev_i32_e32 v117, 4, v117
	v_lshl_add_u32 v117, v117, 3, v158
	ds_write_b64 v117, v[126:127] offset:14336
	v_add_u32_e32 v117, 0x800, v160
	v_ashrrev_i32_e32 v117, 4, v117
	v_lshl_add_u32 v117, v117, 3, v158
	ds_write_b64 v117, v[124:125] offset:16384
	v_add_u32_e32 v117, 0x900, v160
	v_ashrrev_i32_e32 v117, 4, v117
	v_lshl_add_u32 v117, v117, 3, v158
	ds_write_b64 v117, v[2:3] offset:18432
	v_add_u32_e32 v2, 0xa00, v160
	v_ashrrev_i32_e32 v2, 4, v2
	v_lshl_add_u32 v2, v2, 3, v158
	ds_write_b64 v2, v[114:115] offset:20480
	v_add_u32_e32 v2, 0xb00, v160
	v_ashrrev_i32_e32 v2, 4, v2
	v_lshl_add_u32 v2, v2, 3, v158
	ds_write_b64 v2, v[96:97] offset:22528
	v_add_u32_e32 v2, 0xc00, v160
	v_ashrrev_i32_e32 v2, 4, v2
	v_lshl_add_u32 v2, v2, 3, v158
	ds_write_b64 v2, v[80:81] offset:24576
	v_add_u32_e32 v2, 0xd00, v160
	v_ashrrev_i32_e32 v2, 4, v2
	v_lshl_add_u32 v2, v2, 3, v158
	ds_write_b64 v2, v[6:7] offset:26624
	v_add_u32_e32 v2, 0xe00, v160
	v_ashrrev_i32_e32 v2, 4, v2
	v_lshl_add_u32 v2, v2, 3, v158
	ds_write_b64 v2, v[4:5] offset:28672
	v_add_u32_e32 v2, 0xf00, v160
	v_ashrrev_i32_e32 v2, 4, v2
	v_lshl_add_u32 v2, v2, 3, v158
	ds_write_b64 v2, v[82:83] offset:30720
	v_lshlrev_b32_e32 v2, 8, v86
	v_lshl_add_u32 v3, v86, 7, v219
	v_lshlrev_b32_e32 v4, 11, v86
	v_and_b32_e32 v5, 0x78, v116
	v_add3_u32 v159, v3, v4, v5
	v_ashrrev_i32_e32 v2, 1, v2
	s_waitcnt lgkmcnt(0)
	s_barrier
	ds_read_b64 v[6:7], v159
	v_add_u32_e32 v2, v219, v2
	v_add3_u32 v161, v2, v4, v5
	ds_read2_b64 v[2:5], v161 offset0:17 offset1:34
	ds_read2_b64 v[80:83], v161 offset0:51 offset1:68
	ds_read2_b64 v[114:117], v161 offset0:85 offset1:102
	ds_read2_b64 v[118:121], v161 offset0:119 offset1:136
	ds_read2_b64 v[122:125], v161 offset0:153 offset1:170
	ds_read2_b64 v[126:129], v161 offset0:187 offset1:204
	ds_read2_b64 v[130:133], v161 offset0:221 offset1:238
	ds_read_b64 v[96:97], v161 offset:2040
	v_pk_mul_f32 v[136:137], v[0:1], v[0:1] op_sel_hi:[1,0]
	s_waitcnt lgkmcnt(4)
	v_pk_add_f32 v[134:135], v[6:7], v[120:121]
	v_pk_add_f32 v[6:7], v[6:7], v[120:121] neg_lo:[0,1] neg_hi:[0,1]
	s_waitcnt lgkmcnt(2)
	v_pk_add_f32 v[120:121], v[82:83], v[128:129]
	v_pk_add_f32 v[82:83], v[82:83], v[128:129] neg_lo:[0,1] neg_hi:[0,1]
	v_pk_add_f32 v[128:129], v[134:135], v[120:121]
	v_pk_add_f32 v[120:121], v[134:135], v[120:121] neg_lo:[0,1] neg_hi:[0,1]
	v_pk_fma_f32 v[134:135], v[82:83], s[28:29], v[6:7] op_sel:[1,0,0] op_sel_hi:[0,1,1]
	v_pk_fma_f32 v[6:7], v[82:83], s[26:27], v[6:7] op_sel:[1,0,0] op_sel_hi:[0,1,1]
	v_pk_add_f32 v[82:83], v[2:3], v[122:123]
	v_pk_add_f32 v[2:3], v[2:3], v[122:123] neg_lo:[0,1] neg_hi:[0,1]
	s_waitcnt lgkmcnt(1)
	v_pk_add_f32 v[122:123], v[114:115], v[130:131]
	v_pk_add_f32 v[114:115], v[114:115], v[130:131] neg_lo:[0,1] neg_hi:[0,1]
	v_pk_add_f32 v[130:131], v[82:83], v[122:123]
	v_pk_add_f32 v[82:83], v[82:83], v[122:123] neg_lo:[0,1] neg_hi:[0,1]
	v_pk_fma_f32 v[122:123], v[114:115], s[28:29], v[2:3] op_sel:[1,0,0] op_sel_hi:[0,1,1]
	v_pk_fma_f32 v[2:3], v[114:115], s[26:27], v[2:3] op_sel:[1,0,0] op_sel_hi:[0,1,1]
	v_pk_add_f32 v[114:115], v[4:5], v[124:125]
	v_pk_add_f32 v[4:5], v[4:5], v[124:125] neg_lo:[0,1] neg_hi:[0,1]
	v_pk_add_f32 v[124:125], v[116:117], v[132:133]
	v_pk_add_f32 v[116:117], v[116:117], v[132:133] neg_lo:[0,1] neg_hi:[0,1]
	v_pk_add_f32 v[132:133], v[114:115], v[124:125]
	v_pk_add_f32 v[114:115], v[114:115], v[124:125] neg_lo:[0,1] neg_hi:[0,1]
	v_pk_fma_f32 v[124:125], v[116:117], s[28:29], v[4:5] op_sel:[1,0,0] op_sel_hi:[0,1,1]
	v_pk_fma_f32 v[4:5], v[116:117], s[26:27], v[4:5] op_sel:[1,0,0] op_sel_hi:[0,1,1]
	v_pk_add_f32 v[116:117], v[80:81], v[126:127]
	v_pk_add_f32 v[80:81], v[80:81], v[126:127] neg_lo:[0,1] neg_hi:[0,1]
	s_waitcnt lgkmcnt(0)
	v_pk_add_f32 v[126:127], v[118:119], v[96:97]
	v_pk_add_f32 v[96:97], v[118:119], v[96:97] neg_lo:[0,1] neg_hi:[0,1]
	v_pk_add_f32 v[118:119], v[116:117], v[126:127]
	v_pk_add_f32 v[116:117], v[116:117], v[126:127] neg_lo:[0,1] neg_hi:[0,1]
	v_pk_fma_f32 v[126:127], v[96:97], s[28:29], v[80:81] op_sel:[1,0,0] op_sel_hi:[0,1,1]
	v_pk_fma_f32 v[80:81], v[96:97], s[26:27], v[80:81] op_sel:[1,0,0] op_sel_hi:[0,1,1]
	v_pk_mul_f32 v[96:97], v[122:123], s[8:9] op_sel_hi:[0,1]
	v_pk_fma_f32 v[96:97], v[122:123], s[0:1], v[96:97] op_sel:[1,0,0]
	v_pk_mul_f32 v[122:123], v[124:125], s[6:7] op_sel_hi:[0,1]
	v_pk_fma_f32 v[122:123], v[124:125], s[12:13], v[122:123] op_sel:[1,0,0] op_sel_hi:[1,0,1]
	v_pk_mul_f32 v[124:125], v[126:127], s[4:5] op_sel_hi:[0,1]
	v_pk_fma_f32 v[124:125], v[126:127], s[34:35], v[124:125] op_sel:[1,0,0]
	v_pk_mul_f32 v[126:127], v[82:83], s[6:7] op_sel_hi:[0,1]
	v_pk_fma_f32 v[82:83], v[82:83], s[12:13], v[126:127] op_sel:[1,0,0] op_sel_hi:[1,0,1]
	v_pk_mul_f32 v[126:127], v[114:115], s[18:19] op_sel_hi:[0,1]
	v_pk_fma_f32 v[114:115], v[114:115], s[50:51], v[126:127] op_sel:[1,0,0]
	v_pk_mul_f32 v[126:127], v[2:3], s[4:5] op_sel_hi:[0,1]
	v_pk_fma_f32 v[2:3], v[2:3], s[34:35], v[126:127] op_sel:[1,0,0]
	v_pk_mul_f32 v[126:127], v[80:81], s[38:39] op_sel_hi:[0,1]
	v_mul_f32_e32 v86, 0xbf3504f3, v116
	v_pk_fma_f32 v[80:81], v[80:81], s[30:31], v[126:127] op_sel:[1,0,0]
	v_pk_add_f32 v[126:127], v[128:129], v[132:133]
	v_pk_add_f32 v[128:129], v[128:129], v[132:133] neg_lo:[0,1] neg_hi:[0,1]
	v_pk_add_f32 v[132:133], v[130:131], v[118:119]
	v_pk_add_f32 v[118:119], v[130:131], v[118:119] neg_lo:[0,1] neg_hi:[0,1]
	v_pk_fma_f32 v[116:117], v[116:117], s[6:7], v[86:87] op_sel:[1,0,0] op_sel_hi:[1,1,0]
	v_mul_f32_e32 v86, 0xbf3504f3, v4
	v_pk_add_f32 v[130:131], v[126:127], v[132:133]
	v_pk_add_f32 v[126:127], v[126:127], v[132:133] neg_lo:[0,1] neg_hi:[0,1]
	v_pk_fma_f32 v[132:133], v[118:119], s[28:29], v[128:129] op_sel:[1,0,0] op_sel_hi:[0,1,1]
	v_pk_fma_f32 v[118:119], v[118:119], s[26:27], v[128:129] op_sel:[1,0,0] op_sel_hi:[0,1,1]
	v_pk_add_f32 v[128:129], v[134:135], v[122:123]
	v_pk_add_f32 v[122:123], v[134:135], v[122:123] neg_lo:[0,1] neg_hi:[0,1]
	v_pk_add_f32 v[134:135], v[96:97], v[124:125]
	v_pk_add_f32 v[96:97], v[96:97], v[124:125] neg_lo:[0,1] neg_hi:[0,1]
	v_pk_fma_f32 v[4:5], v[4:5], s[6:7], v[86:87] op_sel:[1,0,0] op_sel_hi:[1,1,0]
	v_pk_add_f32 v[124:125], v[128:129], v[134:135]
	v_pk_add_f32 v[128:129], v[128:129], v[134:135] neg_lo:[0,1] neg_hi:[0,1]
	v_pk_fma_f32 v[134:135], v[96:97], s[28:29], v[122:123] op_sel:[1,0,0] op_sel_hi:[0,1,1]
	v_pk_fma_f32 v[96:97], v[96:97], s[26:27], v[122:123] op_sel:[1,0,0] op_sel_hi:[0,1,1]
	v_pk_add_f32 v[122:123], v[120:121], v[114:115]
	v_pk_add_f32 v[114:115], v[120:121], v[114:115] neg_lo:[0,1] neg_hi:[0,1]
	v_pk_add_f32 v[120:121], v[82:83], v[116:117]
	v_pk_add_f32 v[82:83], v[82:83], v[116:117] neg_lo:[0,1] neg_hi:[0,1]
	v_pk_add_f32 v[116:117], v[122:123], v[120:121]
	v_pk_add_f32 v[120:121], v[122:123], v[120:121] neg_lo:[0,1] neg_hi:[0,1]
	v_pk_fma_f32 v[122:123], v[82:83], s[28:29], v[114:115] op_sel:[1,0,0] op_sel_hi:[0,1,1]
	v_pk_fma_f32 v[82:83], v[82:83], s[26:27], v[114:115] op_sel:[1,0,0] op_sel_hi:[0,1,1]
	v_pk_add_f32 v[114:115], v[6:7], v[4:5]
	v_pk_add_f32 v[4:5], v[6:7], v[4:5] neg_lo:[0,1] neg_hi:[0,1]
	v_pk_add_f32 v[6:7], v[2:3], v[80:81]
	v_pk_add_f32 v[2:3], v[2:3], v[80:81] neg_lo:[0,1] neg_hi:[0,1]
	v_pk_add_f32 v[80:81], v[114:115], v[6:7]
	v_pk_add_f32 v[6:7], v[114:115], v[6:7] neg_lo:[0,1] neg_hi:[0,1]
	v_pk_fma_f32 v[114:115], v[2:3], s[28:29], v[4:5] op_sel:[1,0,0] op_sel_hi:[0,1,1]
	v_pk_fma_f32 v[2:3], v[2:3], s[26:27], v[4:5] op_sel:[1,0,0] op_sel_hi:[0,1,1]
	v_pk_mul_f32 v[4:5], v[0:1], s[28:29]
	v_mov_b32_e32 v86, v1
	v_pk_fma_f32 v[136:137], v[86:87], v[4:5], v[136:137] op_sel:[0,1,0] op_sel_hi:[0,0,1]
	v_pk_mul_f32 v[140:141], v[136:137], s[28:29]
	v_pk_mul_f32 v[142:143], v[136:137], v[136:137] op_sel_hi:[1,0]
	v_pk_mul_f32 v[138:139], v[0:1], v[136:137] op_sel_hi:[1,0]
	v_pk_fma_f32 v[142:143], v[136:137], v[140:141], v[142:143] op_sel:[1,1,0] op_sel_hi:[1,0,1]
	v_pk_mul_f32 v[156:157], v[0:1], v[124:125] op_sel_hi:[1,0]
	v_pk_mul_f32 v[144:145], v[0:1], v[142:143] op_sel_hi:[1,0]
	v_pk_fma_f32 v[138:139], v[136:137], v[4:5], v[138:139] op_sel:[1,1,0] op_sel_hi:[1,0,1]
	v_pk_fma_f32 v[144:145], v[142:143], v[4:5], v[144:145] op_sel:[1,1,0] op_sel_hi:[1,0,1]
	v_pk_fma_f32 v[4:5], v[124:125], v[4:5], v[156:157] op_sel:[1,1,0] op_sel_hi:[1,0,1]
	v_pk_mul_f32 v[124:125], v[136:137], v[116:117] op_sel_hi:[1,0]
	v_pk_mul_f32 v[148:149], v[138:139], s[28:29]
	v_pk_fma_f32 v[116:117], v[116:117], v[140:141], v[124:125] op_sel:[1,1,0] op_sel_hi:[1,0,1]
	v_pk_mul_f32 v[124:125], v[138:139], v[80:81] op_sel_hi:[1,0]
	v_pk_mul_f32 v[146:147], v[136:137], v[142:143] op_sel_hi:[1,0]
	v_pk_mul_f32 v[152:153], v[142:143], s[28:29]
	v_pk_fma_f32 v[80:81], v[80:81], v[148:149], v[124:125] op_sel:[1,1,0] op_sel_hi:[1,0,1]
	v_pk_mul_f32 v[124:125], v[142:143], v[132:133] op_sel_hi:[1,0]
	v_pk_fma_f32 v[146:147], v[142:143], v[140:141], v[146:147] op_sel:[1,1,0] op_sel_hi:[1,0,1]
	v_pk_mul_f32 v[150:151], v[138:139], v[142:143] op_sel_hi:[1,0]
	v_pk_fma_f32 v[124:125], v[132:133], v[152:153], v[124:125] op_sel:[1,1,0] op_sel_hi:[1,0,1]
	v_pk_mul_f32 v[132:133], v[144:145], s[28:29]
	v_pk_mul_f32 v[140:141], v[144:145], v[134:135] op_sel_hi:[1,0]
	v_pk_fma_f32 v[150:151], v[142:143], v[148:149], v[150:151] op_sel:[1,1,0] op_sel_hi:[1,0,1]
	v_pk_mul_f32 v[154:155], v[142:143], v[142:143] op_sel_hi:[1,0]
	v_pk_fma_f32 v[132:133], v[134:135], v[132:133], v[140:141] op_sel:[1,1,0] op_sel_hi:[1,0,1]
	v_pk_mul_f32 v[134:135], v[146:147], s[28:29]
	v_pk_mul_f32 v[140:141], v[146:147], v[122:123] op_sel_hi:[1,0]
	v_pk_fma_f32 v[154:155], v[142:143], v[152:153], v[154:155] op_sel:[1,1,0] op_sel_hi:[1,0,1]
	v_pk_fma_f32 v[122:123], v[122:123], v[134:135], v[140:141] op_sel:[1,1,0] op_sel_hi:[1,0,1]
	v_pk_mul_f32 v[134:135], v[150:151], s[28:29]
	v_pk_mul_f32 v[140:141], v[150:151], v[114:115] op_sel_hi:[1,0]
	v_pk_mul_f32 v[0:1], v[0:1], v[154:155] op_sel_hi:[0,1]
	v_pk_fma_f32 v[114:115], v[114:115], v[134:135], v[140:141] op_sel:[1,1,0] op_sel_hi:[1,0,1]
	v_pk_mul_f32 v[134:135], v[154:155], s[28:29]
	v_pk_mul_f32 v[140:141], v[154:155], v[126:127] op_sel_hi:[1,0]
	v_pk_fma_f32 v[0:1], v[86:87], v[134:135], v[0:1] op_sel:[0,1,0] op_sel_hi:[0,0,1]
	v_pk_fma_f32 v[126:127], v[126:127], v[134:135], v[140:141] op_sel:[1,1,0] op_sel_hi:[1,0,1]
	v_pk_mul_f32 v[140:141], v[0:1], s[28:29]
	v_pk_mul_f32 v[0:1], v[0:1], v[128:129] op_sel_hi:[1,0]
	s_mov_b32 s13, 0x62700000
	v_pk_fma_f32 v[0:1], v[128:129], v[140:141], v[0:1] op_sel:[1,1,0] op_sel_hi:[1,0,1]
	v_pk_mul_f32 v[128:129], v[136:137], v[154:155] op_sel_hi:[0,1]
	v_pk_fma_f32 v[128:129], v[136:137], v[134:135], v[128:129] op_sel:[1,1,0] op_sel_hi:[1,0,1]
	v_lshl_add_u32 v86, v160, 7, v158
	v_pk_mul_f32 v[136:137], v[128:129], s[28:29]
	v_pk_mul_f32 v[128:129], v[128:129], v[120:121] op_sel_hi:[1,0]
	s_nop 0
	v_pk_fma_f32 v[120:121], v[120:121], v[136:137], v[128:129] op_sel:[1,1,0] op_sel_hi:[1,0,1]
	v_pk_mul_f32 v[128:129], v[138:139], v[154:155] op_sel_hi:[0,1]
	v_pk_fma_f32 v[128:129], v[138:139], v[134:135], v[128:129] op_sel:[1,1,0] op_sel_hi:[1,0,1]
	s_nop 0
	v_pk_mul_f32 v[136:137], v[128:129], s[28:29]
	v_pk_mul_f32 v[128:129], v[128:129], v[6:7] op_sel_hi:[1,0]
	s_nop 0
	v_pk_fma_f32 v[6:7], v[6:7], v[136:137], v[128:129] op_sel:[1,1,0] op_sel_hi:[1,0,1]
	v_pk_mul_f32 v[128:129], v[142:143], v[154:155] op_sel_hi:[0,1]
	v_pk_fma_f32 v[128:129], v[142:143], v[134:135], v[128:129] op_sel:[1,1,0] op_sel_hi:[1,0,1]
	s_nop 0
	v_pk_mul_f32 v[136:137], v[128:129], s[28:29]
	v_pk_mul_f32 v[128:129], v[128:129], v[118:119] op_sel_hi:[1,0]
	s_nop 0
	v_pk_fma_f32 v[118:119], v[118:119], v[136:137], v[128:129] op_sel:[1,1,0] op_sel_hi:[1,0,1]
	v_pk_mul_f32 v[128:129], v[154:155], v[144:145] op_sel_hi:[1,0]
	s_nop 0
	v_pk_fma_f32 v[128:129], v[144:145], v[134:135], v[128:129] op_sel:[1,1,0] op_sel_hi:[1,0,1]
	s_nop 0
	v_pk_mul_f32 v[136:137], v[128:129], s[28:29]
	v_pk_mul_f32 v[128:129], v[128:129], v[96:97] op_sel_hi:[1,0]
	s_nop 0
	v_pk_fma_f32 v[96:97], v[96:97], v[136:137], v[128:129] op_sel:[1,1,0] op_sel_hi:[1,0,1]
	v_pk_mul_f32 v[128:129], v[154:155], v[146:147] op_sel_hi:[1,0]
	s_nop 0
	v_pk_fma_f32 v[128:129], v[146:147], v[134:135], v[128:129] op_sel:[1,1,0] op_sel_hi:[1,0,1]
	s_nop 0
	v_pk_mul_f32 v[136:137], v[128:129], s[28:29]
	v_pk_mul_f32 v[128:129], v[128:129], v[82:83] op_sel_hi:[1,0]
	s_nop 0
	v_pk_fma_f32 v[82:83], v[82:83], v[136:137], v[128:129] op_sel:[1,1,0] op_sel_hi:[1,0,1]
	v_pk_mul_f32 v[128:129], v[154:155], v[150:151] op_sel_hi:[1,0]
	s_nop 0
	v_pk_fma_f32 v[128:129], v[150:151], v[134:135], v[128:129] op_sel:[1,1,0] op_sel_hi:[1,0,1]
	s_nop 0
	v_pk_mul_f32 v[134:135], v[128:129], s[28:29]
	v_pk_mul_f32 v[128:129], v[128:129], v[2:3] op_sel_hi:[1,0]
	s_nop 0
	v_pk_fma_f32 v[2:3], v[2:3], v[134:135], v[128:129] op_sel:[1,1,0] op_sel_hi:[1,0,1]
	ds_write_b64 v159, v[130:131]
	ds_write2_b64 v161, v[4:5], v[116:117] offset0:17 offset1:34
	ds_write2_b64 v161, v[80:81], v[124:125] offset0:51 offset1:68
	ds_write2_b64 v161, v[132:133], v[122:123] offset0:85 offset1:102
	ds_write2_b64 v161, v[114:115], v[126:127] offset0:119 offset1:136
	ds_write2_b64 v161, v[0:1], v[120:121] offset0:153 offset1:170
	ds_write2_b64 v161, v[6:7], v[118:119] offset0:187 offset1:204
	ds_write2_b64 v161, v[96:97], v[82:83] offset0:221 offset1:238
	ds_write_b64 v161, v[2:3] offset:2040
	v_lshl_add_u64 v[96:97], s[16:17], 0, v[94:95]
	v_add_co_u32_e32 v0, vcc, s13, v96
	s_mov_b32 s13, 0x62701000
	s_nop 0
	v_addc_co_u32_e32 v1, vcc, 0, v97, vcc
	v_add_co_u32_e32 v2, vcc, s13, v96
	s_mov_b32 s13, 0x62702000
	s_nop 0
	v_addc_co_u32_e32 v3, vcc, 0, v97, vcc
	v_add_co_u32_e32 v4, vcc, s13, v96
	s_mov_b32 s13, 0x62703000
	s_nop 0
	v_addc_co_u32_e32 v5, vcc, 0, v97, vcc
	v_add_co_u32_e32 v6, vcc, s13, v96
	s_nop 1
	v_addc_co_u32_e32 v7, vcc, 0, v97, vcc
	global_load_dword v136, v[2:3], off offset:-4096
	global_load_dword v138, v[0:1], off offset:1024
	global_load_dword v139, v[0:1], off offset:2048
	global_load_dword v140, v[0:1], off offset:3072
	global_load_dword v141, v[2:3], off
	global_load_dword v142, v[4:5], off offset:1024
	global_load_dword v143, v[4:5], off offset:2048
	global_load_dword v144, v[4:5], off offset:3072
	global_load_dword v145, v[2:3], off offset:1024
	global_load_dword v146, v[2:3], off offset:2048
	global_load_dword v147, v[2:3], off offset:3072
	global_load_dword v148, v[6:7], off offset:-4096
	global_load_dword v149, v[6:7], off
	global_load_dword v150, v[6:7], off offset:1024
	global_load_dword v151, v[6:7], off offset:2048
	global_load_dword v152, v[6:7], off offset:3072
	s_waitcnt lgkmcnt(0)
	s_barrier
	ds_read2_b64 v[0:3], v86 offset1:1
	ds_read2_b64 v[4:7], v86 offset0:2 offset1:3
	ds_read2_b64 v[80:83], v86 offset0:8 offset1:9
	ds_read2_b64 v[114:117], v86 offset0:4 offset1:5
	ds_read2_b64 v[118:121], v86 offset0:6 offset1:7
	ds_read2_b64 v[122:125], v86 offset0:12 offset1:13
	ds_read2_b64 v[126:129], v86 offset0:10 offset1:11
	ds_read2_b64 v[130:133], v86 offset0:14 offset1:15
	s_waitcnt lgkmcnt(5)
	v_pk_add_f32 v[134:135], v[0:1], v[80:81]
	v_pk_add_f32 v[0:1], v[0:1], v[80:81] neg_lo:[0,1] neg_hi:[0,1]
	s_waitcnt lgkmcnt(2)
	v_pk_add_f32 v[80:81], v[114:115], v[122:123]
	v_pk_add_f32 v[114:115], v[114:115], v[122:123] neg_lo:[0,1] neg_hi:[0,1]
	v_pk_add_f32 v[122:123], v[134:135], v[80:81]
	v_pk_add_f32 v[80:81], v[134:135], v[80:81] neg_lo:[0,1] neg_hi:[0,1]
	v_pk_fma_f32 v[134:135], v[114:115], s[28:29], v[0:1] op_sel:[1,0,0] op_sel_hi:[0,1,1]
	v_pk_fma_f32 v[0:1], v[114:115], s[26:27], v[0:1] op_sel:[1,0,0] op_sel_hi:[0,1,1]
	v_pk_add_f32 v[114:115], v[2:3], v[82:83]
	v_pk_add_f32 v[2:3], v[2:3], v[82:83] neg_lo:[0,1] neg_hi:[0,1]
	v_pk_add_f32 v[82:83], v[116:117], v[124:125]
	v_pk_add_f32 v[116:117], v[116:117], v[124:125] neg_lo:[0,1] neg_hi:[0,1]
	v_pk_add_f32 v[124:125], v[114:115], v[82:83]
	v_pk_add_f32 v[82:83], v[114:115], v[82:83] neg_lo:[0,1] neg_hi:[0,1]
	v_pk_fma_f32 v[114:115], v[116:117], s[28:29], v[2:3] op_sel:[1,0,0] op_sel_hi:[0,1,1]
	v_pk_fma_f32 v[2:3], v[116:117], s[26:27], v[2:3] op_sel:[1,0,0] op_sel_hi:[0,1,1]
	s_waitcnt lgkmcnt(1)
	v_pk_add_f32 v[116:117], v[4:5], v[126:127]
	v_pk_add_f32 v[4:5], v[4:5], v[126:127] neg_lo:[0,1] neg_hi:[0,1]
	s_waitcnt lgkmcnt(0)
	v_pk_add_f32 v[126:127], v[118:119], v[130:131]
	v_pk_add_f32 v[118:119], v[118:119], v[130:131] neg_lo:[0,1] neg_hi:[0,1]
	v_pk_add_f32 v[130:131], v[116:117], v[126:127]
	v_pk_add_f32 v[116:117], v[116:117], v[126:127] neg_lo:[0,1] neg_hi:[0,1]
	v_pk_fma_f32 v[126:127], v[118:119], s[28:29], v[4:5] op_sel:[1,0,0] op_sel_hi:[0,1,1]
	v_pk_fma_f32 v[4:5], v[118:119], s[26:27], v[4:5] op_sel:[1,0,0] op_sel_hi:[0,1,1]
	v_pk_add_f32 v[118:119], v[6:7], v[128:129]
	v_pk_add_f32 v[6:7], v[6:7], v[128:129] neg_lo:[0,1] neg_hi:[0,1]
	v_pk_add_f32 v[128:129], v[120:121], v[132:133]
	v_pk_add_f32 v[120:121], v[120:121], v[132:133] neg_lo:[0,1] neg_hi:[0,1]
	v_pk_add_f32 v[132:133], v[118:119], v[128:129]
	v_pk_add_f32 v[118:119], v[118:119], v[128:129] neg_lo:[0,1] neg_hi:[0,1]
	v_pk_fma_f32 v[128:129], v[120:121], s[28:29], v[6:7] op_sel:[1,0,0] op_sel_hi:[0,1,1]
	v_pk_fma_f32 v[6:7], v[120:121], s[26:27], v[6:7] op_sel:[1,0,0] op_sel_hi:[0,1,1]
	v_pk_mul_f32 v[120:121], v[114:115], s[8:9] op_sel_hi:[0,1]
	v_pk_fma_f32 v[114:115], v[114:115], s[0:1], v[120:121] op_sel:[1,0,0]
	v_pk_mul_f32 v[120:121], v[126:127], s[6:7] op_sel_hi:[0,1]
	v_pk_fma_f32 v[120:121], v[126:127], s[12:13], v[120:121] op_sel:[1,0,0] op_sel_hi:[1,0,1]
	v_pk_mul_f32 v[126:127], v[128:129], s[4:5] op_sel_hi:[0,1]
	v_pk_fma_f32 v[126:127], v[128:129], s[34:35], v[126:127] op_sel:[1,0,0]
	v_pk_mul_f32 v[128:129], v[82:83], s[6:7] op_sel_hi:[0,1]
	v_pk_fma_f32 v[82:83], v[82:83], s[12:13], v[128:129] op_sel:[1,0,0] op_sel_hi:[1,0,1]
	v_pk_mul_f32 v[128:129], v[116:117], s[18:19] op_sel_hi:[0,1]
	v_pk_fma_f32 v[116:117], v[116:117], s[50:51], v[128:129] op_sel:[1,0,0]
	v_pk_mul_f32 v[128:129], v[2:3], s[4:5] op_sel_hi:[0,1]
	v_pk_fma_f32 v[2:3], v[2:3], s[34:35], v[128:129] op_sel:[1,0,0]
	v_pk_mul_f32 v[128:129], v[6:7], s[38:39] op_sel_hi:[0,1]
	v_mul_f32_e32 v86, 0xbf3504f3, v118
	v_pk_fma_f32 v[6:7], v[6:7], s[30:31], v[128:129] op_sel:[1,0,0]
	v_pk_add_f32 v[128:129], v[122:123], v[130:131]
	v_pk_add_f32 v[122:123], v[122:123], v[130:131] neg_lo:[0,1] neg_hi:[0,1]
	v_pk_add_f32 v[130:131], v[124:125], v[132:133]
	v_pk_add_f32 v[124:125], v[124:125], v[132:133] neg_lo:[0,1] neg_hi:[0,1]
	v_pk_fma_f32 v[118:119], v[118:119], s[6:7], v[86:87] op_sel:[1,0,0] op_sel_hi:[1,1,0]
	v_mul_f32_e32 v86, 0xbf3504f3, v4
	v_pk_add_f32 v[132:133], v[128:129], v[130:131]
	v_pk_add_f32 v[128:129], v[128:129], v[130:131] neg_lo:[0,1] neg_hi:[0,1]
	v_pk_fma_f32 v[130:131], v[124:125], s[28:29], v[122:123] op_sel:[1,0,0] op_sel_hi:[0,1,1]
	v_pk_fma_f32 v[122:123], v[124:125], s[26:27], v[122:123] op_sel:[1,0,0] op_sel_hi:[0,1,1]
	v_pk_add_f32 v[124:125], v[134:135], v[120:121]
	v_pk_add_f32 v[120:121], v[134:135], v[120:121] neg_lo:[0,1] neg_hi:[0,1]
	v_pk_add_f32 v[134:135], v[114:115], v[126:127]
	v_pk_add_f32 v[114:115], v[114:115], v[126:127] neg_lo:[0,1] neg_hi:[0,1]
	v_pk_fma_f32 v[4:5], v[4:5], s[6:7], v[86:87] op_sel:[1,0,0] op_sel_hi:[1,1,0]
	v_pk_add_f32 v[126:127], v[124:125], v[134:135]
	v_pk_add_f32 v[124:125], v[124:125], v[134:135] neg_lo:[0,1] neg_hi:[0,1]
	v_pk_fma_f32 v[134:135], v[114:115], s[28:29], v[120:121] op_sel:[1,0,0] op_sel_hi:[0,1,1]
	v_pk_fma_f32 v[114:115], v[114:115], s[26:27], v[120:121] op_sel:[1,0,0] op_sel_hi:[0,1,1]
	v_pk_add_f32 v[120:121], v[80:81], v[116:117]
	v_pk_add_f32 v[80:81], v[80:81], v[116:117] neg_lo:[0,1] neg_hi:[0,1]
	v_pk_add_f32 v[116:117], v[82:83], v[118:119]
	v_pk_add_f32 v[82:83], v[82:83], v[118:119] neg_lo:[0,1] neg_hi:[0,1]
	v_pk_add_f32 v[118:119], v[120:121], v[116:117]
	v_pk_add_f32 v[116:117], v[120:121], v[116:117] neg_lo:[0,1] neg_hi:[0,1]
	v_pk_fma_f32 v[120:121], v[82:83], s[28:29], v[80:81] op_sel:[1,0,0] op_sel_hi:[0,1,1]
	v_pk_fma_f32 v[80:81], v[82:83], s[26:27], v[80:81] op_sel:[1,0,0] op_sel_hi:[0,1,1]
	v_pk_add_f32 v[82:83], v[0:1], v[4:5]
	v_pk_add_f32 v[0:1], v[0:1], v[4:5] neg_lo:[0,1] neg_hi:[0,1]
	v_pk_add_f32 v[4:5], v[2:3], v[6:7]
	v_pk_add_f32 v[2:3], v[2:3], v[6:7] neg_lo:[0,1] neg_hi:[0,1]
	v_pk_add_f32 v[6:7], v[82:83], v[4:5]
	v_pk_add_f32 v[4:5], v[82:83], v[4:5] neg_lo:[0,1] neg_hi:[0,1]
	v_pk_fma_f32 v[82:83], v[2:3], s[28:29], v[0:1] op_sel:[1,0,0] op_sel_hi:[0,1,1]
	v_pk_fma_f32 v[0:1], v[2:3], s[26:27], v[0:1] op_sel:[1,0,0] op_sel_hi:[0,1,1]
	s_waitcnt vmcnt(15)
	v_lshlrev_b32_e32 v2, 16, v136
	v_and_b32_e32 v3, 0xffff0000, v136
	v_pk_mul_f32 v[136:137], v[2:3], s[28:29]
	v_pk_mul_f32 v[2:3], v[132:133], v[2:3] op_sel_hi:[0,1]
	v_pk_fma_f32 v[2:3], v[132:133], v[136:137], v[2:3] op_sel:[1,1,0] op_sel_hi:[1,0,1]
	s_waitcnt vmcnt(14)
	v_lshlrev_b32_e32 v132, 16, v138
	v_and_b32_e32 v133, 0xffff0000, v138
	v_pk_mul_f32 v[136:137], v[132:133], s[28:29]
	v_pk_mul_f32 v[132:133], v[126:127], v[132:133] op_sel_hi:[0,1]
	v_pk_fma_f32 v[126:127], v[126:127], v[136:137], v[132:133] op_sel:[1,1,0] op_sel_hi:[1,0,1]
	s_waitcnt vmcnt(13)
	v_lshlrev_b32_e32 v132, 16, v139
	v_and_b32_e32 v133, 0xffff0000, v139
	v_pk_mul_f32 v[136:137], v[132:133], s[28:29]
	v_pk_mul_f32 v[132:133], v[118:119], v[132:133] op_sel_hi:[0,1]
	v_pk_fma_f32 v[118:119], v[118:119], v[136:137], v[132:133] op_sel:[1,1,0] op_sel_hi:[1,0,1]
	s_waitcnt vmcnt(12)
	v_lshlrev_b32_e32 v132, 16, v140
	v_and_b32_e32 v133, 0xffff0000, v140
	v_pk_mul_f32 v[136:137], v[132:133], s[28:29]
	v_pk_mul_f32 v[132:133], v[6:7], v[132:133] op_sel_hi:[0,1]
	v_pk_fma_f32 v[6:7], v[6:7], v[136:137], v[132:133] op_sel:[1,1,0] op_sel_hi:[1,0,1]
	s_waitcnt vmcnt(11)
	v_lshlrev_b32_e32 v132, 16, v141
	v_and_b32_e32 v133, 0xffff0000, v141
	v_pk_mul_f32 v[136:137], v[132:133], s[28:29]
	v_pk_mul_f32 v[132:133], v[130:131], v[132:133] op_sel_hi:[0,1]
	v_pk_fma_f32 v[130:131], v[130:131], v[136:137], v[132:133] op_sel:[1,1,0] op_sel_hi:[1,0,1]
	s_waitcnt vmcnt(7)
	v_lshlrev_b32_e32 v132, 16, v145
	v_and_b32_e32 v133, 0xffff0000, v145
	v_pk_mul_f32 v[136:137], v[132:133], s[28:29]
	v_pk_mul_f32 v[132:133], v[134:135], v[132:133] op_sel_hi:[0,1]
	v_pk_fma_f32 v[132:133], v[134:135], v[136:137], v[132:133] op_sel:[1,1,0] op_sel_hi:[1,0,1]
	s_waitcnt vmcnt(6)
	v_lshlrev_b32_e32 v134, 16, v146
	v_and_b32_e32 v135, 0xffff0000, v146
	v_pk_mul_f32 v[136:137], v[134:135], s[28:29]
	v_pk_mul_f32 v[134:135], v[120:121], v[134:135] op_sel_hi:[0,1]
	v_pk_fma_f32 v[120:121], v[120:121], v[136:137], v[134:135] op_sel:[1,1,0] op_sel_hi:[1,0,1]
	s_waitcnt vmcnt(5)
	v_lshlrev_b32_e32 v134, 16, v147
	v_and_b32_e32 v135, 0xffff0000, v147
	v_pk_mul_f32 v[136:137], v[134:135], s[28:29]
	v_pk_mul_f32 v[134:135], v[82:83], v[134:135] op_sel_hi:[0,1]
	v_pk_fma_f32 v[134:135], v[82:83], v[136:137], v[134:135] op_sel:[1,1,0] op_sel_hi:[1,0,1]
	s_waitcnt vmcnt(4)
	v_lshlrev_b32_e32 v82, 16, v148
	v_and_b32_e32 v83, 0xffff0000, v148
	v_pk_mul_f32 v[136:137], v[82:83], s[28:29]
	v_pk_mul_f32 v[82:83], v[128:129], v[82:83] op_sel_hi:[0,1]
	v_pk_fma_f32 v[128:129], v[128:129], v[136:137], v[82:83] op_sel:[1,1,0] op_sel_hi:[1,0,1]
	v_lshlrev_b32_e32 v82, 16, v142
	v_and_b32_e32 v83, 0xffff0000, v142
	v_pk_mul_f32 v[136:137], v[82:83], s[28:29]
	v_pk_mul_f32 v[82:83], v[124:125], v[82:83] op_sel_hi:[0,1]
	v_pk_fma_f32 v[124:125], v[124:125], v[136:137], v[82:83] op_sel:[1,1,0] op_sel_hi:[1,0,1]
	v_lshlrev_b32_e32 v82, 16, v143
	v_and_b32_e32 v83, 0xffff0000, v143
	v_pk_mul_f32 v[136:137], v[82:83], s[28:29]
	v_pk_mul_f32 v[82:83], v[116:117], v[82:83] op_sel_hi:[0,1]
	v_pk_fma_f32 v[116:117], v[116:117], v[136:137], v[82:83] op_sel:[1,1,0] op_sel_hi:[1,0,1]
	v_lshlrev_b32_e32 v82, 16, v144
	v_and_b32_e32 v83, 0xffff0000, v144
	v_pk_mul_f32 v[136:137], v[82:83], s[28:29]
	v_pk_mul_f32 v[82:83], v[4:5], v[82:83] op_sel_hi:[0,1]
	v_pk_fma_f32 v[4:5], v[4:5], v[136:137], v[82:83] op_sel:[1,1,0] op_sel_hi:[1,0,1]
	s_waitcnt vmcnt(3)
	v_lshlrev_b32_e32 v82, 16, v149
	v_and_b32_e32 v83, 0xffff0000, v149
	v_pk_mul_f32 v[136:137], v[82:83], s[28:29]
	v_pk_mul_f32 v[82:83], v[122:123], v[82:83] op_sel_hi:[0,1]
	v_pk_fma_f32 v[122:123], v[122:123], v[136:137], v[82:83] op_sel:[1,1,0] op_sel_hi:[1,0,1]
	s_waitcnt vmcnt(2)
	v_lshlrev_b32_e32 v82, 16, v150
	v_and_b32_e32 v83, 0xffff0000, v150
	v_pk_mul_f32 v[136:137], v[82:83], s[28:29]
	v_pk_mul_f32 v[82:83], v[114:115], v[82:83] op_sel_hi:[0,1]
	v_pk_fma_f32 v[136:137], v[114:115], v[136:137], v[82:83] op_sel:[1,1,0] op_sel_hi:[1,0,1]
	s_waitcnt vmcnt(1)
	v_lshlrev_b32_e32 v82, 16, v151
	v_and_b32_e32 v83, 0xffff0000, v151
	v_pk_mul_f32 v[114:115], v[82:83], s[28:29]
	v_pk_mul_f32 v[82:83], v[80:81], v[82:83] op_sel_hi:[0,1]
	v_pk_fma_f32 v[138:139], v[80:81], v[114:115], v[82:83] op_sel:[1,1,0] op_sel_hi:[1,0,1]
	s_waitcnt vmcnt(0)
	v_lshlrev_b32_e32 v80, 16, v152
	v_and_b32_e32 v81, 0xffff0000, v152
	v_pk_add_f32 v[140:141], v[2:3], v[128:129]
	v_pk_add_f32 v[2:3], v[2:3], v[128:129] neg_lo:[0,1] neg_hi:[0,1]
	v_pk_add_f32 v[128:129], v[130:131], v[122:123]
	v_pk_add_f32 v[122:123], v[130:131], v[122:123] neg_lo:[0,1] neg_hi:[0,1]
	v_pk_mul_f32 v[82:83], v[80:81], s[28:29]
	v_pk_mul_f32 v[80:81], v[0:1], v[80:81] op_sel_hi:[0,1]
	v_pk_add_f32 v[130:131], v[140:141], v[128:129]
	v_pk_add_f32 v[128:129], v[140:141], v[128:129] neg_lo:[0,1] neg_hi:[0,1]
	v_pk_fma_f32 v[140:141], v[122:123], s[26:27], v[2:3] op_sel:[1,0,0] op_sel_hi:[0,1,1]
	v_pk_fma_f32 v[2:3], v[122:123], s[28:29], v[2:3] op_sel:[1,0,0] op_sel_hi:[0,1,1]
	v_pk_add_f32 v[122:123], v[126:127], v[124:125]
	v_pk_add_f32 v[124:125], v[126:127], v[124:125] neg_lo:[0,1] neg_hi:[0,1]
	v_pk_add_f32 v[126:127], v[132:133], v[136:137]
	v_pk_add_f32 v[132:133], v[132:133], v[136:137] neg_lo:[0,1] neg_hi:[0,1]
	v_pk_fma_f32 v[0:1], v[0:1], v[82:83], v[80:81] op_sel:[1,1,0] op_sel_hi:[1,0,1]
	v_pk_add_f32 v[136:137], v[122:123], v[126:127]
	v_pk_add_f32 v[122:123], v[122:123], v[126:127] neg_lo:[0,1] neg_hi:[0,1]
	v_pk_fma_f32 v[126:127], v[132:133], s[26:27], v[124:125] op_sel:[1,0,0] op_sel_hi:[0,1,1]
	v_pk_fma_f32 v[124:125], v[132:133], s[28:29], v[124:125] op_sel:[1,0,0] op_sel_hi:[0,1,1]
	v_pk_add_f32 v[132:133], v[118:119], v[116:117]
	v_pk_add_f32 v[116:117], v[118:119], v[116:117] neg_lo:[0,1] neg_hi:[0,1]
	v_pk_add_f32 v[118:119], v[120:121], v[138:139]
	v_pk_add_f32 v[120:121], v[120:121], v[138:139] neg_lo:[0,1] neg_hi:[0,1]
	v_pk_add_f32 v[138:139], v[132:133], v[118:119]
	v_pk_add_f32 v[118:119], v[132:133], v[118:119] neg_lo:[0,1] neg_hi:[0,1]
	v_pk_fma_f32 v[132:133], v[120:121], s[26:27], v[116:117] op_sel:[1,0,0] op_sel_hi:[0,1,1]
	v_pk_fma_f32 v[116:117], v[120:121], s[28:29], v[116:117] op_sel:[1,0,0] op_sel_hi:[0,1,1]
	v_pk_add_f32 v[120:121], v[6:7], v[4:5]
	v_pk_add_f32 v[4:5], v[6:7], v[4:5] neg_lo:[0,1] neg_hi:[0,1]
	v_pk_add_f32 v[6:7], v[134:135], v[0:1]
	v_pk_add_f32 v[0:1], v[134:135], v[0:1] neg_lo:[0,1] neg_hi:[0,1]
	v_pk_add_f32 v[134:135], v[120:121], v[6:7]
	v_pk_add_f32 v[6:7], v[120:121], v[6:7] neg_lo:[0,1] neg_hi:[0,1]
	v_pk_fma_f32 v[120:121], v[0:1], s[26:27], v[4:5] op_sel:[1,0,0] op_sel_hi:[0,1,1]
	v_pk_fma_f32 v[0:1], v[0:1], s[28:29], v[4:5] op_sel:[1,0,0] op_sel_hi:[0,1,1]
	v_pk_mul_f32 v[4:5], v[126:127], s[34:35] op_sel_hi:[0,1]
	s_mov_b32 s31, s34
	v_mul_f32_e32 v86, 0x3f3504f3, v132
	v_pk_fma_f32 v[4:5], v[126:127], s[30:31], v[4:5] op_sel:[1,0,0]
	v_pk_fma_f32 v[126:127], v[132:133], s[36:37], v[86:87] op_sel:[1,0,0] op_sel_hi:[1,1,0]
	v_pk_mul_f32 v[132:133], v[120:121], s[0:1] op_sel_hi:[0,1]
	s_mov_b32 s19, s27
	v_pk_fma_f32 v[120:121], v[120:121], s[38:39], v[132:133] op_sel:[1,0,0]
	v_pk_mul_f32 v[132:133], v[118:119], s[18:19] op_sel_hi:[0,1]
	s_mov_b32 s6, s26
	s_mov_b32 s7, s18
	v_pk_fma_f32 v[118:119], v[118:119], s[6:7], v[132:133] op_sel:[1,0,0]
	v_pk_mul_f32 v[132:133], v[6:7], s[36:37] op_sel_hi:[0,1]
	v_pk_fma_f32 v[6:7], v[6:7], s[36:37], v[132:133] op_sel:[1,0,0] op_sel_hi:[1,0,1]
	v_pk_mul_f32 v[132:133], v[124:125], s[0:1] op_sel_hi:[0,1]
	s_min_i32 s0, s56, s59
	s_mul_i32 s0, s0, s3
	v_pk_fma_f32 v[124:125], v[124:125], s[38:39], v[132:133] op_sel:[1,0,0]
	v_pk_mul_f32 v[132:133], v[116:117], s[36:37] op_sel_hi:[0,1]
	s_mov_b32 s39, s30
	s_add_i32 s0, s0, s2
	v_pk_fma_f32 v[116:117], v[116:117], s[36:37], v[132:133] op_sel:[1,0,0] op_sel_hi:[1,0,1]
	v_pk_mul_f32 v[132:133], v[0:1], s[38:39] op_sel_hi:[0,1]
	s_mul_hi_i32 s1, s0, 0x2aaaaaab
	v_pk_fma_f32 v[0:1], v[0:1], s[4:5], v[132:133] op_sel:[1,0,0]
	s_lshr_b32 s4, s1, 31
	s_lshr_b32 s1, s1, 7
	v_mul_f32_e32 v86, 0x3f3504f3, v122
	v_pk_add_f32 v[132:133], v[130:131], v[138:139]
	v_pk_add_f32 v[130:131], v[130:131], v[138:139] neg_lo:[0,1] neg_hi:[0,1]
	v_pk_add_f32 v[138:139], v[136:137], v[134:135]
	v_pk_add_f32 v[134:135], v[136:137], v[134:135] neg_lo:[0,1] neg_hi:[0,1]
	s_add_i32 s1, s1, s4
	v_pk_fma_f32 v[122:123], v[122:123], s[36:37], v[86:87] op_sel:[1,0,0] op_sel_hi:[1,1,0]
	v_pk_add_f32 v[136:137], v[132:133], v[138:139]
	v_pk_add_f32 v[132:133], v[132:133], v[138:139] neg_lo:[0,1] neg_hi:[0,1]
	v_pk_fma_f32 v[138:139], v[134:135], s[26:27], v[130:131] op_sel:[1,0,0] op_sel_hi:[0,1,1]
	v_pk_fma_f32 v[130:131], v[134:135], s[28:29], v[130:131] op_sel:[1,0,0] op_sel_hi:[0,1,1]
	v_pk_add_f32 v[134:135], v[140:141], v[126:127]
	v_pk_add_f32 v[126:127], v[140:141], v[126:127] neg_lo:[0,1] neg_hi:[0,1]
	v_pk_add_f32 v[140:141], v[4:5], v[120:121]
	v_pk_add_f32 v[4:5], v[4:5], v[120:121] neg_lo:[0,1] neg_hi:[0,1]
	s_mulk_i32 s1, 0x300
	v_pk_add_f32 v[120:121], v[134:135], v[140:141]
	v_pk_add_f32 v[134:135], v[134:135], v[140:141] neg_lo:[0,1] neg_hi:[0,1]
	v_pk_fma_f32 v[140:141], v[4:5], s[26:27], v[126:127] op_sel:[1,0,0] op_sel_hi:[0,1,1]
	v_pk_fma_f32 v[4:5], v[4:5], s[28:29], v[126:127] op_sel:[1,0,0] op_sel_hi:[0,1,1]
	v_pk_add_f32 v[126:127], v[128:129], v[118:119]
	v_pk_add_f32 v[118:119], v[128:129], v[118:119] neg_lo:[0,1] neg_hi:[0,1]
	v_pk_add_f32 v[128:129], v[122:123], v[6:7]
	v_pk_add_f32 v[6:7], v[122:123], v[6:7] neg_lo:[0,1] neg_hi:[0,1]
	s_sub_i32 s0, s0, s1
	v_mov_b32_e32 v115, v220
	v_mov_b32_e32 v81, v221
	v_mov_b32_e32 v114, v217
	v_mov_b32_e32 v80, v218
	v_mov_b32_e32 v82, v215
	v_pk_add_f32 v[122:123], v[126:127], v[128:129]
	v_pk_add_f32 v[126:127], v[126:127], v[128:129] neg_lo:[0,1] neg_hi:[0,1]
	v_pk_fma_f32 v[128:129], v[6:7], s[26:27], v[118:119] op_sel:[1,0,0] op_sel_hi:[0,1,1]
	v_pk_fma_f32 v[6:7], v[6:7], s[28:29], v[118:119] op_sel:[1,0,0] op_sel_hi:[0,1,1]
	v_pk_add_f32 v[118:119], v[2:3], v[116:117]
	v_pk_add_f32 v[2:3], v[2:3], v[116:117] neg_lo:[0,1] neg_hi:[0,1]
	v_pk_add_f32 v[116:117], v[124:125], v[0:1]
	v_pk_add_f32 v[0:1], v[124:125], v[0:1] neg_lo:[0,1] neg_hi:[0,1]
	s_cmpk_lt_i32 s0, 0x200
	v_pk_add_f32 v[124:125], v[118:119], v[116:117]
	v_pk_add_f32 v[116:117], v[118:119], v[116:117] neg_lo:[0,1] neg_hi:[0,1]
	v_pk_fma_f32 v[118:119], v[0:1], s[26:27], v[2:3] op_sel:[1,0,0] op_sel_hi:[0,1,1]
	v_pk_fma_f32 v[0:1], v[0:1], s[28:29], v[2:3] op_sel:[1,0,0] op_sel_hi:[0,1,1]
	v_lshlrev_b32_e32 v83, 3, v82
	v_lshlrev_b32_e32 v2, 7, v82
	s_cselect_b64 vcc, -1, 0
	v_add3_u32 v2, v219, v83, v2
	v_cndmask_b32_e32 v86, v211, v212, vcc
	ds_write2_b64 v2, v[136:137], v[120:121] offset1:1
	ds_write2_b64 v2, v[122:123], v[124:125] offset0:2 offset1:3
	ds_write2_b64 v2, v[138:139], v[140:141] offset0:4 offset1:5
	ds_write2_b64 v2, v[128:129], v[118:119] offset0:6 offset1:7
	ds_write2_b64 v2, v[132:133], v[134:135] offset0:8 offset1:9
	ds_write2_b64 v2, v[126:127], v[116:117] offset0:10 offset1:11
	ds_write2_b64 v2, v[130:131], v[4:5] offset0:12 offset1:13
	ds_write2_b64 v2, v[6:7], v[0:1] offset0:14 offset1:15
	v_mul_f32_e32 v1, v48, v86
	v_mul_f32_e32 v2, v52, v86
	v_mov_b32_e32 v0, v87
	v_cvt_pk_fp8_f32 v0, v1, v2
	v_mul_f32_e32 v2, v49, v86
	v_mul_f32_e32 v5, v53, v86
	v_mov_b32_e32 v1, v87
	v_cvt_pk_fp8_f32 v1, v2, v5
	v_mul_f32_e32 v3, v64, v86
	v_mul_f32_e32 v4, v68, v86
	v_cvt_pk_fp8_f32 v0, v3, v4 op_sel:[0,0,1]
	v_mul_f32_e32 v2, v65, v86
	v_mul_f32_e32 v3, v69, v86
	v_cvt_pk_fp8_f32 v1, v2, v3 op_sel:[0,0,1]
	v_mul_f32_e32 v3, v50, v86
	v_mul_f32_e32 v4, v54, v86
	v_mov_b32_e32 v2, v87
	v_cvt_pk_fp8_f32 v2, v3, v4
	v_mul_f32_e32 v4, v51, v86
	v_mul_f32_e32 v7, v55, v86
	v_mov_b32_e32 v3, v87
	v_cvt_pk_fp8_f32 v3, v4, v7
	v_mul_f32_e32 v5, v66, v86
	v_mul_f32_e32 v6, v70, v86
	v_cvt_pk_fp8_f32 v2, v5, v6 op_sel:[0,0,1]
	v_mul_f32_e32 v4, v67, v86
	v_mul_f32_e32 v5, v71, v86
	v_cvt_pk_fp8_f32 v3, v4, v5 op_sel:[0,0,1]
	v_mul_f32_e32 v5, v40, v86
	v_mul_f32_e32 v6, v86, v44
	v_mov_b32_e32 v4, v87
	v_cvt_pk_fp8_f32 v4, v5, v6
	v_mul_f32_e32 v6, v41, v86
	v_mul_f32_e32 v41, v86, v45
	v_mov_b32_e32 v5, v87
	v_cvt_pk_fp8_f32 v5, v6, v41
	v_mul_f32_e32 v7, v86, v56
	v_mul_f32_e32 v40, v86, v60
	v_cvt_pk_fp8_f32 v4, v7, v40 op_sel:[0,0,1]
	v_mul_f32_e32 v6, v86, v57
	v_mul_f32_e32 v7, v86, v61
	v_cvt_pk_fp8_f32 v5, v6, v7 op_sel:[0,0,1]
	v_mul_f32_e32 v7, v42, v86
	v_mul_f32_e32 v40, v86, v46
	v_mov_b32_e32 v6, v87
	s_min_i32 s0, s62, s59
	v_cvt_pk_fp8_f32 v6, v7, v40
	v_mul_f32_e32 v40, v43, v86
	v_mul_f32_e32 v43, v86, v47
	v_mov_b32_e32 v7, v87
	s_mul_i32 s0, s0, s3
	v_cvt_pk_fp8_f32 v7, v40, v43
	s_add_i32 s1, s0, s2
	s_mul_hi_i32 s0, s1, 0x2aaaaaab
	v_mul_f32_e32 v41, v86, v58
	v_mul_f32_e32 v42, v86, v62
	s_lshr_b32 s4, s0, 31
	s_ashr_i32 s0, s0, 7
	v_cvt_pk_fp8_f32 v6, v41, v42 op_sel:[0,0,1]
	v_mul_f32_e32 v40, v86, v59
	v_mul_f32_e32 v41, v86, v63
	s_add_i32 s4, s0, s4
	v_cvt_pk_fp8_f32 v7, v40, v41 op_sel:[0,0,1]
	s_add_i32 s0, s4, 18
	s_mulk_i32 s4, 0x300
	s_sub_i32 s19, s1, s4
	s_cmpk_lt_i32 s19, 0x200
	s_cselect_b64 s[4:5], -1, 0
	s_cmpk_gt_i32 s19, 0x1ff
	s_mov_b64 s[12:13], -1
	s_waitcnt lgkmcnt(0)
	s_barrier
	ds_write_b128 v236, v[0:3]
	ds_write_b128 v237, v[4:7]
	s_cbranch_scc0 .LBB0_807
	s_load_dwordx2 s[6:7], s[14:15], 0x110
	s_ashr_i32 s1, s0, 31
	s_lshl_b64 s[12:13], s[0:1], 24
	s_mov_b32 s9, s18
	s_waitcnt lgkmcnt(0)
	s_add_u32 s6, s6, s12
	s_addc_u32 s7, s7, s13
	s_lshl_b32 s1, s19, 3
	s_and_b32 s1, s1, 0x7fffffc0
	s_add_i32 s8, s1, 0xfffff000
	s_mov_b64 s[12:13], 0

.LBB0_809:
	s_lshl_b64 s[8:9], s[8:9], 13
	s_add_u32 s0, s6, s8
	s_addc_u32 s7, s7, s9
	s_lshl_b32 s1, s19, s1
	s_and_b32 s1, s1, 0x700
	s_lshl_b32 s1, s1, 2
	s_add_u32 s6, s0, s1
	s_addc_u32 s7, s7, 0
	s_cmp_gt_i32 s62, s59
	s_cselect_b64 s[0:1], -1, 0
	v_cndmask_b32_e64 v0, v180, 0, s[0:1]
	s_and_b64 s[8:9], s[0:1], exec
	s_cselect_b32 s8, 0, 0x800
	v_lshlrev_b32_e32 v86, 2, v0
	v_lshl_add_u64 v[40:41], s[6:7], 0, v[86:87]
	v_mad_i64_i32 v[0:1], s[6:7], s8, v181, 0
	v_mad_i64_i32 v[2:3], s[6:7], s8, v182, 0
	v_lshl_add_u64 v[0:1], v[0:1], 2, v[40:41]
	v_lshl_add_u64 v[2:3], v[2:3], 2, v[40:41]
	global_load_dwordx4 v[48:51], v[0:1], off nt
	global_load_dwordx4 v[52:55], v[2:3], off nt
	v_mad_i64_i32 v[0:1], s[6:7], s8, v183, 0
	v_mad_i64_i32 v[2:3], s[6:7], s8, v184, 0
	v_lshl_add_u64 v[0:1], v[0:1], 2, v[40:41]
	v_lshl_add_u64 v[2:3], v[2:3], 2, v[40:41]
	global_load_dwordx4 v[56:59], v[0:1], off nt
	global_load_dwordx4 v[60:63], v[2:3], off nt
	v_mad_i64_i32 v[0:1], s[6:7], s8, v185, 0
	v_mad_i64_i32 v[2:3], s[6:7], s8, v186, 0
	v_mad_i64_i32 v[42:43], s[6:7], s8, v187, 0
	v_mad_i64_i32 v[44:45], s[6:7], s8, v188, 0
	v_lshl_add_u64 v[0:1], v[0:1], 2, v[40:41]
	v_lshl_add_u64 v[4:5], v[2:3], 2, v[40:41]
	v_lshl_add_u64 v[42:43], v[42:43], 2, v[40:41]
	v_lshl_add_u64 v[44:45], v[44:45], 2, v[40:41]
	global_load_dwordx4 v[0:3], v[0:1], off nt
	s_nop 0
	global_load_dwordx4 v[4:7], v[4:5], off nt
	s_nop 0
	global_load_dwordx4 v[40:43], v[42:43], off nt
	s_nop 0
	global_load_dwordx4 v[44:47], v[44:45], off nt
	s_add_i32 s19, s62, -3
	s_cmp_gt_i32 s62, 2
	s_cselect_b32 s6, s19, 0
	s_min_i32 s6, s6, s59
	s_mul_i32 s6, s6, s3
	s_add_i32 s7, s6, s2
	s_mul_hi_i32 s6, s7, 0x2aaaaaab
	s_lshr_b32 s8, s6, 31
	s_ashr_i32 s6, s6, 7
	s_add_i32 s8, s6, s8
	s_add_i32 s6, s8, 18
	s_mulk_i32 s8, 0x300
	s_sub_i32 s31, s7, s8
	s_ashr_i32 s7, s6, 31
	s_cmpk_gt_i32 s31, 0x1ff
	s_mov_b64 s[12:13], -1
	s_cbranch_scc0 .LBB0_811
	s_lshl_b32 s8, s31, 3
	s_and_b32 s12, s8, 0x7fffffc0
	s_lshl_b32 s8, s31, 19
	s_and_b32 s13, s8, 0x380000
	s_lshl_b64 s[8:9], s[6:7], 22
	s_add_u32 s8, s16, s8
	s_addc_u32 s9, s17, s9
	s_add_u32 s8, s8, s13
	s_addc_u32 s9, s9, 0
	s_add_u32 s8, s8, s12
	s_addc_u32 s9, s9, 0
	s_add_u32 s8, s8, 0x24dff000
	s_addc_u32 s9, s9, 0
	s_mov_b64 s[12:13], 0

.LBB0_813:
	s_add_i32 s76, s62, 1
	s_cmp_lt_i32 s62, 3
	s_cselect_b64 s[6:7], -1, 0
	s_cmp_gt_i32 s19, s59
	s_cselect_b64 s[50:51], -1, 0
	s_or_b64 s[6:7], s[6:7], s[50:51]
	s_and_b64 s[6:7], s[6:7], exec
	s_cselect_b32 s6, s65, s8
	s_cselect_b32 s8, 0x80, s12
	v_mul_i32_i24_e32 v64, s8, v191
	v_or_b32_e32 v64, v64, v189
	v_ashrrev_i32_e32 v65, 31, v64
	s_cselect_b32 s7, s66, s9
	v_lshlrev_b64 v[64:65], 11, v[64:65]
	v_add_u32_e32 v235, v199, v190
	v_lshl_add_u64 v[64:65], s[6:7], 0, v[64:65]
	v_lshl_add_u64 v[116:117], v[64:65], 0, v[88:89]
	v_add_u32_e32 v238, v199, v200
	ds_read_b32 v64, v235
	ds_read_b32 v65, v235 offset:1040
	ds_read_b32 v66, v235 offset:2080
	ds_read_b32 v67, v235 offset:3120
	ds_read_b32 v68, v238
	ds_read_b32 v69, v238 offset:1040
	ds_read_b32 v70, v238 offset:2080
	ds_read_b32 v71, v238 offset:3120
	s_waitcnt lgkmcnt(4)
	global_store_dwordx4 v[116:117], v[64:67], off
	v_pk_mul_f32 v[80:81], v[80:81], s[28:29]
	s_mov_b32 s31, s34
	v_mul_i32_i24_e32 v64, s8, v201
	v_or_b32_e32 v64, v64, v189
	v_ashrrev_i32_e32 v65, 31, v64
	v_lshlrev_b64 v[64:65], 11, v[64:65]
	v_lshl_add_u64 v[64:65], s[6:7], 0, v[64:65]
	v_lshl_add_u64 v[64:65], v[64:65], 0, v[88:89]
	s_waitcnt lgkmcnt(0)
	global_store_dwordx4 v[64:65], v[68:71], off
	v_ashrrev_i32_e32 v64, 4, v82
	v_lshlrev_b32_e32 v65, 8, v64
	v_pk_mul_f32 v[142:143], v[80:81], s[28:29]
	v_pk_mul_f32 v[144:145], v[80:81], v[80:81] op_sel_hi:[1,0]
	v_ashrrev_i32_e32 v65, 1, v65
	v_pk_fma_f32 v[144:145], v[80:81], v[142:143], v[144:145] op_sel:[1,1,0] op_sel_hi:[1,0,1]
	v_lshlrev_b32_e32 v67, 11, v64
	v_and_b32_e32 v68, 0x78, v83
	v_add_u32_e32 v65, v219, v65
	v_pk_mul_f32 v[148:149], v[144:145], s[28:29]
	v_pk_mul_f32 v[150:151], v[144:145], v[144:145] op_sel_hi:[1,0]
	v_lshl_add_u32 v66, v64, 7, v219
	v_add3_u32 v65, v65, v67, v68
	v_pk_fma_f32 v[150:151], v[144:145], v[148:149], v[150:151] op_sel:[1,1,0] op_sel_hi:[1,0,1]
	v_add3_u32 v166, v66, v67, v68
	ds_read2_b64 v[66:69], v65 offset0:17 offset1:34
	ds_read2_b64 v[116:119], v65 offset0:51 offset1:68
	ds_read2_b64 v[120:123], v65 offset0:85 offset1:102
	ds_read2_b64 v[124:127], v65 offset0:119 offset1:136
	ds_read2_b64 v[128:131], v65 offset0:153 offset1:170
	ds_read2_b64 v[132:135], v65 offset0:187 offset1:204
	ds_read2_b64 v[136:139], v65 offset0:221 offset1:238
	ds_read_b64 v[70:71], v166
	ds_read_b64 v[140:141], v65 offset:2040
	v_pk_mul_f32 v[146:147], v[80:81], v[144:145] op_sel_hi:[1,0]
	v_pk_mul_f32 v[152:153], v[80:81], v[150:151] op_sel_hi:[1,0]
	s_waitcnt lgkmcnt(8)
	v_pk_mul_f32 v[164:165], v[80:81], v[66:67] op_sel_hi:[1,0]
	v_pk_fma_f32 v[146:147], v[144:145], v[142:143], v[146:147] op_sel:[1,1,0] op_sel_hi:[1,0,1]
	v_pk_fma_f32 v[152:153], v[150:151], v[142:143], v[152:153] op_sel:[1,1,0] op_sel_hi:[1,0,1]
	v_pk_fma_f32 v[66:67], v[66:67], v[142:143], v[164:165] op_sel:[1,1,0] op_sel_hi:[1,0,1]
	v_pk_mul_f32 v[142:143], v[144:145], v[68:69] op_sel_hi:[1,0]
	v_pk_mul_f32 v[156:157], v[146:147], s[28:29]
	v_pk_fma_f32 v[68:69], v[68:69], v[148:149], v[142:143] op_sel:[1,1,0] op_sel_hi:[1,0,1]
	s_waitcnt lgkmcnt(7)
	v_pk_mul_f32 v[142:143], v[146:147], v[116:117] op_sel_hi:[1,0]
	v_pk_mul_f32 v[154:155], v[144:145], v[150:151] op_sel_hi:[1,0]
	v_pk_mul_f32 v[160:161], v[150:151], s[28:29]
	v_pk_fma_f32 v[116:117], v[116:117], v[156:157], v[142:143] op_sel:[1,1,0] op_sel_hi:[1,0,1]
	v_pk_mul_f32 v[142:143], v[150:151], v[118:119] op_sel_hi:[1,0]
	v_pk_fma_f32 v[154:155], v[150:151], v[148:149], v[154:155] op_sel:[1,1,0] op_sel_hi:[1,0,1]
	v_pk_mul_f32 v[158:159], v[146:147], v[150:151] op_sel_hi:[1,0]
	v_pk_fma_f32 v[118:119], v[118:119], v[160:161], v[142:143] op_sel:[1,1,0] op_sel_hi:[1,0,1]
	v_pk_mul_f32 v[142:143], v[152:153], s[28:29]
	s_waitcnt lgkmcnt(6)
	v_pk_mul_f32 v[148:149], v[152:153], v[120:121] op_sel_hi:[1,0]
	v_pk_fma_f32 v[158:159], v[150:151], v[156:157], v[158:159] op_sel:[1,1,0] op_sel_hi:[1,0,1]
	v_pk_mul_f32 v[162:163], v[150:151], v[150:151] op_sel_hi:[1,0]
	v_pk_fma_f32 v[120:121], v[120:121], v[142:143], v[148:149] op_sel:[1,1,0] op_sel_hi:[1,0,1]
	v_pk_mul_f32 v[142:143], v[154:155], s[28:29]
	v_pk_mul_f32 v[148:149], v[154:155], v[122:123] op_sel_hi:[1,0]
	v_pk_fma_f32 v[162:163], v[150:151], v[160:161], v[162:163] op_sel:[1,1,0] op_sel_hi:[1,0,1]
	v_pk_fma_f32 v[122:123], v[122:123], v[142:143], v[148:149] op_sel:[1,1,0] op_sel_hi:[1,0,1]
	v_pk_mul_f32 v[142:143], v[158:159], s[28:29]
	s_waitcnt lgkmcnt(5)
	v_pk_mul_f32 v[148:149], v[158:159], v[124:125] op_sel_hi:[1,0]
	s_mov_b32 s6, s35
	v_pk_fma_f32 v[124:125], v[124:125], v[142:143], v[148:149] op_sel:[1,1,0] op_sel_hi:[1,0,1]
	v_pk_mul_f32 v[142:143], v[162:163], s[28:29]
	v_pk_mul_f32 v[148:149], v[162:163], v[126:127] op_sel_hi:[1,0]
	s_mov_b32 s7, s34
	v_pk_fma_f32 v[126:127], v[126:127], v[142:143], v[148:149] op_sel:[1,1,0] op_sel_hi:[1,0,1]
	v_pk_mul_f32 v[148:149], v[80:81], v[162:163] op_sel_hi:[0,1]
	v_pk_fma_f32 v[80:81], v[80:81], v[142:143], v[148:149] op_sel:[1,1,0] op_sel_hi:[1,0,1]
	s_mov_b32 s39, s35
	v_pk_mul_f32 v[148:149], v[80:81], s[28:29]
	s_waitcnt lgkmcnt(4)
	v_pk_mul_f32 v[80:81], v[80:81], v[128:129] op_sel_hi:[1,0]
	s_mov_b32 s19, s27
	v_pk_fma_f32 v[80:81], v[128:129], v[148:149], v[80:81] op_sel:[1,1,0] op_sel_hi:[1,0,1]
	v_pk_mul_f32 v[128:129], v[144:145], v[162:163] op_sel_hi:[0,1]
	v_pk_fma_f32 v[128:129], v[144:145], v[142:143], v[128:129] op_sel:[1,1,0] op_sel_hi:[1,0,1]
	s_mov_b32 s8, s26
	v_pk_mul_f32 v[144:145], v[128:129], s[28:29]
	v_pk_mul_f32 v[128:129], v[128:129], v[130:131] op_sel_hi:[1,0]
	s_mov_b32 s9, s18
	v_pk_fma_f32 v[128:129], v[130:131], v[144:145], v[128:129] op_sel:[1,1,0] op_sel_hi:[1,0,1]
	v_pk_mul_f32 v[130:131], v[146:147], v[162:163] op_sel_hi:[0,1]
	v_pk_fma_f32 v[130:131], v[146:147], v[142:143], v[130:131] op_sel:[1,1,0] op_sel_hi:[1,0,1]
	v_add_u32_e32 v240, v202, v197
	v_pk_mul_f32 v[144:145], v[130:131], s[28:29]
	s_waitcnt lgkmcnt(3)
	v_pk_mul_f32 v[130:131], v[130:131], v[132:133] op_sel_hi:[1,0]
	v_add_u32_e32 v241, v202, v198
	v_pk_fma_f32 v[130:131], v[132:133], v[144:145], v[130:131] op_sel:[1,1,0] op_sel_hi:[1,0,1]
	v_pk_mul_f32 v[132:133], v[150:151], v[162:163] op_sel_hi:[0,1]
	v_pk_fma_f32 v[132:133], v[150:151], v[142:143], v[132:133] op_sel:[1,1,0] op_sel_hi:[1,0,1]
	s_mov_b64 s[52:53], -1
	v_pk_mul_f32 v[144:145], v[132:133], s[28:29]
	v_pk_mul_f32 v[132:133], v[132:133], v[134:135] op_sel_hi:[1,0]
	s_nop 0
	v_pk_fma_f32 v[132:133], v[134:135], v[144:145], v[132:133] op_sel:[1,1,0] op_sel_hi:[1,0,1]
	v_pk_mul_f32 v[134:135], v[162:163], v[152:153] op_sel_hi:[1,0]
	s_nop 0
	v_pk_fma_f32 v[134:135], v[152:153], v[142:143], v[134:135] op_sel:[1,1,0] op_sel_hi:[1,0,1]
	s_nop 0
	v_pk_mul_f32 v[144:145], v[134:135], s[28:29]
	s_waitcnt lgkmcnt(2)
	v_pk_mul_f32 v[134:135], v[134:135], v[136:137] op_sel_hi:[1,0]
	s_nop 0
	v_pk_fma_f32 v[134:135], v[136:137], v[144:145], v[134:135] op_sel:[1,1,0] op_sel_hi:[1,0,1]
	v_pk_mul_f32 v[136:137], v[162:163], v[154:155] op_sel_hi:[1,0]
	s_nop 0
	v_pk_fma_f32 v[136:137], v[154:155], v[142:143], v[136:137] op_sel:[1,1,0] op_sel_hi:[1,0,1]
	s_nop 0
	v_pk_mul_f32 v[144:145], v[136:137], s[28:29]
	v_pk_mul_f32 v[136:137], v[136:137], v[138:139] op_sel_hi:[1,0]
	s_nop 0
	v_pk_fma_f32 v[136:137], v[138:139], v[144:145], v[136:137] op_sel:[1,1,0] op_sel_hi:[1,0,1]
	v_pk_mul_f32 v[138:139], v[162:163], v[158:159] op_sel_hi:[1,0]
	s_nop 0
	v_pk_fma_f32 v[138:139], v[158:159], v[142:143], v[138:139] op_sel:[1,1,0] op_sel_hi:[1,0,1]
	s_nop 0
	v_pk_mul_f32 v[142:143], v[138:139], s[28:29]
	s_waitcnt lgkmcnt(0)
	v_pk_mul_f32 v[138:139], v[138:139], v[140:141] op_sel_hi:[1,0]
	s_nop 0
	v_pk_fma_f32 v[138:139], v[140:141], v[142:143], v[138:139] op_sel:[1,1,0] op_sel_hi:[1,0,1]
	v_pk_add_f32 v[140:141], v[70:71], v[126:127]
	v_pk_add_f32 v[70:71], v[70:71], v[126:127] neg_lo:[0,1] neg_hi:[0,1]
	v_pk_add_f32 v[126:127], v[118:119], v[132:133]
	v_pk_add_f32 v[118:119], v[118:119], v[132:133] neg_lo:[0,1] neg_hi:[0,1]
	v_pk_add_f32 v[132:133], v[140:141], v[126:127]
	v_pk_add_f32 v[126:127], v[140:141], v[126:127] neg_lo:[0,1] neg_hi:[0,1]
	v_pk_fma_f32 v[140:141], v[118:119], s[26:27], v[70:71] op_sel:[1,0,0] op_sel_hi:[0,1,1]
	v_pk_fma_f32 v[70:71], v[118:119], s[28:29], v[70:71] op_sel:[1,0,0] op_sel_hi:[0,1,1]
	v_pk_add_f32 v[118:119], v[66:67], v[80:81]
	v_pk_add_f32 v[66:67], v[66:67], v[80:81] neg_lo:[0,1] neg_hi:[0,1]
	v_pk_add_f32 v[80:81], v[120:121], v[134:135]
	v_pk_add_f32 v[120:121], v[120:121], v[134:135] neg_lo:[0,1] neg_hi:[0,1]
	v_pk_add_f32 v[134:135], v[118:119], v[80:81]
	v_pk_add_f32 v[80:81], v[118:119], v[80:81] neg_lo:[0,1] neg_hi:[0,1]
	v_pk_fma_f32 v[118:119], v[120:121], s[26:27], v[66:67] op_sel:[1,0,0] op_sel_hi:[0,1,1]
	v_pk_fma_f32 v[66:67], v[120:121], s[28:29], v[66:67] op_sel:[1,0,0] op_sel_hi:[0,1,1]
	v_pk_add_f32 v[120:121], v[68:69], v[128:129]
	v_pk_add_f32 v[68:69], v[68:69], v[128:129] neg_lo:[0,1] neg_hi:[0,1]
	v_pk_add_f32 v[128:129], v[122:123], v[136:137]
	v_pk_add_f32 v[122:123], v[122:123], v[136:137] neg_lo:[0,1] neg_hi:[0,1]
	v_pk_add_f32 v[136:137], v[120:121], v[128:129]
	v_pk_add_f32 v[120:121], v[120:121], v[128:129] neg_lo:[0,1] neg_hi:[0,1]
	v_pk_fma_f32 v[128:129], v[122:123], s[26:27], v[68:69] op_sel:[1,0,0] op_sel_hi:[0,1,1]
	v_pk_fma_f32 v[68:69], v[122:123], s[28:29], v[68:69] op_sel:[1,0,0] op_sel_hi:[0,1,1]
	v_pk_add_f32 v[122:123], v[116:117], v[130:131]
	v_pk_add_f32 v[116:117], v[116:117], v[130:131] neg_lo:[0,1] neg_hi:[0,1]
	v_pk_add_f32 v[130:131], v[124:125], v[138:139]
	v_pk_add_f32 v[124:125], v[124:125], v[138:139] neg_lo:[0,1] neg_hi:[0,1]
	v_pk_add_f32 v[138:139], v[122:123], v[130:131]
	v_pk_add_f32 v[122:123], v[122:123], v[130:131] neg_lo:[0,1] neg_hi:[0,1]
	v_pk_fma_f32 v[130:131], v[124:125], s[26:27], v[116:117] op_sel:[1,0,0] op_sel_hi:[0,1,1]
	v_pk_fma_f32 v[116:117], v[124:125], s[28:29], v[116:117] op_sel:[1,0,0] op_sel_hi:[0,1,1]
	v_pk_mul_f32 v[124:125], v[118:119], s[34:35] op_sel_hi:[0,1]
	v_mul_f32_e32 v86, 0x3f3504f3, v128
	v_pk_fma_f32 v[118:119], v[118:119], s[30:31], v[124:125] op_sel:[1,0,0]
	v_pk_fma_f32 v[124:125], v[128:129], s[36:37], v[86:87] op_sel:[1,0,0] op_sel_hi:[1,1,0]
	v_pk_mul_f32 v[128:129], v[130:131], s[6:7] op_sel_hi:[0,1]
	v_pk_fma_f32 v[128:129], v[130:131], s[38:39], v[128:129] op_sel:[1,0,0]
	v_pk_mul_f32 v[130:131], v[120:121], s[18:19] op_sel_hi:[0,1]
	v_pk_fma_f32 v[120:121], v[120:121], s[8:9], v[130:131] op_sel:[1,0,0]
	v_pk_mul_f32 v[130:131], v[122:123], s[36:37] op_sel_hi:[0,1]
	v_pk_fma_f32 v[122:123], v[122:123], s[36:37], v[130:131] op_sel:[1,0,0] op_sel_hi:[1,0,1]
	v_pk_mul_f32 v[130:131], v[66:67], s[6:7] op_sel_hi:[0,1]
	v_pk_fma_f32 v[66:67], v[66:67], s[38:39], v[130:131] op_sel:[1,0,0]
	v_pk_mul_f32 v[130:131], v[68:69], s[36:37] op_sel_hi:[0,1]
	s_mov_b32 s39, s30
	v_pk_fma_f32 v[68:69], v[68:69], s[36:37], v[130:131] op_sel:[1,0,0] op_sel_hi:[1,0,1]
	v_pk_mul_f32 v[130:131], v[116:117], s[38:39] op_sel_hi:[0,1]
	s_mov_b32 s7, s38
	s_add_i32 s19, s62, -1
	v_pk_fma_f32 v[116:117], v[116:117], s[6:7], v[130:131] op_sel:[1,0,0]
	s_min_i32 s6, s19, s59
	s_mul_i32 s6, s6, s3
	s_add_i32 s6, s6, s2
	s_mul_hi_i32 s7, s6, 0x2aaaaaab
	s_lshr_b32 s8, s7, 31
	s_lshr_b32 s7, s7, 7
	s_add_i32 s7, s7, s8
	v_mul_f32_e32 v86, 0x3f3504f3, v80
	v_pk_add_f32 v[130:131], v[132:133], v[136:137]
	v_pk_add_f32 v[132:133], v[132:133], v[136:137] neg_lo:[0,1] neg_hi:[0,1]
	v_pk_add_f32 v[136:137], v[134:135], v[138:139]
	v_pk_add_f32 v[134:135], v[134:135], v[138:139] neg_lo:[0,1] neg_hi:[0,1]
	s_mulk_i32 s7, 0x300
	v_pk_fma_f32 v[80:81], v[80:81], s[36:37], v[86:87] op_sel:[1,0,0] op_sel_hi:[1,1,0]
	v_pk_add_f32 v[138:139], v[130:131], v[136:137]
	v_pk_add_f32 v[130:131], v[130:131], v[136:137] neg_lo:[0,1] neg_hi:[0,1]
	v_pk_fma_f32 v[136:137], v[134:135], s[26:27], v[132:133] op_sel:[1,0,0] op_sel_hi:[0,1,1]
	v_pk_fma_f32 v[132:133], v[134:135], s[28:29], v[132:133] op_sel:[1,0,0] op_sel_hi:[0,1,1]
	v_pk_add_f32 v[134:135], v[140:141], v[124:125]
	v_pk_add_f32 v[124:125], v[140:141], v[124:125] neg_lo:[0,1] neg_hi:[0,1]
	v_pk_add_f32 v[140:141], v[118:119], v[128:129]
	v_pk_add_f32 v[118:119], v[118:119], v[128:129] neg_lo:[0,1] neg_hi:[0,1]
	s_sub_i32 s6, s6, s7
	v_pk_add_f32 v[128:129], v[134:135], v[140:141]
	v_pk_add_f32 v[134:135], v[134:135], v[140:141] neg_lo:[0,1] neg_hi:[0,1]
	v_pk_fma_f32 v[140:141], v[118:119], s[26:27], v[124:125] op_sel:[1,0,0] op_sel_hi:[0,1,1]
	v_pk_fma_f32 v[118:119], v[118:119], s[28:29], v[124:125] op_sel:[1,0,0] op_sel_hi:[0,1,1]
	v_pk_add_f32 v[124:125], v[126:127], v[120:121]
	v_pk_add_f32 v[120:121], v[126:127], v[120:121] neg_lo:[0,1] neg_hi:[0,1]
	v_pk_add_f32 v[126:127], v[80:81], v[122:123]
	v_pk_add_f32 v[80:81], v[80:81], v[122:123] neg_lo:[0,1] neg_hi:[0,1]
	s_cmpk_lt_i32 s6, 0x200
	v_pk_add_f32 v[122:123], v[124:125], v[126:127]
	v_pk_add_f32 v[124:125], v[124:125], v[126:127] neg_lo:[0,1] neg_hi:[0,1]
	v_pk_fma_f32 v[126:127], v[80:81], s[26:27], v[120:121] op_sel:[1,0,0] op_sel_hi:[0,1,1]
	v_pk_fma_f32 v[80:81], v[80:81], s[28:29], v[120:121] op_sel:[1,0,0] op_sel_hi:[0,1,1]
	v_pk_add_f32 v[120:121], v[70:71], v[68:69]
	v_pk_add_f32 v[68:69], v[70:71], v[68:69] neg_lo:[0,1] neg_hi:[0,1]
	v_pk_add_f32 v[70:71], v[66:67], v[116:117]
	v_pk_add_f32 v[66:67], v[66:67], v[116:117] neg_lo:[0,1] neg_hi:[0,1]
	s_cselect_b64 vcc, -1, 0
	v_pk_add_f32 v[116:117], v[120:121], v[70:71]
	v_pk_add_f32 v[70:71], v[120:121], v[70:71] neg_lo:[0,1] neg_hi:[0,1]
	v_pk_fma_f32 v[120:121], v[66:67], s[26:27], v[68:69] op_sel:[1,0,0] op_sel_hi:[0,1,1]
	v_pk_fma_f32 v[66:67], v[66:67], s[28:29], v[68:69] op_sel:[1,0,0] op_sel_hi:[0,1,1]
	ds_write_b64 v166, v[138:139]
	ds_write2_b64 v65, v[128:129], v[122:123] offset0:17 offset1:34
	ds_write2_b64 v65, v[116:117], v[136:137] offset0:51 offset1:68
	ds_write2_b64 v65, v[140:141], v[126:127] offset0:85 offset1:102
	ds_write2_b64 v65, v[120:121], v[130:131] offset0:119 offset1:136
	ds_write2_b64 v65, v[134:135], v[124:125] offset0:153 offset1:170
	ds_write2_b64 v65, v[70:71], v[132:133] offset0:187 offset1:204
	ds_write2_b64 v65, v[118:119], v[80:81] offset0:221 offset1:238
	ds_write_b64 v65, v[66:67] offset:2040
	v_cndmask_b32_e32 v65, v211, v212, vcc
	v_mul_f32_e32 v20, v65, v20
	v_mul_f32_e32 v66, v65, v16
	v_mov_b32_e32 v16, v87
	v_cvt_pk_fp8_f32 v16, v20, v66
	v_mul_f32_e32 v20, v65, v21
	v_mul_f32_e32 v21, v65, v17
	v_mov_b32_e32 v17, v87
	v_cvt_pk_fp8_f32 v17, v20, v21
	v_mul_f32_e32 v20, v65, v37
	v_mul_f32_e32 v21, v65, v33
	v_mul_f32_e32 v12, v65, v12
	v_cvt_pk_fp8_f32 v17, v20, v21 op_sel:[0,0,1]
	v_mul_f32_e32 v20, v65, v22
	v_mul_f32_e32 v21, v65, v18
	v_mov_b32_e32 v18, v87
	v_cvt_pk_fp8_f32 v18, v20, v21
	v_mul_f32_e32 v20, v65, v23
	v_mul_f32_e32 v21, v65, v19
	v_mov_b32_e32 v19, v87
	v_cvt_pk_fp8_f32 v19, v20, v21
	v_mul_f32_e32 v20, v65, v39
	v_mul_f32_e32 v21, v65, v35
	s_min_i32 s6, s76, s59
	v_cvt_pk_fp8_f32 v19, v20, v21 op_sel:[0,0,1]
	v_mul_f32_e32 v20, v65, v8
	v_mov_b32_e32 v8, v87
	v_cvt_pk_fp8_f32 v8, v12, v20
	v_mul_f32_e32 v12, v65, v13
	v_mul_f32_e32 v13, v65, v9
	v_mov_b32_e32 v9, v87
	v_cvt_pk_fp8_f32 v9, v12, v13
	v_mul_f32_e32 v12, v65, v29
	v_mul_f32_e32 v13, v65, v25
	s_mul_i32 s6, s6, s3
	v_cvt_pk_fp8_f32 v9, v12, v13 op_sel:[0,0,1]
	v_mul_f32_e32 v12, v65, v14
	v_mul_f32_e32 v13, v65, v10
	v_mov_b32_e32 v10, v87
	v_cvt_pk_fp8_f32 v10, v12, v13
	v_mul_f32_e32 v12, v65, v15
	v_mul_f32_e32 v13, v65, v11
	v_mov_b32_e32 v11, v87
	v_cvt_pk_fp8_f32 v11, v12, v13
	s_add_i32 s7, s6, s2
	v_mul_f32_e32 v36, v65, v36
	v_mul_f32_e32 v32, v65, v32
	s_mul_hi_i32 s6, s7, 0x2aaaaaab
	v_cvt_pk_fp8_f32 v16, v36, v32 op_sel:[0,0,1]
	v_mul_f32_e32 v22, v65, v38
	v_mul_f32_e32 v32, v65, v34
	s_lshr_b32 s8, s6, 31
	s_ashr_i32 s6, s6, 7
	v_cvt_pk_fp8_f32 v18, v22, v32 op_sel:[0,0,1]
	v_mul_f32_e32 v21, v65, v28
	v_mul_f32_e32 v22, v65, v24
	v_mul_f32_e32 v14, v65, v30
	v_mul_f32_e32 v20, v65, v26
	v_mul_f32_e32 v12, v65, v31
	v_mul_f32_e32 v13, v65, v27
	s_add_i32 s8, s6, s8
	v_cvt_pk_fp8_f32 v8, v21, v22 op_sel:[0,0,1]
	v_cvt_pk_fp8_f32 v10, v14, v20 op_sel:[0,0,1]
	v_cvt_pk_fp8_f32 v11, v12, v13 op_sel:[0,0,1]
	s_add_i32 s6, s8, 18
	s_mulk_i32 s8, 0x300
	s_sub_i32 s31, s7, s8
	s_cmpk_lt_i32 s31, 0x200
	s_cselect_b64 s[8:9], -1, 0
	s_cmpk_gt_i32 s31, 0x1ff
	s_waitcnt lgkmcnt(0)
	s_barrier
	ds_write_b128 v240, v[16:19]
	ds_write_b128 v241, v[8:11]
	s_cbranch_scc0 .LBB0_815
	s_load_dwordx2 s[12:13], s[14:15], 0x110
	s_ashr_i32 s7, s6, 31
	s_lshl_b64 s[52:53], s[6:7], 24
	s_mov_b32 s51, s18
	s_waitcnt lgkmcnt(0)
	s_add_u32 s12, s12, s52
	s_addc_u32 s13, s13, s53
	s_lshl_b32 s7, s31, 3
	s_and_b32 s7, s7, 0x7fffffc0
	s_add_i32 s50, s7, 0xfffff000
	s_mov_b64 s[52:53], 0

.LBB0_817:
	s_lshl_b64 s[50:51], s[50:51], 13
	s_add_u32 s6, s12, s50
	s_addc_u32 s12, s13, s51
	s_lshl_b32 s7, s31, s7
	s_and_b32 s7, s7, 0x700
	s_lshl_b32 s7, s7, 2
	s_add_u32 s6, s6, s7
	s_addc_u32 s7, s12, 0
	s_cmp_ge_i32 s62, s59
	s_cselect_b64 s[54:55], -1, 0
	v_cndmask_b32_e64 v8, v180, 0, s[54:55]
	s_and_b64 s[12:13], s[54:55], exec
	s_cselect_b32 s12, 0, 0x800
	v_lshlrev_b32_e32 v86, 2, v8
	v_lshl_add_u64 v[8:9], s[6:7], 0, v[86:87]
	v_mad_i64_i32 v[10:11], s[6:7], s12, v181, 0
	v_mad_i64_i32 v[12:13], s[6:7], s12, v182, 0
	v_lshl_add_u64 v[10:11], v[10:11], 2, v[8:9]
	v_lshl_add_u64 v[12:13], v[12:13], 2, v[8:9]
	global_load_dwordx4 v[32:35], v[10:11], off nt
	global_load_dwordx4 v[36:39], v[12:13], off nt
	v_mad_i64_i32 v[10:11], s[6:7], s12, v183, 0
	v_mad_i64_i32 v[12:13], s[6:7], s12, v184, 0
	v_lshl_add_u64 v[10:11], v[10:11], 2, v[8:9]
	v_lshl_add_u64 v[12:13], v[12:13], 2, v[8:9]
	global_load_dwordx4 v[24:27], v[10:11], off nt
	global_load_dwordx4 v[28:31], v[12:13], off nt
	v_mad_i64_i32 v[10:11], s[6:7], s12, v185, 0
	v_mad_i64_i32 v[12:13], s[6:7], s12, v186, 0
	v_lshl_add_u64 v[10:11], v[10:11], 2, v[8:9]
	v_lshl_add_u64 v[12:13], v[12:13], 2, v[8:9]
	global_load_dwordx4 v[16:19], v[10:11], off nt
	global_load_dwordx4 v[20:23], v[12:13], off nt
	v_mad_i64_i32 v[10:11], s[6:7], s12, v187, 0
	v_mad_i64_i32 v[12:13], s[6:7], s12, v188, 0
	v_lshl_add_u64 v[10:11], v[10:11], 2, v[8:9]
	v_lshl_add_u64 v[12:13], v[12:13], 2, v[8:9]
	global_load_dwordx4 v[8:11], v[10:11], off nt
	s_nop 0
	global_load_dwordx4 v[12:15], v[12:13], off nt
	s_cmp_gt_i32 s62, 1
	s_cselect_b32 s6, s56, 0
	s_min_i32 s6, s6, s59
	s_mul_i32 s6, s6, s3
	s_add_i32 s7, s6, s2
	s_mul_hi_i32 s6, s7, 0x2aaaaaab
	s_lshr_b32 s12, s6, 31
	s_ashr_i32 s6, s6, 7
	s_add_i32 s12, s6, s12
	s_add_i32 s6, s12, 18
	s_mulk_i32 s12, 0x300
	s_sub_i32 s31, s7, s12
	s_ashr_i32 s7, s6, 31
	s_cmpk_gt_i32 s31, 0x1ff
	s_mov_b64 s[50:51], -1
	s_cbranch_scc0 .LBB0_819
	s_lshl_b32 s12, s31, 3
	s_and_b32 s33, s12, 0x7fffffc0
	s_lshl_b32 s12, s31, 19
	s_and_b32 s39, s12, 0x380000
	s_lshl_b64 s[12:13], s[6:7], 22
	s_add_u32 s12, s16, s12
	s_addc_u32 s13, s17, s13
	s_add_u32 s12, s12, s39
	s_addc_u32 s13, s13, 0
	s_add_u32 s12, s12, s33
	s_addc_u32 s13, s13, 0
	s_add_u32 s12, s12, 0x24dff000
	s_addc_u32 s13, s13, 0
	s_mov_b64 s[50:51], 0

.LBB0_821:
	s_add_i32 s33, s62, 2
	s_cmp_lt_i32 s62, 2
	s_cselect_b64 s[6:7], -1, 0
	s_cmp_gt_i32 s56, s59
	s_cselect_b64 s[50:51], -1, 0
	s_or_b64 s[6:7], s[6:7], s[50:51]
	s_and_b64 s[6:7], s[6:7], exec
	s_cselect_b32 s6, s65, s12
	s_cselect_b32 s12, 0x80, s39
	v_mul_i32_i24_e32 v65, s12, v191
	v_or_b32_e32 v66, v65, v189
	v_ashrrev_i32_e32 v67, 31, v66
	s_cselect_b32 s7, s66, s13
	v_lshlrev_b64 v[66:67], 11, v[66:67]
	v_add_u32_e32 v239, v203, v190
	v_lshl_add_u64 v[66:67], s[6:7], 0, v[66:67]
	v_lshl_add_u64 v[70:71], v[66:67], 0, v[88:89]
	v_add_u32_e32 v242, v203, v200
	ds_read_b32 v66, v239
	ds_read_b32 v67, v239 offset:1040
	ds_read_b32 v68, v239 offset:2080
	ds_read_b32 v69, v239 offset:3120
	ds_read_b32 v116, v242
	ds_read_b32 v117, v242 offset:1040
	ds_read_b32 v118, v242 offset:2080
	ds_read_b32 v119, v242 offset:3120
	v_mul_i32_i24_e32 v65, s12, v201
	s_waitcnt lgkmcnt(4)
	global_store_dwordx4 v[70:71], v[66:69], off
	v_lshlrev_b32_e32 v64, 3, v64
	v_add3_u32 v64, v219, v64, v83
	v_or_b32_e32 v66, v65, v189
	v_ashrrev_i32_e32 v67, 31, v66
	v_lshlrev_b64 v[66:67], 11, v[66:67]
	v_lshl_add_u64 v[66:67], s[6:7], 0, v[66:67]
	v_lshl_add_u64 v[66:67], v[66:67], 0, v[88:89]
	s_waitcnt lgkmcnt(0)
	global_store_dwordx4 v[66:67], v[116:119], off
	v_add_u32_e32 v65, 0x100, v82
	v_add_u32_e32 v66, 0x200, v82
	v_add_u32_e32 v67, 0x300, v82
	v_ashrrev_i32_e32 v65, 4, v65
	v_ashrrev_i32_e32 v66, 4, v66
	v_ashrrev_i32_e32 v67, 4, v67
	v_lshlrev_b32_e32 v65, 3, v65
	v_lshlrev_b32_e32 v66, 3, v66
	v_lshlrev_b32_e32 v67, 3, v67
	v_add3_u32 v65, v219, v65, v83
	v_add3_u32 v66, v219, v66, v83
	v_add3_u32 v67, v219, v67, v83
	ds_read_b64 v[116:117], v64
	ds_read_b64 v[130:131], v65 offset:2048
	ds_read_b64 v[122:123], v66 offset:4096
	ds_read_b64 v[132:133], v67 offset:6144
	v_add_u32_e32 v64, 0x400, v82
	v_ashrrev_i32_e32 v64, 4, v64
	v_add_u32_e32 v65, 0x500, v82
	v_add_u32_e32 v66, 0x600, v82
	v_add_u32_e32 v67, 0x700, v82
	v_lshlrev_b32_e32 v64, 3, v64
	v_ashrrev_i32_e32 v65, 4, v65
	v_ashrrev_i32_e32 v66, 4, v66
	v_ashrrev_i32_e32 v67, 4, v67
	v_add3_u32 v64, v219, v64, v83
	v_lshlrev_b32_e32 v65, 3, v65
	v_lshlrev_b32_e32 v66, 3, v66
	v_lshlrev_b32_e32 v67, 3, v67
	v_add3_u32 v65, v219, v65, v83
	v_add3_u32 v66, v219, v66, v83
	v_add3_u32 v67, v219, v67, v83
	ds_read_b64 v[118:119], v64 offset:8192
	ds_read_b64 v[138:139], v65 offset:10240
	ds_read_b64 v[126:127], v66 offset:12288
	ds_read_b64 v[136:137], v67 offset:14336
	v_add_u32_e32 v64, 0x800, v82
	v_ashrrev_i32_e32 v64, 4, v64
	v_add_u32_e32 v65, 0x900, v82
	v_add_u32_e32 v66, 0xa00, v82
	v_add_u32_e32 v67, 0xb00, v82
	v_lshlrev_b32_e32 v64, 3, v64
	v_ashrrev_i32_e32 v65, 4, v65
	v_ashrrev_i32_e32 v66, 4, v66
	v_ashrrev_i32_e32 v67, 4, v67
	v_add3_u32 v64, v219, v64, v83
	v_lshlrev_b32_e32 v65, 3, v65
	v_lshlrev_b32_e32 v66, 3, v66
	v_lshlrev_b32_e32 v67, 3, v67
	v_add3_u32 v65, v219, v65, v83
	v_add3_u32 v66, v219, v66, v83
	v_add3_u32 v67, v219, v67, v83
	ds_read_b64 v[120:121], v64 offset:16384
	ds_read_b64 v[142:143], v65 offset:18432
	ds_read_b64 v[128:129], v66 offset:20480
	ds_read_b64 v[140:141], v67 offset:22528
	v_add_u32_e32 v64, 0xc00, v82
	v_ashrrev_i32_e32 v64, 4, v64
	v_add_u32_e32 v65, 0xd00, v82
	v_add_u32_e32 v66, 0xe00, v82
	v_add_u32_e32 v67, 0xf00, v82
	v_lshlrev_b32_e32 v64, 3, v64
	v_ashrrev_i32_e32 v65, 4, v65
	v_ashrrev_i32_e32 v66, 4, v66
	v_ashrrev_i32_e32 v67, 4, v67
	v_add3_u32 v64, v219, v64, v83
	v_lshlrev_b32_e32 v65, 3, v65
	v_lshlrev_b32_e32 v66, 3, v66
	v_lshlrev_b32_e32 v67, 3, v67
	v_add3_u32 v65, v219, v65, v83
	v_add3_u32 v66, v219, v66, v83
	v_add3_u32 v67, v219, v67, v83
	ds_read_b64 v[124:125], v64 offset:24576
	ds_read_b64 v[146:147], v65 offset:26624
	ds_read_b64 v[134:135], v66 offset:28672
	ds_read_b64 v[144:145], v67 offset:30720
	v_cndmask_b32_e64 v64, v211, v212, s[4:5]
	s_waitcnt vmcnt(19)
	v_mul_f32_e32 v65, v64, v48
	s_waitcnt vmcnt(18)
	v_mul_f32_e32 v52, v64, v52
	v_mov_b32_e32 v48, v87
	v_cvt_pk_fp8_f32 v48, v65, v52
	v_mul_f32_e32 v52, v64, v49
	v_mul_f32_e32 v53, v64, v53
	v_mov_b32_e32 v49, v87
	v_cvt_pk_fp8_f32 v49, v52, v53
	s_waitcnt vmcnt(17)
	v_mul_f32_e32 v52, v64, v57
	s_waitcnt vmcnt(16)
	v_mul_f32_e32 v53, v64, v61
	s_waitcnt vmcnt(14)
	v_mul_f32_e32 v4, v64, v4
	v_cvt_pk_fp8_f32 v49, v52, v53 op_sel:[0,0,1]
	v_mul_f32_e32 v52, v64, v50
	v_mul_f32_e32 v53, v64, v54
	v_mov_b32_e32 v50, v87
	v_cvt_pk_fp8_f32 v50, v52, v53
	v_mul_f32_e32 v52, v64, v51
	v_mul_f32_e32 v53, v64, v55
	v_mov_b32_e32 v51, v87
	v_cvt_pk_fp8_f32 v51, v52, v53
	v_mul_f32_e32 v52, v64, v59
	v_mul_f32_e32 v53, v64, v63
	v_mul_f32_e32 v5, v64, v5
	v_cvt_pk_fp8_f32 v51, v52, v53 op_sel:[0,0,1]
	v_mul_f32_e32 v52, v64, v0
	v_mov_b32_e32 v0, v87
	v_cvt_pk_fp8_f32 v0, v52, v4
	v_mul_f32_e32 v4, v64, v1
	v_mov_b32_e32 v1, v87
	v_cvt_pk_fp8_f32 v1, v4, v5
	s_waitcnt vmcnt(13)
	v_mul_f32_e32 v4, v64, v41
	s_waitcnt vmcnt(12)
	v_mul_f32_e32 v5, v64, v45
	s_min_i32 s4, s33, s59
	v_cvt_pk_fp8_f32 v1, v4, v5 op_sel:[0,0,1]
	v_mul_f32_e32 v4, v64, v2
	v_mul_f32_e32 v5, v64, v6
	v_mov_b32_e32 v2, v87
	s_mul_i32 s4, s4, s3
	v_cvt_pk_fp8_f32 v2, v4, v5
	v_mul_f32_e32 v4, v64, v3
	v_mul_f32_e32 v5, v64, v7
	v_mov_b32_e32 v3, v87
	s_add_i32 s5, s4, s2
	v_cvt_pk_fp8_f32 v3, v4, v5
	s_mul_hi_i32 s4, s5, 0x2aaaaaab
	v_mul_f32_e32 v56, v64, v56
	v_mul_f32_e32 v60, v64, v60
	s_lshr_b32 s6, s4, 31
	s_ashr_i32 s4, s4, 7
	v_cvt_pk_fp8_f32 v48, v56, v60 op_sel:[0,0,1]
	v_mul_f32_e32 v54, v64, v58
	v_mul_f32_e32 v56, v64, v62
	v_mul_f32_e32 v40, v64, v40
	v_mul_f32_e32 v44, v64, v44
	s_add_i32 s6, s4, s6
	v_cvt_pk_fp8_f32 v50, v54, v56 op_sel:[0,0,1]
	v_cvt_pk_fp8_f32 v0, v40, v44 op_sel:[0,0,1]
	v_mul_f32_e32 v6, v64, v42
	v_mul_f32_e32 v40, v64, v46
	v_mul_f32_e32 v4, v64, v43
	v_mul_f32_e32 v5, v64, v47
	s_add_i32 s4, s6, 18
	s_mulk_i32 s6, 0x300
	v_cvt_pk_fp8_f32 v2, v6, v40 op_sel:[0,0,1]
	v_cvt_pk_fp8_f32 v3, v4, v5 op_sel:[0,0,1]
	s_sub_i32 s31, s5, s6
	s_cmpk_lt_i32 s31, 0x200
	s_cselect_b64 s[6:7], -1, 0
	s_cmpk_gt_i32 s31, 0x1ff
	s_mov_b64 s[52:53], -1
	s_waitcnt lgkmcnt(0)
	s_barrier
	ds_write_b128 v236, v[48:51]
	ds_write_b128 v237, v[0:3]
	s_cbranch_scc0 .LBB0_823
	s_load_dwordx2 s[12:13], s[14:15], 0x110
	s_ashr_i32 s5, s4, 31
	s_lshl_b64 s[52:53], s[4:5], 24
	s_mov_b32 s51, s18
	s_waitcnt lgkmcnt(0)
	s_add_u32 s12, s12, s52
	s_addc_u32 s13, s13, s53
	s_lshl_b32 s5, s31, 3
	s_and_b32 s5, s5, 0x7fffffc0
	s_add_i32 s50, s5, 0xfffff000
	s_mov_b64 s[52:53], 0

.LBB0_825:
	s_lshl_b64 s[50:51], s[50:51], 13
	s_add_u32 s4, s12, s50
	s_addc_u32 s12, s13, s51
	s_lshl_b32 s5, s31, s5
	s_and_b32 s5, s5, 0x700
	s_lshl_b32 s5, s5, 2
	s_add_u32 s4, s4, s5
	s_addc_u32 s5, s12, 0
	s_add_i32 s56, s56, 4
	s_cmp_gt_i32 s56, s59
	s_cselect_b64 s[50:51], -1, 0
	v_cndmask_b32_e64 v0, v180, 0, s[50:51]
	s_and_b64 s[12:13], s[50:51], exec
	s_cselect_b32 s12, 0, 0x800
	v_lshlrev_b32_e32 v86, 2, v0
	v_lshl_add_u64 v[0:1], s[4:5], 0, v[86:87]
	v_mad_i64_i32 v[2:3], s[4:5], s12, v181, 0
	v_lshl_add_u64 v[2:3], v[2:3], 2, v[0:1]
	v_mad_i64_i32 v[4:5], s[4:5], s12, v182, 0
	v_lshl_add_u64 v[4:5], v[4:5], 2, v[0:1]
	global_load_dwordx4 v[56:59], v[2:3], off nt
	global_load_dwordx4 v[60:63], v[4:5], off nt
	v_mad_i64_i32 v[2:3], s[4:5], s12, v183, 0
	v_lshl_add_u64 v[2:3], v[2:3], 2, v[0:1]
	v_mad_i64_i32 v[4:5], s[4:5], s12, v184, 0
	v_lshl_add_u64 v[4:5], v[4:5], 2, v[0:1]
	global_load_dwordx4 v[64:67], v[2:3], off nt
	global_load_dwordx4 v[68:71], v[4:5], off nt
	v_mad_i64_i32 v[2:3], s[4:5], s12, v185, 0
	v_lshl_add_u64 v[2:3], v[2:3], 2, v[0:1]
	v_mad_i64_i32 v[4:5], s[4:5], s12, v186, 0
	v_lshl_add_u64 v[4:5], v[4:5], 2, v[0:1]
	global_load_dwordx4 v[40:43], v[2:3], off nt
	global_load_dwordx4 v[44:47], v[4:5], off nt
	v_mad_i64_i32 v[2:3], s[4:5], s12, v187, 0
	v_lshl_add_u64 v[2:3], v[2:3], 2, v[0:1]
	v_mad_i64_i32 v[4:5], s[4:5], s12, v188, 0
	v_lshl_add_u64 v[0:1], v[4:5], 2, v[0:1]
	global_load_dwordx4 v[48:51], v[2:3], off nt
	global_load_dwordx4 v[52:55], v[0:1], off nt
	s_cmp_gt_i32 s62, 0
	s_cselect_b32 s4, s19, 0
	s_min_i32 s4, s4, s59
	s_mul_i32 s4, s4, s3
	s_add_i32 s5, s4, s2
	s_mul_hi_i32 s4, s5, 0x2aaaaaab
	s_lshr_b32 s12, s4, 31
	s_ashr_i32 s4, s4, 7
	s_add_i32 s12, s4, s12
	s_add_i32 s4, s12, 18
	s_mulk_i32 s12, 0x300
	s_sub_i32 s31, s5, s12
	s_ashr_i32 s5, s4, 31
	s_cmpk_gt_i32 s31, 0x1ff
	s_mov_b64 s[52:53], -1
	s_cbranch_scc0 .LBB0_827
	s_lshl_b32 s12, s31, 3
	s_and_b32 s39, s12, 0x7fffffc0
	s_lshl_b32 s12, s31, 19
	s_and_b32 s52, s12, 0x380000
	s_lshl_b64 s[12:13], s[4:5], 22
	s_add_u32 s12, s16, s12
	s_addc_u32 s13, s17, s13
	s_add_u32 s12, s12, s52
	s_addc_u32 s13, s13, 0
	s_add_u32 s12, s12, s39
	s_addc_u32 s13, s13, 0
	s_add_u32 s12, s12, 0x24dff000
	s_addc_u32 s13, s13, 0
	s_mov_b64 s[52:53], 0

.LBB0_829:
	s_add_i32 s77, s62, 3
	s_cmp_lt_i32 s62, 1
	s_cselect_b64 s[4:5], -1, 0
	s_cmp_gt_i32 s19, s59
	s_cselect_b64 s[52:53], -1, 0
	s_or_b64 s[4:5], s[4:5], s[52:53]
	s_and_b64 s[4:5], s[4:5], exec
	s_cselect_b32 s4, s65, s12
	s_cselect_b32 s12, 0x80, s39
	v_mul_i32_i24_e32 v0, s12, v191
	v_or_b32_e32 v0, v0, v189
	v_ashrrev_i32_e32 v1, 31, v0
	s_cselect_b32 s5, s66, s13
	v_lshlrev_b64 v[0:1], 11, v[0:1]
	v_lshl_add_u64 v[0:1], s[4:5], 0, v[0:1]
	v_lshl_add_u64 v[80:81], v[0:1], 0, v[88:89]
	ds_read_b32 v0, v235
	ds_read_b32 v1, v235 offset:1040
	ds_read_b32 v2, v235 offset:2080
	ds_read_b32 v3, v235 offset:3120
	ds_read_b32 v4, v238
	ds_read_b32 v5, v238 offset:1040
	ds_read_b32 v6, v238 offset:2080
	ds_read_b32 v7, v238 offset:3120
	s_waitcnt lgkmcnt(4)
	global_store_dwordx4 v[80:81], v[0:3], off
	s_mov_b64 s[56:57], -1
	s_nop 0
	v_mul_i32_i24_e32 v0, s12, v201
	v_or_b32_e32 v0, v0, v189
	v_ashrrev_i32_e32 v1, 31, v0
	v_lshlrev_b64 v[0:1], 11, v[0:1]
	v_lshl_add_u64 v[0:1], s[4:5], 0, v[0:1]
	v_lshl_add_u64 v[0:1], v[0:1], 0, v[88:89]
	s_mov_b32 s4, 0x45700000
	s_waitcnt lgkmcnt(0)
	global_store_dwordx4 v[0:1], v[4:7], off
	v_add_co_u32_e32 v0, vcc, s4, v84
	s_mov_b32 s4, 0x46300000
	s_nop 0
	v_addc_co_u32_e32 v1, vcc, 0, v85, vcc
	v_add_co_u32_e32 v4, vcc, s4, v84
	s_min_i32 s4, s77, s59
	s_nop 0
	v_addc_co_u32_e32 v5, vcc, 0, v85, vcc
	global_load_dwordx4 v[0:3], v[0:1], off
	s_nop 0
	global_load_dwordx4 v[4:7], v[4:5], off
	ds_write_b128 v234, v[72:75]
	ds_write_b128 v234, v[76:79] offset:4096
	v_cndmask_b32_e64 v72, v211, v212, s[8:9]
	s_waitcnt vmcnt(21)
	v_mul_f32_e32 v73, v72, v32
	s_waitcnt vmcnt(20)
	v_mul_f32_e32 v36, v72, v36
	v_mov_b32_e32 v32, v87
	v_cvt_pk_fp8_f32 v32, v73, v36
	v_mul_f32_e32 v36, v72, v33
	v_mul_f32_e32 v37, v72, v37
	v_mov_b32_e32 v33, v87
	v_cvt_pk_fp8_f32 v33, v36, v37
	s_waitcnt vmcnt(19)
	v_mul_f32_e32 v24, v72, v24
	s_waitcnt vmcnt(18)
	v_mul_f32_e32 v28, v72, v28
	v_cvt_pk_fp8_f32 v32, v24, v28 op_sel:[0,0,1]
	v_mul_f32_e32 v24, v72, v25
	v_mul_f32_e32 v25, v72, v29
	v_cvt_pk_fp8_f32 v33, v24, v25 op_sel:[0,0,1]
	v_mul_f32_e32 v24, v72, v34
	v_mul_f32_e32 v25, v72, v38
	v_mov_b32_e32 v34, v87
	v_cvt_pk_fp8_f32 v34, v24, v25
	v_mul_f32_e32 v24, v72, v35
	v_mul_f32_e32 v25, v72, v39
	v_mov_b32_e32 v35, v87
	v_cvt_pk_fp8_f32 v35, v24, v25
	v_mul_f32_e32 v24, v72, v27
	v_mul_f32_e32 v25, v72, v31
	s_waitcnt vmcnt(16)
	v_mul_f32_e32 v20, v72, v20
	v_cvt_pk_fp8_f32 v35, v24, v25 op_sel:[0,0,1]
	v_mul_f32_e32 v24, v72, v16
	v_mov_b32_e32 v16, v87
	v_cvt_pk_fp8_f32 v16, v24, v20
	v_mul_f32_e32 v20, v72, v17
	v_mul_f32_e32 v21, v72, v21
	v_mov_b32_e32 v17, v87
	v_cvt_pk_fp8_f32 v17, v20, v21
	s_waitcnt vmcnt(15)
	v_mul_f32_e32 v8, v72, v8
	s_waitcnt vmcnt(14)
	v_mul_f32_e32 v12, v72, v12
	v_cvt_pk_fp8_f32 v16, v8, v12 op_sel:[0,0,1]
	v_mul_f32_e32 v8, v72, v9
	v_mul_f32_e32 v9, v72, v13
	v_cvt_pk_fp8_f32 v17, v8, v9 op_sel:[0,0,1]
	v_mul_f32_e32 v8, v72, v18
	v_mul_f32_e32 v9, v72, v22
	v_mov_b32_e32 v18, v87
	s_mul_i32 s4, s4, s3
	v_cvt_pk_fp8_f32 v18, v8, v9
	v_mul_f32_e32 v8, v72, v19
	v_mul_f32_e32 v9, v72, v23
	v_mov_b32_e32 v19, v87
	s_add_i32 s4, s4, s2
	v_cvt_pk_fp8_f32 v19, v8, v9
	s_mul_hi_i32 s5, s4, 0x2aaaaaab
	s_lshr_b32 s8, s5, 31
	s_ashr_i32 s5, s5, 7
	v_mul_f32_e32 v26, v72, v26
	v_mul_f32_e32 v28, v72, v30
	s_add_i32 s5, s5, s8
	v_cvt_pk_fp8_f32 v34, v26, v28 op_sel:[0,0,1]
	v_mul_f32_e32 v10, v72, v10
	v_mul_f32_e32 v12, v72, v14
	v_mul_f32_e32 v8, v72, v11
	v_mul_f32_e32 v9, v72, v15
	s_add_i32 s8, s5, 18
	s_mulk_i32 s5, 0x300
	v_cvt_pk_fp8_f32 v18, v10, v12 op_sel:[0,0,1]
	v_cvt_pk_fp8_f32 v19, v8, v9 op_sel:[0,0,1]
	s_sub_i32 s31, s4, s5
	s_cmpk_lt_i32 s31, 0x200
	s_cselect_b64 s[4:5], -1, 0
	s_cmpk_gt_i32 s31, 0x1ff
	s_waitcnt lgkmcnt(0)
	s_barrier
	ds_write_b128 v240, v[32:35]
	ds_write_b128 v241, v[16:19]
	s_cbranch_scc0 .LBB0_831
	s_load_dwordx2 s[12:13], s[14:15], 0x110
	s_ashr_i32 s9, s8, 31
	s_lshl_b64 s[56:57], s[8:9], 24
	s_mov_b32 s53, s18
	s_waitcnt lgkmcnt(0)
	s_add_u32 s12, s12, s56
	s_addc_u32 s13, s13, s57
	s_lshl_b32 s9, s31, 3
	s_and_b32 s9, s9, 0x7fffffc0
	s_add_i32 s52, s9, 0xfffff000
	s_mov_b64 s[56:57], 0

.LBB0_833:
	s_lshl_b64 s[52:53], s[52:53], 13
	s_add_u32 s8, s12, s52
	s_addc_u32 s12, s13, s53
	s_lshl_b32 s9, s31, s9
	s_and_b32 s9, s9, 0x700
	s_lshl_b32 s9, s9, 2
	s_add_u32 s8, s8, s9
	s_addc_u32 s9, s12, 0
	s_add_i32 s19, s19, 4
	s_cmp_gt_i32 s19, s59
	s_cselect_b64 s[52:53], -1, 0
	v_cndmask_b32_e64 v8, v180, 0, s[52:53]
	s_and_b64 s[12:13], s[52:53], exec
	s_cselect_b32 s12, 0, 0x800
	v_lshlrev_b32_e32 v86, 2, v8
	v_lshl_add_u64 v[16:17], s[8:9], 0, v[86:87]
	v_mad_i64_i32 v[8:9], s[8:9], s12, v181, 0
	v_mad_i64_i32 v[10:11], s[8:9], s12, v182, 0
	v_lshl_add_u64 v[8:9], v[8:9], 2, v[16:17]
	v_lshl_add_u64 v[10:11], v[10:11], 2, v[16:17]
	global_load_dwordx4 v[24:27], v[8:9], off nt
	global_load_dwordx4 v[28:31], v[10:11], off nt
	v_mad_i64_i32 v[8:9], s[8:9], s12, v183, 0
	v_mad_i64_i32 v[10:11], s[8:9], s12, v184, 0
	v_lshl_add_u64 v[8:9], v[8:9], 2, v[16:17]
	v_lshl_add_u64 v[10:11], v[10:11], 2, v[16:17]
	global_load_dwordx4 v[32:35], v[8:9], off nt
	global_load_dwordx4 v[36:39], v[10:11], off nt
	v_mad_i64_i32 v[8:9], s[8:9], s12, v185, 0
	v_mad_i64_i32 v[10:11], s[8:9], s12, v186, 0
	v_mad_i64_i32 v[18:19], s[8:9], s12, v187, 0
	v_mad_i64_i32 v[20:21], s[8:9], s12, v188, 0
	v_lshl_add_u64 v[8:9], v[8:9], 2, v[16:17]
	v_lshl_add_u64 v[12:13], v[10:11], 2, v[16:17]
	v_lshl_add_u64 v[18:19], v[18:19], 2, v[16:17]
	v_lshl_add_u64 v[20:21], v[20:21], 2, v[16:17]
	global_load_dwordx4 v[8:11], v[8:9], off nt
	s_nop 0
	global_load_dwordx4 v[12:15], v[12:13], off nt
	s_nop 0
	global_load_dwordx4 v[16:19], v[18:19], off nt
	s_nop 0
	global_load_dwordx4 v[20:23], v[20:21], off nt
	s_max_i32 s8, s62, 0
	s_min_i32 s8, s8, s59
	s_mul_i32 s8, s8, s3
	s_add_i32 s9, s8, s2
	s_mul_hi_i32 s8, s9, 0x2aaaaaab
	s_lshr_b32 s12, s8, 31
	s_ashr_i32 s8, s8, 7
	s_add_i32 s12, s8, s12
	s_add_i32 s8, s12, 18
	s_mulk_i32 s12, 0x300
	s_sub_i32 s19, s9, s12
	s_ashr_i32 s9, s8, 31
	s_cmpk_gt_i32 s19, 0x1ff
	s_mov_b64 s[56:57], -1
	s_cbranch_scc0 .LBB0_835
	s_lshl_b32 s12, s19, 3
	s_and_b32 s31, s12, 0x7fffffc0
	s_lshl_b32 s12, s19, 19
	s_and_b32 s39, s12, 0x380000
	s_lshl_b64 s[12:13], s[8:9], 22
	s_add_u32 s12, s16, s12
	s_addc_u32 s13, s17, s13
	s_add_u32 s12, s12, s39
	s_addc_u32 s13, s13, 0
	s_add_u32 s12, s12, s31
	s_addc_u32 s13, s13, 0
	s_add_u32 s12, s12, 0x24dff000
	s_addc_u32 s13, s13, 0
	s_mov_b64 s[56:57], 0

.LBB0_837:
	s_cmp_lt_i32 s62, 0
	s_cselect_b64 s[8:9], -1, 0
	s_or_b64 s[0:1], s[8:9], s[0:1]
	s_and_b64 s[0:1], s[0:1], exec
	s_cselect_b32 s8, 0x80, s31
	v_mul_i32_i24_e32 v76, s8, v191
	ds_read_b32 v72, v239
	ds_read_b32 v73, v239 offset:1040
	ds_read_b32 v74, v239 offset:2080
	ds_read_b32 v75, v239 offset:3120
	v_or_b32_e32 v76, v76, v189
	v_ashrrev_i32_e32 v77, 31, v76
	s_cselect_b32 s1, s66, s13
	s_cselect_b32 s0, s65, s12
	v_lshlrev_b64 v[76:77], 11, v[76:77]
	v_lshl_add_u64 v[76:77], s[0:1], 0, v[76:77]
	v_lshl_add_u64 v[78:79], v[76:77], 0, v[88:89]
	ds_read_b32 v76, v242
	ds_read_b32 v77, v242 offset:1040
	ds_read_b32 v148, v233 offset:112
	s_waitcnt lgkmcnt(3)
	global_store_dwordx4 v[78:79], v[72:75], off
	ds_read_b32 v78, v242 offset:2080
	ds_read_b32 v79, v242 offset:3120
	v_mul_i32_i24_e32 v72, s8, v201
	v_or_b32_e32 v72, v72, v189
	v_ashrrev_i32_e32 v73, 31, v72
	v_lshlrev_b64 v[72:73], 11, v[72:73]
	v_lshl_add_u64 v[72:73], s[0:1], 0, v[72:73]
	v_lshl_add_u64 v[72:73], v[72:73], 0, v[88:89]
	s_waitcnt lgkmcnt(0)
	global_store_dwordx4 v[72:73], v[76:79], off
	ds_read2_b32 v[152:153], v233 offset0:11 offset1:17
	ds_read_b96 v[80:82], v233 offset:48
	ds_read2_b32 v[168:169], v233 offset0:9 offset1:10
	ds_read2_b32 v[150:151], v233 offset0:15 offset1:16
	v_mov_b32_e32 v86, v215
	v_mov_b32_e32 v149, v148
	v_lshlrev_b32_e32 v243, 3, v86
	v_ashrrev_i32_e32 v245, 3, v86
	v_and_b32_e32 v72, 56, v243
	v_cmp_ne_u32_e64 s[8:9], 0, v72
	v_cmp_ne_u32_e32 vcc, 56, v72
	v_add_u32_e32 v72, -1, v245
	v_lshl_add_u32 v244, v86, 4, v216
	v_cmp_gt_u32_e64 s[12:13], 32, v72
	v_mov_b64_e32 v[162:163], v[148:149]
	v_mov_b64_e32 v[164:165], v[148:149]
	v_mov_b64_e32 v[166:167], v[148:149]
	v_mov_b64_e32 v[156:157], v[148:149]
	v_mov_b64_e32 v[154:155], v[148:149]
	v_mov_b64_e32 v[158:159], v[148:149]
	v_mov_b64_e32 v[160:161], v[148:149]
	s_and_saveexec_b64 s[0:1], s[12:13]
	s_cbranch_execz .LBB0_847
	v_add_u32_e32 v72, 0xffffff80, v244
	ds_read_b128 v[76:79], v72
	v_mov_b32_e32 v161, 0
	v_mov_b32_e32 v154, 0
	s_and_saveexec_b64 s[12:13], s[8:9]
	s_cbranch_execz .LBB0_840
	v_add_u32_e32 v72, 0xffffff7e, v244
	ds_read_u16 v72, v72
	s_waitcnt lgkmcnt(0)
	v_lshlrev_b32_e32 v154, 16, v72

.LBB0_867:
	s_or_b64 exec, exec, s[0:1]
	v_pk_add_f32 v[72:73], v[146:147], v[170:171]
	v_pk_add_f32 v[74:75], v[168:169], v[172:173]
	v_pk_add_f32 v[76:77], v[132:133], v[136:137]
	v_pk_add_f32 v[72:73], v[72:73], v[74:75]
	v_pk_add_f32 v[74:75], v[130:131], v[134:135]
	v_pk_add_f32 v[78:79], v[138:139], v[142:143]
	v_pk_add_f32 v[74:75], v[74:75], v[76:77]
	v_pk_add_f32 v[76:77], v[144:145], v[140:141]
	v_pk_add_f32 v[82:83], v[122:123], v[126:127]
	v_pk_add_f32 v[76:77], v[76:77], v[78:79]
	v_lshlrev_b32_e32 v78, 2, v86
	v_and_b32_e32 v78, -8, v78
	v_lshlrev_b32_e32 v79, 3, v243
	v_add3_u32 v80, v219, v78, v79
	v_mov_b32_e32 v78, v156
	v_mov_b32_e32 v79, v148
	v_mov_b32_e32 v148, v157
	ds_write2_b64 v80, v[78:79], v[148:149] offset1:1
	v_mov_b32_e32 v78, v154
	v_mov_b32_e32 v79, v162
	v_mov_b32_e32 v162, v155
	ds_write2_b64 v80, v[78:79], v[162:163] offset0:2 offset1:3
	v_mov_b32_e32 v78, v158
	v_mov_b32_e32 v79, v164
	v_mov_b32_e32 v164, v159
	ds_write2_b64 v80, v[78:79], v[164:165] offset0:4 offset1:5
	v_mov_b32_e32 v78, v160
	v_mov_b32_e32 v79, v166
	v_mov_b32_e32 v166, v161
	ds_write2_b64 v80, v[78:79], v[166:167] offset0:6 offset1:7
	s_waitcnt lgkmcnt(0)
	s_barrier
	ds_read_b32 v78, v233 offset:120
	v_pk_add_f32 v[80:81], v[128:129], v[124:125]
	s_mov_b32 s56, s34
	v_pk_add_f32 v[80:81], v[80:81], v[82:83]
	ds_read_b64 v[82:83], v222
	ds_read_b64 v[124:125], v223 offset:2048
	ds_read_b64 v[126:127], v224 offset:4096
	ds_read_b64 v[128:129], v225 offset:6144
	ds_read_b64 v[130:131], v226 offset:8192
	ds_read_b64 v[132:133], v227 offset:10240
	ds_read_b64 v[134:135], v228 offset:12288
	ds_read_b64 v[136:137], v229 offset:14336
	s_waitcnt lgkmcnt(8)
	v_pk_fma_f32 v[74:75], v[110:111], v[78:79], v[74:75] op_sel_hi:[1,0,1]
	v_pk_fma_f32 v[114:115], v[102:103], v[78:79], v[114:115] op_sel_hi:[1,0,1]
	s_waitcnt lgkmcnt(6)
	v_pk_mul_f32 v[110:111], v[124:125], v[74:75]
	v_pk_fma_f32 v[76:77], v[108:109], v[78:79], v[76:77] op_sel_hi:[1,0,1]
	s_waitcnt lgkmcnt(2)
	v_pk_mul_f32 v[102:103], v[114:115], v[132:133]
	v_pk_fma_f32 v[116:117], v[100:101], v[78:79], v[116:117] op_sel_hi:[1,0,1]
	v_pk_fma_f32 v[74:75], v[124:125], v[74:75], 0 op_sel_hi:[1,1,0]
	v_pk_fma_f32 v[114:115], v[114:115], v[132:133], 0 op_sel_hi:[1,1,0]
	v_pk_fma_f32 v[122:123], v[112:113], v[78:79], v[72:73] op_sel_hi:[1,0,1]
	v_pk_mul_f32 v[108:109], v[126:127], v[76:77]
	v_pk_fma_f32 v[80:81], v[106:107], v[78:79], v[80:81] op_sel_hi:[1,0,1]
	v_pk_fma_f32 v[120:121], v[104:105], v[78:79], v[120:121] op_sel_hi:[1,0,1]
	s_waitcnt lgkmcnt(1)
	v_pk_mul_f32 v[100:101], v[116:117], v[134:135]
	v_pk_fma_f32 v[78:79], v[98:99], v[78:79], v[118:119] op_sel_hi:[1,0,1]
	v_pk_add_f32 v[124:125], v[74:75], v[114:115]
	v_pk_add_f32 v[74:75], v[74:75], v[114:115] neg_lo:[0,1] neg_hi:[0,1]
	v_pk_fma_f32 v[114:115], v[102:103], s[28:29], v[110:111] op_sel:[1,0,0] op_sel_hi:[0,1,1]
	v_pk_fma_f32 v[76:77], v[126:127], v[76:77], 0 op_sel_hi:[1,1,0]
	v_pk_fma_f32 v[116:117], v[116:117], v[134:135], 0 op_sel_hi:[1,1,0]
	s_mov_b32 s57, s30
	v_pk_mul_f32 v[106:107], v[128:129], v[80:81]
	s_waitcnt lgkmcnt(0)
	v_pk_mul_f32 v[98:99], v[78:79], v[136:137]
	v_pk_add_f32 v[126:127], v[76:77], v[116:117]
	v_pk_add_f32 v[76:77], v[76:77], v[116:117] neg_lo:[0,1] neg_hi:[0,1]
	v_pk_fma_f32 v[116:117], v[100:101], s[28:29], v[108:109] op_sel:[1,0,0] op_sel_hi:[0,1,1]
	v_pk_fma_f32 v[80:81], v[128:129], v[80:81], 0 op_sel_hi:[1,1,0]
	v_pk_fma_f32 v[78:79], v[78:79], v[136:137], 0 op_sel_hi:[1,1,0]
	v_pk_mul_f32 v[138:139], v[114:115], s[56:57] op_sel_hi:[0,1]
	s_mov_b32 s0, s35
	s_mov_b32 s1, s34
	s_mov_b32 s12, s37
	s_mov_b32 s13, s36
	v_pk_add_f32 v[128:129], v[80:81], v[78:79]
	v_pk_add_f32 v[78:79], v[80:81], v[78:79] neg_lo:[0,1] neg_hi:[0,1]
	v_pk_fma_f32 v[80:81], v[98:99], s[28:29], v[106:107] op_sel:[1,0,0] op_sel_hi:[0,1,1]
	v_pk_fma_f32 v[114:115], v[114:115], s[0:1], v[138:139] op_sel:[1,0,0]
	v_pk_mul_f32 v[138:139], v[116:117], s[12:13] op_sel_hi:[0,1]
	s_mov_b32 s58, s37
	s_mov_b32 s8, s35
	s_mov_b32 s9, s38
	v_pk_fma_f32 v[116:117], v[116:117], s[58:59], v[138:139] op_sel:[1,0,0] op_sel_hi:[1,0,1]
	v_pk_mul_f32 v[138:139], v[80:81], s[8:9] op_sel_hi:[0,1]
	v_pk_fma_f32 v[80:81], v[80:81], s[34:35], v[138:139] op_sel:[1,0,0]
	v_pk_mul_f32 v[138:139], v[74:75], s[12:13] op_sel_hi:[0,1]
	s_mov_b32 s19, s26
	v_pk_fma_f32 v[132:133], v[102:103], s[26:27], v[110:111] op_sel:[1,0,0] op_sel_hi:[0,1,1]
	v_pk_fma_f32 v[74:75], v[74:75], s[58:59], v[138:139] op_sel:[1,0,0] op_sel_hi:[1,0,1]
	v_pk_mul_f32 v[138:139], v[76:77], s[18:19] op_sel_hi:[0,1]
	s_mov_b32 s60, s27
	s_mov_b32 s61, s18
	v_pk_mul_f32 v[112:113], v[82:83], v[122:123]
	v_pk_mul_f32 v[104:105], v[120:121], v[130:131]
	v_pk_fma_f32 v[82:83], v[82:83], v[122:123], 0 op_sel_hi:[1,1,0]
	v_pk_fma_f32 v[120:121], v[120:121], v[130:131], 0 op_sel_hi:[1,1,0]
	v_pk_fma_f32 v[136:137], v[98:99], s[26:27], v[106:107] op_sel:[1,0,0] op_sel_hi:[0,1,1]
	v_pk_fma_f32 v[76:77], v[76:77], s[60:61], v[138:139] op_sel:[1,0,0]
	v_pk_mul_f32 v[138:139], v[132:133], s[8:9] op_sel_hi:[0,1]
	s_mov_b32 s39, s35
	v_pk_add_f32 v[122:123], v[82:83], v[120:121]
	v_pk_fma_f32 v[132:133], v[132:133], s[34:35], v[138:139] op_sel:[1,0,0]
	v_pk_mul_f32 v[138:139], v[136:137], s[38:39] op_sel_hi:[0,1]
	s_mov_b32 s31, s38
	v_pk_add_f32 v[82:83], v[82:83], v[120:121] neg_lo:[0,1] neg_hi:[0,1]
	v_pk_fma_f32 v[120:121], v[104:105], s[28:29], v[112:113] op_sel:[1,0,0] op_sel_hi:[0,1,1]
	v_pk_fma_f32 v[134:135], v[100:101], s[26:27], v[108:109] op_sel:[1,0,0] op_sel_hi:[0,1,1]
	v_mul_f32_e32 v86, 0xbf3504f3, v78
	v_pk_fma_f32 v[136:137], v[136:137], s[30:31], v[138:139] op_sel:[1,0,0]
	v_pk_add_f32 v[138:139], v[122:123], v[126:127]
	v_pk_add_f32 v[122:123], v[122:123], v[126:127] neg_lo:[0,1] neg_hi:[0,1]
	v_pk_add_f32 v[126:127], v[124:125], v[128:129]
	v_pk_add_f32 v[124:125], v[124:125], v[128:129] neg_lo:[0,1] neg_hi:[0,1]
	v_pk_fma_f32 v[78:79], v[78:79], s[12:13], v[86:87] op_sel:[1,0,0] op_sel_hi:[1,1,0]
	v_mul_f32_e32 v86, 0xbf3504f3, v134
	v_pk_add_f32 v[128:129], v[138:139], v[126:127]
	v_pk_add_f32 v[126:127], v[138:139], v[126:127] neg_lo:[0,1] neg_hi:[0,1]
	v_pk_fma_f32 v[138:139], v[124:125], s[28:29], v[122:123] op_sel:[1,0,0] op_sel_hi:[0,1,1]
	v_pk_fma_f32 v[122:123], v[124:125], s[26:27], v[122:123] op_sel:[1,0,0] op_sel_hi:[0,1,1]
	v_pk_add_f32 v[124:125], v[120:121], v[116:117]
	v_pk_add_f32 v[116:117], v[120:121], v[116:117] neg_lo:[0,1] neg_hi:[0,1]
	v_pk_add_f32 v[120:121], v[114:115], v[80:81]
	v_pk_add_f32 v[80:81], v[114:115], v[80:81] neg_lo:[0,1] neg_hi:[0,1]
	v_pk_fma_f32 v[130:131], v[104:105], s[26:27], v[112:113] op_sel:[1,0,0] op_sel_hi:[0,1,1]
	v_pk_fma_f32 v[134:135], v[134:135], s[12:13], v[86:87] op_sel:[1,0,0] op_sel_hi:[1,1,0]
	v_pk_add_f32 v[114:115], v[124:125], v[120:121]
	v_pk_add_f32 v[120:121], v[124:125], v[120:121] neg_lo:[0,1] neg_hi:[0,1]
	v_pk_fma_f32 v[124:125], v[80:81], s[28:29], v[116:117] op_sel:[1,0,0] op_sel_hi:[0,1,1]
	v_pk_fma_f32 v[80:81], v[80:81], s[26:27], v[116:117] op_sel:[1,0,0] op_sel_hi:[0,1,1]
	v_pk_add_f32 v[116:117], v[82:83], v[76:77]
	v_pk_add_f32 v[76:77], v[82:83], v[76:77] neg_lo:[0,1] neg_hi:[0,1]
	v_pk_add_f32 v[82:83], v[74:75], v[78:79]
	v_pk_add_f32 v[74:75], v[74:75], v[78:79] neg_lo:[0,1] neg_hi:[0,1]
	v_mov_b32_e32 v118, v217
	v_mov_b32_e32 v72, v218
	v_mov_b32_e32 v162, v215
	v_mov_b32_e32 v119, v220
	v_mov_b32_e32 v73, v221
	v_pk_add_f32 v[78:79], v[116:117], v[82:83]
	v_pk_add_f32 v[82:83], v[116:117], v[82:83] neg_lo:[0,1] neg_hi:[0,1]
	v_pk_fma_f32 v[116:117], v[74:75], s[28:29], v[76:77] op_sel:[1,0,0] op_sel_hi:[0,1,1]
	v_pk_fma_f32 v[74:75], v[74:75], s[26:27], v[76:77] op_sel:[1,0,0] op_sel_hi:[0,1,1]
	v_pk_add_f32 v[76:77], v[130:131], v[134:135]
	v_pk_add_f32 v[130:131], v[130:131], v[134:135] neg_lo:[0,1] neg_hi:[0,1]
	v_pk_add_f32 v[134:135], v[132:133], v[136:137]
	v_pk_add_f32 v[132:133], v[132:133], v[136:137] neg_lo:[0,1] neg_hi:[0,1]
	v_pk_add_f32 v[136:137], v[76:77], v[134:135]
	v_pk_add_f32 v[76:77], v[76:77], v[134:135] neg_lo:[0,1] neg_hi:[0,1]
	v_pk_fma_f32 v[134:135], v[132:133], s[28:29], v[130:131] op_sel:[1,0,0] op_sel_hi:[0,1,1]
	v_pk_fma_f32 v[130:131], v[132:133], s[26:27], v[130:131] op_sel:[1,0,0] op_sel_hi:[0,1,1]
	v_pk_mul_f32 v[132:133], v[118:119], s[28:29]
	v_mov_b32_e32 v86, v119
	v_pk_mul_f32 v[140:141], v[118:119], v[118:119] op_sel_hi:[1,0]
	v_pk_mul_f32 v[160:161], v[118:119], v[114:115] op_sel_hi:[1,0]
	v_pk_fma_f32 v[140:141], v[86:87], v[132:133], v[140:141] op_sel:[0,1,0] op_sel_hi:[0,0,1]
	v_pk_mul_f32 v[144:145], v[140:141], s[28:29]
	v_pk_mul_f32 v[146:147], v[140:141], v[140:141] op_sel_hi:[1,0]
	v_pk_mul_f32 v[142:143], v[118:119], v[140:141] op_sel_hi:[1,0]
	v_pk_fma_f32 v[146:147], v[140:141], v[144:145], v[146:147] op_sel:[1,1,0] op_sel_hi:[1,0,1]
	v_pk_fma_f32 v[142:143], v[140:141], v[132:133], v[142:143] op_sel:[1,1,0] op_sel_hi:[1,0,1]
	v_pk_mul_f32 v[148:149], v[118:119], v[146:147] op_sel_hi:[1,0]
	v_pk_fma_f32 v[114:115], v[114:115], v[132:133], v[160:161] op_sel:[1,1,0] op_sel_hi:[1,0,1]
	v_pk_fma_f32 v[148:149], v[146:147], v[132:133], v[148:149] op_sel:[1,1,0] op_sel_hi:[1,0,1]
	v_pk_mul_f32 v[132:133], v[140:141], v[78:79] op_sel_hi:[1,0]
	v_pk_mul_f32 v[152:153], v[142:143], s[28:29]
	v_pk_fma_f32 v[78:79], v[78:79], v[144:145], v[132:133] op_sel:[1,1,0] op_sel_hi:[1,0,1]
	v_pk_mul_f32 v[132:133], v[136:137], v[142:143] op_sel_hi:[0,1]
	v_pk_mul_f32 v[150:151], v[140:141], v[146:147] op_sel_hi:[1,0]
	v_pk_mul_f32 v[156:157], v[146:147], s[28:29]
	v_pk_fma_f32 v[132:133], v[136:137], v[152:153], v[132:133] op_sel:[1,1,0] op_sel_hi:[1,0,1]
	v_pk_mul_f32 v[136:137], v[138:139], v[146:147] op_sel_hi:[0,1]
	v_pk_fma_f32 v[150:151], v[146:147], v[144:145], v[150:151] op_sel:[1,1,0] op_sel_hi:[1,0,1]
	v_pk_mul_f32 v[154:155], v[142:143], v[146:147] op_sel_hi:[1,0]
	v_pk_fma_f32 v[136:137], v[138:139], v[156:157], v[136:137] op_sel:[1,1,0] op_sel_hi:[1,0,1]
	v_pk_mul_f32 v[138:139], v[148:149], s[28:29]
	v_pk_mul_f32 v[144:145], v[124:125], v[148:149] op_sel_hi:[0,1]
	v_pk_fma_f32 v[154:155], v[146:147], v[152:153], v[154:155] op_sel:[1,1,0] op_sel_hi:[1,0,1]
	v_pk_mul_f32 v[158:159], v[146:147], v[146:147] op_sel_hi:[1,0]
	v_pk_fma_f32 v[124:125], v[124:125], v[138:139], v[144:145] op_sel:[1,1,0] op_sel_hi:[1,0,1]
	v_pk_mul_f32 v[138:139], v[150:151], s[28:29]
	v_pk_mul_f32 v[144:145], v[116:117], v[150:151] op_sel_hi:[0,1]
	v_pk_fma_f32 v[158:159], v[146:147], v[156:157], v[158:159] op_sel:[1,1,0] op_sel_hi:[1,0,1]
	v_pk_fma_f32 v[116:117], v[116:117], v[138:139], v[144:145] op_sel:[1,1,0] op_sel_hi:[1,0,1]
	v_pk_mul_f32 v[138:139], v[154:155], s[28:29]
	v_pk_mul_f32 v[144:145], v[134:135], v[154:155] op_sel_hi:[0,1]
	v_pk_fma_f32 v[134:135], v[134:135], v[138:139], v[144:145] op_sel:[1,1,0] op_sel_hi:[1,0,1]
	v_pk_mul_f32 v[138:139], v[158:159], s[28:29]
	v_pk_mul_f32 v[118:119], v[118:119], v[158:159] op_sel_hi:[0,1]
	v_pk_mul_f32 v[144:145], v[126:127], v[158:159] op_sel_hi:[0,1]
	v_pk_fma_f32 v[118:119], v[86:87], v[138:139], v[118:119] op_sel:[0,1,0] op_sel_hi:[0,0,1]
	v_pk_fma_f32 v[126:127], v[126:127], v[138:139], v[144:145] op_sel:[1,1,0] op_sel_hi:[1,0,1]
	v_pk_mul_f32 v[144:145], v[118:119], s[28:29]
	v_pk_mul_f32 v[118:119], v[120:121], v[118:119] op_sel_hi:[0,1]
	v_pk_fma_f32 v[118:119], v[120:121], v[144:145], v[118:119] op_sel:[1,1,0] op_sel_hi:[1,0,1]
	v_pk_mul_f32 v[120:121], v[140:141], v[158:159] op_sel_hi:[0,1]
	v_pk_fma_f32 v[120:121], v[140:141], v[138:139], v[120:121] op_sel:[1,1,0] op_sel_hi:[1,0,1]
	v_ashrrev_i32_e32 v86, 4, v162
	v_pk_mul_f32 v[140:141], v[120:121], s[28:29]
	v_pk_mul_f32 v[120:121], v[82:83], v[120:121] op_sel_hi:[0,1]
	v_pk_fma_f32 v[82:83], v[82:83], v[140:141], v[120:121] op_sel:[1,1,0] op_sel_hi:[1,0,1]
	v_pk_mul_f32 v[120:121], v[142:143], v[158:159] op_sel_hi:[0,1]
	v_pk_fma_f32 v[120:121], v[142:143], v[138:139], v[120:121] op_sel:[1,1,0] op_sel_hi:[1,0,1]
	s_mov_b32 s79, 0x62704000
	v_pk_mul_f32 v[140:141], v[120:121], s[28:29]
	v_pk_mul_f32 v[120:121], v[76:77], v[120:121] op_sel_hi:[0,1]
	v_pk_fma_f32 v[76:77], v[76:77], v[140:141], v[120:121] op_sel:[1,1,0] op_sel_hi:[1,0,1]
	v_pk_mul_f32 v[120:121], v[146:147], v[158:159] op_sel_hi:[0,1]
	v_pk_fma_f32 v[120:121], v[146:147], v[138:139], v[120:121] op_sel:[1,1,0] op_sel_hi:[1,0,1]
	s_add_i32 s78, s62, 4
	v_pk_mul_f32 v[140:141], v[120:121], s[28:29]
	v_pk_mul_f32 v[120:121], v[122:123], v[120:121] op_sel_hi:[0,1]
	v_pk_fma_f32 v[120:121], v[122:123], v[140:141], v[120:121] op_sel:[1,1,0] op_sel_hi:[1,0,1]
	v_pk_mul_f32 v[122:123], v[158:159], v[148:149] op_sel_hi:[1,0]
	s_nop 0
	v_pk_fma_f32 v[122:123], v[148:149], v[138:139], v[122:123] op_sel:[1,1,0] op_sel_hi:[1,0,1]
	s_nop 0
	v_pk_mul_f32 v[140:141], v[122:123], s[28:29]
	v_pk_mul_f32 v[122:123], v[80:81], v[122:123] op_sel_hi:[0,1]
	v_pk_fma_f32 v[80:81], v[80:81], v[140:141], v[122:123] op_sel:[1,1,0] op_sel_hi:[1,0,1]
	v_pk_mul_f32 v[122:123], v[158:159], v[150:151] op_sel_hi:[1,0]
	s_nop 0
	v_pk_fma_f32 v[122:123], v[150:151], v[138:139], v[122:123] op_sel:[1,1,0] op_sel_hi:[1,0,1]
	s_nop 0
	v_pk_mul_f32 v[140:141], v[122:123], s[28:29]
	v_pk_mul_f32 v[122:123], v[74:75], v[122:123] op_sel_hi:[0,1]
	v_pk_fma_f32 v[74:75], v[74:75], v[140:141], v[122:123] op_sel:[1,1,0] op_sel_hi:[1,0,1]
	v_pk_mul_f32 v[122:123], v[158:159], v[154:155] op_sel_hi:[1,0]
	s_nop 0
	v_pk_fma_f32 v[122:123], v[154:155], v[138:139], v[122:123] op_sel:[1,1,0] op_sel_hi:[1,0,1]
	s_nop 0
	v_pk_mul_f32 v[138:139], v[122:123], s[28:29]
	v_pk_mul_f32 v[122:123], v[130:131], v[122:123] op_sel_hi:[0,1]
	v_pk_fma_f32 v[122:123], v[130:131], v[138:139], v[122:123] op_sel:[1,1,0] op_sel_hi:[1,0,1]
	v_lshlrev_b32_e32 v130, 3, v162
	v_add_u32_e32 v160, v219, v130
	v_lshl_add_u32 v131, v86, 3, v160
	ds_write_b64 v131, v[128:129]
	v_add_u32_e32 v128, 0x100, v162
	v_ashrrev_i32_e32 v128, 4, v128
	v_lshl_add_u32 v128, v128, 3, v160
	ds_write_b64 v128, v[114:115] offset:2048
	v_add_u32_e32 v114, 0x200, v162
	v_ashrrev_i32_e32 v114, 4, v114
	v_lshl_add_u32 v114, v114, 3, v160
	ds_write_b64 v114, v[78:79] offset:4096
	v_add_u32_e32 v78, 0x300, v162
	v_ashrrev_i32_e32 v78, 4, v78
	v_lshl_add_u32 v78, v78, 3, v160
	ds_write_b64 v78, v[132:133] offset:6144
	v_add_u32_e32 v78, 0x400, v162
	v_ashrrev_i32_e32 v78, 4, v78
	v_lshl_add_u32 v78, v78, 3, v160
	ds_write_b64 v78, v[136:137] offset:8192
	v_add_u32_e32 v78, 0x500, v162
	v_ashrrev_i32_e32 v78, 4, v78
	v_lshl_add_u32 v78, v78, 3, v160
	ds_write_b64 v78, v[124:125] offset:10240
	v_add_u32_e32 v78, 0x600, v162
	v_ashrrev_i32_e32 v78, 4, v78
	v_lshl_add_u32 v78, v78, 3, v160
	ds_write_b64 v78, v[116:117] offset:12288
	v_add_u32_e32 v78, 0x700, v162
	v_ashrrev_i32_e32 v78, 4, v78
	v_lshl_add_u32 v78, v78, 3, v160
	ds_write_b64 v78, v[134:135] offset:14336
	v_add_u32_e32 v78, 0x800, v162
	v_ashrrev_i32_e32 v78, 4, v78
	v_lshl_add_u32 v78, v78, 3, v160
	ds_write_b64 v78, v[126:127] offset:16384
	v_add_u32_e32 v78, 0x900, v162
	v_ashrrev_i32_e32 v78, 4, v78
	v_lshl_add_u32 v78, v78, 3, v160
	ds_write_b64 v78, v[118:119] offset:18432
	v_add_u32_e32 v78, 0xa00, v162
	v_ashrrev_i32_e32 v78, 4, v78
	v_lshl_add_u32 v78, v78, 3, v160
	ds_write_b64 v78, v[82:83] offset:20480
	v_add_u32_e32 v78, 0xb00, v162
	v_ashrrev_i32_e32 v78, 4, v78
	v_lshl_add_u32 v78, v78, 3, v160
	ds_write_b64 v78, v[76:77] offset:22528
	v_add_u32_e32 v76, 0xc00, v162
	v_ashrrev_i32_e32 v76, 4, v76
	v_lshl_add_u32 v76, v76, 3, v160
	ds_write_b64 v76, v[120:121] offset:24576
	v_add_u32_e32 v76, 0xd00, v162
	v_ashrrev_i32_e32 v76, 4, v76
	v_lshl_add_u32 v76, v76, 3, v160
	ds_write_b64 v76, v[80:81] offset:26624
	v_add_u32_e32 v76, 0xe00, v162
	v_ashrrev_i32_e32 v76, 4, v76
	v_lshl_add_u32 v76, v76, 3, v160
	ds_write_b64 v76, v[74:75] offset:28672
	v_add_u32_e32 v74, 0xf00, v162
	v_ashrrev_i32_e32 v74, 4, v74
	v_lshl_add_u32 v74, v74, 3, v160
	ds_write_b64 v74, v[122:123] offset:30720
	v_lshlrev_b32_e32 v74, 8, v86
	v_lshl_add_u32 v75, v86, 7, v219
	v_lshlrev_b32_e32 v76, 11, v86
	v_and_b32_e32 v77, 0x78, v130
	v_add3_u32 v161, v75, v76, v77
	v_ashrrev_i32_e32 v74, 1, v74
	s_waitcnt lgkmcnt(0)
	s_barrier
	ds_read_b64 v[82:83], v161
	v_add_u32_e32 v74, v219, v74
	v_add3_u32 v163, v74, v76, v77
	ds_read2_b64 v[74:77], v163 offset0:17 offset1:34
	ds_read2_b64 v[78:81], v163 offset0:51 offset1:68
	ds_read2_b64 v[114:117], v163 offset0:85 offset1:102
	ds_read2_b64 v[118:121], v163 offset0:119 offset1:136
	ds_read2_b64 v[122:125], v163 offset0:153 offset1:170
	ds_read2_b64 v[126:129], v163 offset0:187 offset1:204
	ds_read2_b64 v[130:133], v163 offset0:221 offset1:238
	ds_read_b64 v[134:135], v163 offset:2040
	v_pk_mul_f32 v[138:139], v[72:73], v[72:73] op_sel_hi:[1,0]
	s_waitcnt lgkmcnt(4)
	v_pk_add_f32 v[136:137], v[82:83], v[120:121]
	v_pk_add_f32 v[82:83], v[82:83], v[120:121] neg_lo:[0,1] neg_hi:[0,1]
	s_waitcnt lgkmcnt(2)
	v_pk_add_f32 v[120:121], v[80:81], v[128:129]
	v_pk_add_f32 v[80:81], v[80:81], v[128:129] neg_lo:[0,1] neg_hi:[0,1]
	v_pk_add_f32 v[128:129], v[136:137], v[120:121]
	v_pk_add_f32 v[120:121], v[136:137], v[120:121] neg_lo:[0,1] neg_hi:[0,1]
	v_pk_fma_f32 v[136:137], v[80:81], s[28:29], v[82:83] op_sel:[1,0,0] op_sel_hi:[0,1,1]
	v_pk_fma_f32 v[80:81], v[80:81], s[26:27], v[82:83] op_sel:[1,0,0] op_sel_hi:[0,1,1]
	v_pk_add_f32 v[82:83], v[74:75], v[122:123]
	v_pk_add_f32 v[74:75], v[74:75], v[122:123] neg_lo:[0,1] neg_hi:[0,1]
	s_waitcnt lgkmcnt(1)
	v_pk_add_f32 v[122:123], v[114:115], v[130:131]
	v_pk_add_f32 v[114:115], v[114:115], v[130:131] neg_lo:[0,1] neg_hi:[0,1]
	v_pk_add_f32 v[130:131], v[82:83], v[122:123]
	v_pk_add_f32 v[82:83], v[82:83], v[122:123] neg_lo:[0,1] neg_hi:[0,1]
	v_pk_fma_f32 v[122:123], v[114:115], s[28:29], v[74:75] op_sel:[1,0,0] op_sel_hi:[0,1,1]
	v_pk_fma_f32 v[74:75], v[114:115], s[26:27], v[74:75] op_sel:[1,0,0] op_sel_hi:[0,1,1]
	v_pk_add_f32 v[114:115], v[76:77], v[124:125]
	v_pk_add_f32 v[76:77], v[76:77], v[124:125] neg_lo:[0,1] neg_hi:[0,1]
	v_pk_add_f32 v[124:125], v[116:117], v[132:133]
	v_pk_add_f32 v[116:117], v[116:117], v[132:133] neg_lo:[0,1] neg_hi:[0,1]
	v_pk_add_f32 v[132:133], v[114:115], v[124:125]
	v_pk_add_f32 v[114:115], v[114:115], v[124:125] neg_lo:[0,1] neg_hi:[0,1]
	v_pk_fma_f32 v[124:125], v[116:117], s[28:29], v[76:77] op_sel:[1,0,0] op_sel_hi:[0,1,1]
	v_pk_fma_f32 v[76:77], v[116:117], s[26:27], v[76:77] op_sel:[1,0,0] op_sel_hi:[0,1,1]
	v_pk_add_f32 v[116:117], v[78:79], v[126:127]
	v_pk_add_f32 v[78:79], v[78:79], v[126:127] neg_lo:[0,1] neg_hi:[0,1]
	s_waitcnt lgkmcnt(0)
	v_pk_add_f32 v[126:127], v[118:119], v[134:135]
	v_pk_add_f32 v[118:119], v[118:119], v[134:135] neg_lo:[0,1] neg_hi:[0,1]
	v_pk_add_f32 v[134:135], v[116:117], v[126:127]
	v_pk_add_f32 v[116:117], v[116:117], v[126:127] neg_lo:[0,1] neg_hi:[0,1]
	v_pk_fma_f32 v[126:127], v[118:119], s[28:29], v[78:79] op_sel:[1,0,0] op_sel_hi:[0,1,1]
	v_pk_fma_f32 v[78:79], v[118:119], s[26:27], v[78:79] op_sel:[1,0,0] op_sel_hi:[0,1,1]
	v_pk_mul_f32 v[118:119], v[122:123], s[56:57] op_sel_hi:[0,1]
	v_pk_fma_f32 v[118:119], v[122:123], s[0:1], v[118:119] op_sel:[1,0,0]
	v_pk_mul_f32 v[122:123], v[124:125], s[12:13] op_sel_hi:[0,1]
	v_pk_fma_f32 v[122:123], v[124:125], s[58:59], v[122:123] op_sel:[1,0,0] op_sel_hi:[1,0,1]
	v_pk_mul_f32 v[124:125], v[126:127], s[8:9] op_sel_hi:[0,1]
	v_pk_fma_f32 v[124:125], v[126:127], s[34:35], v[124:125] op_sel:[1,0,0]
	v_pk_mul_f32 v[126:127], v[82:83], s[12:13] op_sel_hi:[0,1]
	v_pk_fma_f32 v[82:83], v[82:83], s[58:59], v[126:127] op_sel:[1,0,0] op_sel_hi:[1,0,1]
	v_pk_mul_f32 v[126:127], v[114:115], s[18:19] op_sel_hi:[0,1]
	v_pk_fma_f32 v[114:115], v[114:115], s[60:61], v[126:127] op_sel:[1,0,0]
	v_pk_mul_f32 v[126:127], v[74:75], s[8:9] op_sel_hi:[0,1]
	v_pk_fma_f32 v[74:75], v[74:75], s[34:35], v[126:127] op_sel:[1,0,0]
	v_pk_mul_f32 v[126:127], v[78:79], s[38:39] op_sel_hi:[0,1]
	v_mul_f32_e32 v86, 0xbf3504f3, v116
	v_pk_fma_f32 v[78:79], v[78:79], s[30:31], v[126:127] op_sel:[1,0,0]
	v_pk_add_f32 v[126:127], v[128:129], v[132:133]
	v_pk_add_f32 v[128:129], v[128:129], v[132:133] neg_lo:[0,1] neg_hi:[0,1]
	v_pk_add_f32 v[132:133], v[130:131], v[134:135]
	v_pk_add_f32 v[130:131], v[130:131], v[134:135] neg_lo:[0,1] neg_hi:[0,1]
	v_pk_fma_f32 v[116:117], v[116:117], s[12:13], v[86:87] op_sel:[1,0,0] op_sel_hi:[1,1,0]
	v_mul_f32_e32 v86, 0xbf3504f3, v76
	v_pk_add_f32 v[134:135], v[126:127], v[132:133]
	v_pk_add_f32 v[126:127], v[126:127], v[132:133] neg_lo:[0,1] neg_hi:[0,1]
	v_pk_fma_f32 v[132:133], v[130:131], s[28:29], v[128:129] op_sel:[1,0,0] op_sel_hi:[0,1,1]
	v_pk_fma_f32 v[128:129], v[130:131], s[26:27], v[128:129] op_sel:[1,0,0] op_sel_hi:[0,1,1]
	v_pk_add_f32 v[130:131], v[136:137], v[122:123]
	v_pk_add_f32 v[122:123], v[136:137], v[122:123] neg_lo:[0,1] neg_hi:[0,1]
	v_pk_add_f32 v[136:137], v[118:119], v[124:125]
	v_pk_add_f32 v[118:119], v[118:119], v[124:125] neg_lo:[0,1] neg_hi:[0,1]
	v_pk_fma_f32 v[76:77], v[76:77], s[12:13], v[86:87] op_sel:[1,0,0] op_sel_hi:[1,1,0]
	v_pk_add_f32 v[124:125], v[130:131], v[136:137]
	v_pk_add_f32 v[130:131], v[130:131], v[136:137] neg_lo:[0,1] neg_hi:[0,1]
	v_pk_fma_f32 v[136:137], v[118:119], s[28:29], v[122:123] op_sel:[1,0,0] op_sel_hi:[0,1,1]
	v_pk_fma_f32 v[118:119], v[118:119], s[26:27], v[122:123] op_sel:[1,0,0] op_sel_hi:[0,1,1]
	v_pk_add_f32 v[122:123], v[120:121], v[114:115]
	v_pk_add_f32 v[114:115], v[120:121], v[114:115] neg_lo:[0,1] neg_hi:[0,1]
	v_pk_add_f32 v[120:121], v[82:83], v[116:117]
	v_pk_add_f32 v[82:83], v[82:83], v[116:117] neg_lo:[0,1] neg_hi:[0,1]
	v_pk_add_f32 v[116:117], v[122:123], v[120:121]
	v_pk_add_f32 v[120:121], v[122:123], v[120:121] neg_lo:[0,1] neg_hi:[0,1]
	v_pk_fma_f32 v[122:123], v[82:83], s[28:29], v[114:115] op_sel:[1,0,0] op_sel_hi:[0,1,1]
	v_pk_fma_f32 v[82:83], v[82:83], s[26:27], v[114:115] op_sel:[1,0,0] op_sel_hi:[0,1,1]
	v_pk_add_f32 v[114:115], v[80:81], v[76:77]
	v_pk_add_f32 v[76:77], v[80:81], v[76:77] neg_lo:[0,1] neg_hi:[0,1]
	v_pk_add_f32 v[80:81], v[74:75], v[78:79]
	v_pk_add_f32 v[74:75], v[74:75], v[78:79] neg_lo:[0,1] neg_hi:[0,1]
	v_pk_add_f32 v[78:79], v[114:115], v[80:81]
	v_pk_add_f32 v[80:81], v[114:115], v[80:81] neg_lo:[0,1] neg_hi:[0,1]
	v_pk_fma_f32 v[114:115], v[74:75], s[28:29], v[76:77] op_sel:[1,0,0] op_sel_hi:[0,1,1]
	v_pk_fma_f32 v[74:75], v[74:75], s[26:27], v[76:77] op_sel:[1,0,0] op_sel_hi:[0,1,1]
	v_pk_mul_f32 v[76:77], v[72:73], s[28:29]
	v_mov_b32_e32 v86, v73
	v_pk_fma_f32 v[138:139], v[86:87], v[76:77], v[138:139] op_sel:[0,1,0] op_sel_hi:[0,0,1]
	v_pk_mul_f32 v[142:143], v[138:139], s[28:29]
	v_pk_mul_f32 v[144:145], v[138:139], v[138:139] op_sel_hi:[1,0]
	v_pk_mul_f32 v[140:141], v[72:73], v[138:139] op_sel_hi:[1,0]
	v_pk_fma_f32 v[144:145], v[138:139], v[142:143], v[144:145] op_sel:[1,1,0] op_sel_hi:[1,0,1]
	v_pk_mul_f32 v[158:159], v[72:73], v[124:125] op_sel_hi:[1,0]
	v_pk_mul_f32 v[146:147], v[72:73], v[144:145] op_sel_hi:[1,0]
	v_pk_fma_f32 v[140:141], v[138:139], v[76:77], v[140:141] op_sel:[1,1,0] op_sel_hi:[1,0,1]
	v_pk_fma_f32 v[146:147], v[144:145], v[76:77], v[146:147] op_sel:[1,1,0] op_sel_hi:[1,0,1]
	v_pk_fma_f32 v[76:77], v[124:125], v[76:77], v[158:159] op_sel:[1,1,0] op_sel_hi:[1,0,1]
	v_pk_mul_f32 v[124:125], v[138:139], v[116:117] op_sel_hi:[1,0]
	v_pk_mul_f32 v[150:151], v[140:141], s[28:29]
	v_pk_fma_f32 v[116:117], v[116:117], v[142:143], v[124:125] op_sel:[1,1,0] op_sel_hi:[1,0,1]
	v_pk_mul_f32 v[124:125], v[140:141], v[78:79] op_sel_hi:[1,0]
	v_pk_mul_f32 v[148:149], v[138:139], v[144:145] op_sel_hi:[1,0]
	v_pk_mul_f32 v[154:155], v[144:145], s[28:29]
	v_pk_fma_f32 v[78:79], v[78:79], v[150:151], v[124:125] op_sel:[1,1,0] op_sel_hi:[1,0,1]
	v_pk_mul_f32 v[124:125], v[144:145], v[132:133] op_sel_hi:[1,0]
	v_pk_fma_f32 v[148:149], v[144:145], v[142:143], v[148:149] op_sel:[1,1,0] op_sel_hi:[1,0,1]
	v_pk_mul_f32 v[152:153], v[140:141], v[144:145] op_sel_hi:[1,0]
	v_pk_fma_f32 v[124:125], v[132:133], v[154:155], v[124:125] op_sel:[1,1,0] op_sel_hi:[1,0,1]
	v_pk_mul_f32 v[132:133], v[146:147], s[28:29]
	v_pk_mul_f32 v[142:143], v[146:147], v[136:137] op_sel_hi:[1,0]
	v_pk_fma_f32 v[152:153], v[144:145], v[150:151], v[152:153] op_sel:[1,1,0] op_sel_hi:[1,0,1]
	v_pk_mul_f32 v[156:157], v[144:145], v[144:145] op_sel_hi:[1,0]
	v_pk_fma_f32 v[132:133], v[136:137], v[132:133], v[142:143] op_sel:[1,1,0] op_sel_hi:[1,0,1]
	v_pk_mul_f32 v[136:137], v[148:149], s[28:29]
	v_pk_mul_f32 v[142:143], v[148:149], v[122:123] op_sel_hi:[1,0]
	v_pk_fma_f32 v[156:157], v[144:145], v[154:155], v[156:157] op_sel:[1,1,0] op_sel_hi:[1,0,1]
	v_pk_fma_f32 v[122:123], v[122:123], v[136:137], v[142:143] op_sel:[1,1,0] op_sel_hi:[1,0,1]
	v_pk_mul_f32 v[136:137], v[152:153], s[28:29]
	v_pk_mul_f32 v[142:143], v[152:153], v[114:115] op_sel_hi:[1,0]
	v_pk_mul_f32 v[72:73], v[72:73], v[156:157] op_sel_hi:[0,1]
	v_pk_fma_f32 v[114:115], v[114:115], v[136:137], v[142:143] op_sel:[1,1,0] op_sel_hi:[1,0,1]
	v_pk_mul_f32 v[136:137], v[156:157], s[28:29]
	v_pk_mul_f32 v[142:143], v[156:157], v[126:127] op_sel_hi:[1,0]
	v_pk_fma_f32 v[72:73], v[86:87], v[136:137], v[72:73] op_sel:[0,1,0] op_sel_hi:[0,0,1]
	v_pk_fma_f32 v[126:127], v[126:127], v[136:137], v[142:143] op_sel:[1,1,0] op_sel_hi:[1,0,1]
	v_pk_mul_f32 v[142:143], v[72:73], s[28:29]
	v_pk_mul_f32 v[72:73], v[72:73], v[130:131] op_sel_hi:[1,0]
	v_lshl_add_u32 v86, v162, 7, v160
	v_pk_fma_f32 v[72:73], v[130:131], v[142:143], v[72:73] op_sel:[1,1,0] op_sel_hi:[1,0,1]
	v_pk_mul_f32 v[130:131], v[138:139], v[156:157] op_sel_hi:[0,1]
	v_pk_fma_f32 v[130:131], v[138:139], v[136:137], v[130:131] op_sel:[1,1,0] op_sel_hi:[1,0,1]
	s_nop 0
	v_pk_mul_f32 v[138:139], v[130:131], s[28:29]
	v_pk_mul_f32 v[130:131], v[130:131], v[120:121] op_sel_hi:[1,0]
	s_nop 0
	v_pk_fma_f32 v[120:121], v[120:121], v[138:139], v[130:131] op_sel:[1,1,0] op_sel_hi:[1,0,1]
	v_pk_mul_f32 v[130:131], v[140:141], v[156:157] op_sel_hi:[0,1]
	v_pk_fma_f32 v[130:131], v[140:141], v[136:137], v[130:131] op_sel:[1,1,0] op_sel_hi:[1,0,1]
	s_nop 0
	v_pk_mul_f32 v[138:139], v[130:131], s[28:29]
	v_pk_mul_f32 v[130:131], v[130:131], v[80:81] op_sel_hi:[1,0]
	s_nop 0
	v_pk_fma_f32 v[80:81], v[80:81], v[138:139], v[130:131] op_sel:[1,1,0] op_sel_hi:[1,0,1]
	v_pk_mul_f32 v[130:131], v[144:145], v[156:157] op_sel_hi:[0,1]
	v_pk_fma_f32 v[130:131], v[144:145], v[136:137], v[130:131] op_sel:[1,1,0] op_sel_hi:[1,0,1]
	s_nop 0
	v_pk_mul_f32 v[138:139], v[130:131], s[28:29]
	v_pk_mul_f32 v[130:131], v[130:131], v[128:129] op_sel_hi:[1,0]
	s_nop 0
	v_pk_fma_f32 v[128:129], v[128:129], v[138:139], v[130:131] op_sel:[1,1,0] op_sel_hi:[1,0,1]
	v_pk_mul_f32 v[130:131], v[156:157], v[146:147] op_sel_hi:[1,0]
	s_nop 0
	v_pk_fma_f32 v[130:131], v[146:147], v[136:137], v[130:131] op_sel:[1,1,0] op_sel_hi:[1,0,1]
	s_nop 0
	v_pk_mul_f32 v[138:139], v[130:131], s[28:29]
	v_pk_mul_f32 v[130:131], v[130:131], v[118:119] op_sel_hi:[1,0]
	s_nop 0
	v_pk_fma_f32 v[118:119], v[118:119], v[138:139], v[130:131] op_sel:[1,1,0] op_sel_hi:[1,0,1]
	v_pk_mul_f32 v[130:131], v[156:157], v[148:149] op_sel_hi:[1,0]
	s_nop 0
	v_pk_fma_f32 v[130:131], v[148:149], v[136:137], v[130:131] op_sel:[1,1,0] op_sel_hi:[1,0,1]
	s_nop 0
	v_pk_mul_f32 v[138:139], v[130:131], s[28:29]
	v_pk_mul_f32 v[130:131], v[130:131], v[82:83] op_sel_hi:[1,0]
	s_nop 0
	v_pk_fma_f32 v[82:83], v[82:83], v[138:139], v[130:131] op_sel:[1,1,0] op_sel_hi:[1,0,1]
	v_pk_mul_f32 v[130:131], v[156:157], v[152:153] op_sel_hi:[1,0]
	s_nop 0
	v_pk_fma_f32 v[130:131], v[152:153], v[136:137], v[130:131] op_sel:[1,1,0] op_sel_hi:[1,0,1]
	s_nop 0
	v_pk_mul_f32 v[136:137], v[130:131], s[28:29]
	v_pk_mul_f32 v[130:131], v[130:131], v[74:75] op_sel_hi:[1,0]
	s_nop 0
	v_pk_fma_f32 v[74:75], v[74:75], v[136:137], v[130:131] op_sel:[1,1,0] op_sel_hi:[1,0,1]
	ds_write_b64 v161, v[134:135]
	ds_write2_b64 v163, v[76:77], v[116:117] offset0:17 offset1:34
	ds_write2_b64 v163, v[78:79], v[124:125] offset0:51 offset1:68
	ds_write2_b64 v163, v[132:133], v[122:123] offset0:85 offset1:102
	ds_write2_b64 v163, v[114:115], v[126:127] offset0:119 offset1:136
	ds_write2_b64 v163, v[72:73], v[120:121] offset0:153 offset1:170
	ds_write2_b64 v163, v[80:81], v[128:129] offset0:187 offset1:204
	ds_write2_b64 v163, v[118:119], v[82:83] offset0:221 offset1:238
	ds_write_b64 v163, v[74:75] offset:2040
	v_add_co_u32_e32 v72, vcc, s79, v96
	s_mov_b32 s79, 0x62705000
	s_nop 0
	v_addc_co_u32_e32 v73, vcc, 0, v97, vcc
	v_add_co_u32_e32 v74, vcc, s79, v96
	s_mov_b32 s79, 0x62706000
	s_nop 0
	v_addc_co_u32_e32 v75, vcc, 0, v97, vcc
	v_add_co_u32_e32 v76, vcc, s79, v96
	s_mov_b32 s79, 0x62707000
	s_nop 0
	v_addc_co_u32_e32 v77, vcc, 0, v97, vcc
	v_add_co_u32_e32 v78, vcc, s79, v96
	s_nop 1
	v_addc_co_u32_e32 v79, vcc, 0, v97, vcc
	global_load_dword v134, v[74:75], off offset:-4096
	global_load_dword v136, v[72:73], off offset:1024
	global_load_dword v137, v[72:73], off offset:2048
	global_load_dword v138, v[72:73], off offset:3072
	global_load_dword v139, v[74:75], off
	global_load_dword v140, v[76:77], off offset:1024
	global_load_dword v141, v[76:77], off offset:2048
	global_load_dword v142, v[76:77], off offset:3072
	global_load_dword v143, v[74:75], off offset:1024
	global_load_dword v144, v[74:75], off offset:2048
	global_load_dword v145, v[74:75], off offset:3072
	global_load_dword v146, v[78:79], off offset:-4096
	global_load_dword v147, v[78:79], off
	global_load_dword v148, v[78:79], off offset:1024
	global_load_dword v149, v[78:79], off offset:2048
	global_load_dword v150, v[78:79], off offset:3072
	s_waitcnt lgkmcnt(0)
	s_barrier
	ds_read2_b64 v[72:75], v86 offset1:1
	ds_read2_b64 v[76:79], v86 offset0:2 offset1:3
	ds_read2_b64 v[80:83], v86 offset0:8 offset1:9
	ds_read2_b64 v[114:117], v86 offset0:4 offset1:5
	ds_read2_b64 v[118:121], v86 offset0:6 offset1:7
	ds_read2_b64 v[122:125], v86 offset0:12 offset1:13
	ds_read2_b64 v[126:129], v86 offset0:10 offset1:11
	ds_read2_b64 v[130:133], v86 offset0:14 offset1:15
	s_waitcnt lgkmcnt(5)
	v_pk_add_f32 v[96:97], v[72:73], v[80:81]
	v_pk_add_f32 v[72:73], v[72:73], v[80:81] neg_lo:[0,1] neg_hi:[0,1]
	s_waitcnt lgkmcnt(2)
	v_pk_add_f32 v[80:81], v[114:115], v[122:123]
	v_pk_add_f32 v[114:115], v[114:115], v[122:123] neg_lo:[0,1] neg_hi:[0,1]
	v_pk_add_f32 v[122:123], v[96:97], v[80:81]
	v_pk_add_f32 v[80:81], v[96:97], v[80:81] neg_lo:[0,1] neg_hi:[0,1]
	v_pk_fma_f32 v[96:97], v[114:115], s[28:29], v[72:73] op_sel:[1,0,0] op_sel_hi:[0,1,1]
	v_pk_fma_f32 v[72:73], v[114:115], s[26:27], v[72:73] op_sel:[1,0,0] op_sel_hi:[0,1,1]
	v_pk_add_f32 v[114:115], v[74:75], v[82:83]
	v_pk_add_f32 v[74:75], v[74:75], v[82:83] neg_lo:[0,1] neg_hi:[0,1]
	v_pk_add_f32 v[82:83], v[116:117], v[124:125]
	v_pk_add_f32 v[116:117], v[116:117], v[124:125] neg_lo:[0,1] neg_hi:[0,1]
	v_pk_add_f32 v[124:125], v[114:115], v[82:83]
	v_pk_add_f32 v[82:83], v[114:115], v[82:83] neg_lo:[0,1] neg_hi:[0,1]
	v_pk_fma_f32 v[114:115], v[116:117], s[28:29], v[74:75] op_sel:[1,0,0] op_sel_hi:[0,1,1]
	v_pk_fma_f32 v[74:75], v[116:117], s[26:27], v[74:75] op_sel:[1,0,0] op_sel_hi:[0,1,1]
	s_waitcnt lgkmcnt(1)
	v_pk_add_f32 v[116:117], v[76:77], v[126:127]
	v_pk_add_f32 v[76:77], v[76:77], v[126:127] neg_lo:[0,1] neg_hi:[0,1]
	s_waitcnt lgkmcnt(0)
	v_pk_add_f32 v[126:127], v[118:119], v[130:131]
	v_pk_add_f32 v[118:119], v[118:119], v[130:131] neg_lo:[0,1] neg_hi:[0,1]
	v_pk_add_f32 v[130:131], v[116:117], v[126:127]
	v_pk_add_f32 v[116:117], v[116:117], v[126:127] neg_lo:[0,1] neg_hi:[0,1]
	v_pk_fma_f32 v[126:127], v[118:119], s[28:29], v[76:77] op_sel:[1,0,0] op_sel_hi:[0,1,1]
	v_pk_fma_f32 v[76:77], v[118:119], s[26:27], v[76:77] op_sel:[1,0,0] op_sel_hi:[0,1,1]
	v_pk_add_f32 v[118:119], v[78:79], v[128:129]
	v_pk_add_f32 v[78:79], v[78:79], v[128:129] neg_lo:[0,1] neg_hi:[0,1]
	v_pk_add_f32 v[128:129], v[120:121], v[132:133]
	v_pk_add_f32 v[120:121], v[120:121], v[132:133] neg_lo:[0,1] neg_hi:[0,1]
	v_pk_add_f32 v[132:133], v[118:119], v[128:129]
	v_pk_add_f32 v[118:119], v[118:119], v[128:129] neg_lo:[0,1] neg_hi:[0,1]
	v_pk_fma_f32 v[128:129], v[120:121], s[28:29], v[78:79] op_sel:[1,0,0] op_sel_hi:[0,1,1]
	v_pk_fma_f32 v[78:79], v[120:121], s[26:27], v[78:79] op_sel:[1,0,0] op_sel_hi:[0,1,1]
	v_pk_mul_f32 v[120:121], v[114:115], s[56:57] op_sel_hi:[0,1]
	v_pk_fma_f32 v[114:115], v[114:115], s[0:1], v[120:121] op_sel:[1,0,0]
	v_pk_mul_f32 v[120:121], v[126:127], s[12:13] op_sel_hi:[0,1]
	v_pk_fma_f32 v[120:121], v[126:127], s[58:59], v[120:121] op_sel:[1,0,0] op_sel_hi:[1,0,1]
	v_pk_mul_f32 v[126:127], v[128:129], s[8:9] op_sel_hi:[0,1]
	v_pk_fma_f32 v[126:127], v[128:129], s[34:35], v[126:127] op_sel:[1,0,0]
	v_pk_mul_f32 v[128:129], v[82:83], s[12:13] op_sel_hi:[0,1]
	v_pk_fma_f32 v[82:83], v[82:83], s[58:59], v[128:129] op_sel:[1,0,0] op_sel_hi:[1,0,1]
	v_pk_mul_f32 v[128:129], v[116:117], s[18:19] op_sel_hi:[0,1]
	v_pk_fma_f32 v[116:117], v[116:117], s[60:61], v[128:129] op_sel:[1,0,0]
	v_pk_mul_f32 v[128:129], v[74:75], s[8:9] op_sel_hi:[0,1]
	v_pk_fma_f32 v[74:75], v[74:75], s[34:35], v[128:129] op_sel:[1,0,0]
	v_pk_mul_f32 v[128:129], v[78:79], s[38:39] op_sel_hi:[0,1]
	v_mul_f32_e32 v86, 0xbf3504f3, v118
	v_pk_fma_f32 v[78:79], v[78:79], s[30:31], v[128:129] op_sel:[1,0,0]
	v_pk_add_f32 v[128:129], v[122:123], v[130:131]
	v_pk_add_f32 v[122:123], v[122:123], v[130:131] neg_lo:[0,1] neg_hi:[0,1]
	v_pk_add_f32 v[130:131], v[124:125], v[132:133]
	v_pk_add_f32 v[124:125], v[124:125], v[132:133] neg_lo:[0,1] neg_hi:[0,1]
	v_pk_fma_f32 v[118:119], v[118:119], s[12:13], v[86:87] op_sel:[1,0,0] op_sel_hi:[1,1,0]
	v_mul_f32_e32 v86, 0xbf3504f3, v76
	v_pk_add_f32 v[132:133], v[128:129], v[130:131]
	v_pk_add_f32 v[128:129], v[128:129], v[130:131] neg_lo:[0,1] neg_hi:[0,1]
	v_pk_fma_f32 v[130:131], v[124:125], s[28:29], v[122:123] op_sel:[1,0,0] op_sel_hi:[0,1,1]
	v_pk_fma_f32 v[122:123], v[124:125], s[26:27], v[122:123] op_sel:[1,0,0] op_sel_hi:[0,1,1]
	v_pk_add_f32 v[124:125], v[96:97], v[120:121]
	v_pk_add_f32 v[96:97], v[96:97], v[120:121] neg_lo:[0,1] neg_hi:[0,1]
	v_pk_add_f32 v[120:121], v[114:115], v[126:127]
	v_pk_add_f32 v[114:115], v[114:115], v[126:127] neg_lo:[0,1] neg_hi:[0,1]
	v_pk_fma_f32 v[76:77], v[76:77], s[12:13], v[86:87] op_sel:[1,0,0] op_sel_hi:[1,1,0]
	v_pk_add_f32 v[126:127], v[124:125], v[120:121]
	v_pk_add_f32 v[120:121], v[124:125], v[120:121] neg_lo:[0,1] neg_hi:[0,1]
	v_pk_fma_f32 v[124:125], v[114:115], s[28:29], v[96:97] op_sel:[1,0,0] op_sel_hi:[0,1,1]
	v_pk_fma_f32 v[96:97], v[114:115], s[26:27], v[96:97] op_sel:[1,0,0] op_sel_hi:[0,1,1]
	v_pk_add_f32 v[114:115], v[80:81], v[116:117]
	v_pk_add_f32 v[80:81], v[80:81], v[116:117] neg_lo:[0,1] neg_hi:[0,1]
	v_pk_add_f32 v[116:117], v[82:83], v[118:119]
	v_pk_add_f32 v[82:83], v[82:83], v[118:119] neg_lo:[0,1] neg_hi:[0,1]
	v_pk_add_f32 v[118:119], v[114:115], v[116:117]
	v_pk_add_f32 v[114:115], v[114:115], v[116:117] neg_lo:[0,1] neg_hi:[0,1]
	v_pk_fma_f32 v[116:117], v[82:83], s[28:29], v[80:81] op_sel:[1,0,0] op_sel_hi:[0,1,1]
	v_pk_fma_f32 v[80:81], v[82:83], s[26:27], v[80:81] op_sel:[1,0,0] op_sel_hi:[0,1,1]
	v_pk_add_f32 v[82:83], v[72:73], v[76:77]
	v_pk_add_f32 v[72:73], v[72:73], v[76:77] neg_lo:[0,1] neg_hi:[0,1]
	v_pk_add_f32 v[76:77], v[74:75], v[78:79]
	v_pk_add_f32 v[74:75], v[74:75], v[78:79] neg_lo:[0,1] neg_hi:[0,1]
	v_pk_add_f32 v[78:79], v[82:83], v[76:77]
	v_pk_add_f32 v[76:77], v[82:83], v[76:77] neg_lo:[0,1] neg_hi:[0,1]
	v_pk_fma_f32 v[82:83], v[74:75], s[28:29], v[72:73] op_sel:[1,0,0] op_sel_hi:[0,1,1]
	v_pk_fma_f32 v[72:73], v[74:75], s[26:27], v[72:73] op_sel:[1,0,0] op_sel_hi:[0,1,1]
	s_waitcnt vmcnt(15)
	v_lshlrev_b32_e32 v74, 16, v134
	v_and_b32_e32 v75, 0xffff0000, v134
	v_pk_mul_f32 v[134:135], v[74:75], s[28:29]
	v_pk_mul_f32 v[74:75], v[132:133], v[74:75] op_sel_hi:[0,1]
	v_pk_fma_f32 v[132:133], v[132:133], v[134:135], v[74:75] op_sel:[1,1,0] op_sel_hi:[1,0,1]
	s_waitcnt vmcnt(14)
	v_lshlrev_b32_e32 v74, 16, v136
	v_and_b32_e32 v75, 0xffff0000, v136
	v_pk_mul_f32 v[134:135], v[74:75], s[28:29]
	v_pk_mul_f32 v[74:75], v[126:127], v[74:75] op_sel_hi:[0,1]
	v_pk_fma_f32 v[126:127], v[126:127], v[134:135], v[74:75] op_sel:[1,1,0] op_sel_hi:[1,0,1]
	s_waitcnt vmcnt(13)
	v_lshlrev_b32_e32 v74, 16, v137
	v_and_b32_e32 v75, 0xffff0000, v137
	v_pk_mul_f32 v[134:135], v[74:75], s[28:29]
	v_pk_mul_f32 v[74:75], v[118:119], v[74:75] op_sel_hi:[0,1]
	v_pk_fma_f32 v[118:119], v[118:119], v[134:135], v[74:75] op_sel:[1,1,0] op_sel_hi:[1,0,1]
	s_waitcnt vmcnt(12)
	v_lshlrev_b32_e32 v74, 16, v138
	v_and_b32_e32 v75, 0xffff0000, v138
	v_pk_mul_f32 v[134:135], v[74:75], s[28:29]
	v_pk_mul_f32 v[74:75], v[78:79], v[74:75] op_sel_hi:[0,1]
	v_pk_fma_f32 v[78:79], v[78:79], v[134:135], v[74:75] op_sel:[1,1,0] op_sel_hi:[1,0,1]
	s_waitcnt vmcnt(11)
	v_lshlrev_b32_e32 v74, 16, v139
	v_and_b32_e32 v75, 0xffff0000, v139
	v_pk_mul_f32 v[134:135], v[74:75], s[28:29]
	v_pk_mul_f32 v[74:75], v[130:131], v[74:75] op_sel_hi:[0,1]
	v_pk_fma_f32 v[130:131], v[130:131], v[134:135], v[74:75] op_sel:[1,1,0] op_sel_hi:[1,0,1]
	s_waitcnt vmcnt(7)
	v_lshlrev_b32_e32 v74, 16, v143
	v_and_b32_e32 v75, 0xffff0000, v143
	v_pk_mul_f32 v[134:135], v[74:75], s[28:29]
	v_pk_mul_f32 v[74:75], v[124:125], v[74:75] op_sel_hi:[0,1]
	v_pk_fma_f32 v[124:125], v[124:125], v[134:135], v[74:75] op_sel:[1,1,0] op_sel_hi:[1,0,1]
	s_waitcnt vmcnt(6)
	v_lshlrev_b32_e32 v74, 16, v144
	v_and_b32_e32 v75, 0xffff0000, v144
	v_pk_mul_f32 v[134:135], v[74:75], s[28:29]
	v_pk_mul_f32 v[74:75], v[116:117], v[74:75] op_sel_hi:[0,1]
	v_pk_fma_f32 v[116:117], v[116:117], v[134:135], v[74:75] op_sel:[1,1,0] op_sel_hi:[1,0,1]
	s_waitcnt vmcnt(5)
	v_lshlrev_b32_e32 v74, 16, v145
	v_and_b32_e32 v75, 0xffff0000, v145
	v_pk_mul_f32 v[134:135], v[74:75], s[28:29]
	v_pk_mul_f32 v[74:75], v[82:83], v[74:75] op_sel_hi:[0,1]
	v_pk_fma_f32 v[82:83], v[82:83], v[134:135], v[74:75] op_sel:[1,1,0] op_sel_hi:[1,0,1]
	s_waitcnt vmcnt(4)
	v_lshlrev_b32_e32 v74, 16, v146
	v_and_b32_e32 v75, 0xffff0000, v146
	v_pk_mul_f32 v[134:135], v[74:75], s[28:29]
	v_pk_mul_f32 v[74:75], v[128:129], v[74:75] op_sel_hi:[0,1]
	v_pk_fma_f32 v[128:129], v[128:129], v[134:135], v[74:75] op_sel:[1,1,0] op_sel_hi:[1,0,1]
	v_lshlrev_b32_e32 v74, 16, v140
	v_and_b32_e32 v75, 0xffff0000, v140
	v_pk_mul_f32 v[134:135], v[74:75], s[28:29]
	v_pk_mul_f32 v[74:75], v[120:121], v[74:75] op_sel_hi:[0,1]
	v_pk_fma_f32 v[120:121], v[120:121], v[134:135], v[74:75] op_sel:[1,1,0] op_sel_hi:[1,0,1]
	v_lshlrev_b32_e32 v74, 16, v141
	v_and_b32_e32 v75, 0xffff0000, v141
	v_pk_mul_f32 v[134:135], v[74:75], s[28:29]
	v_pk_mul_f32 v[74:75], v[114:115], v[74:75] op_sel_hi:[0,1]
	v_pk_fma_f32 v[114:115], v[114:115], v[134:135], v[74:75] op_sel:[1,1,0] op_sel_hi:[1,0,1]
	v_lshlrev_b32_e32 v74, 16, v142
	v_and_b32_e32 v75, 0xffff0000, v142
	v_pk_mul_f32 v[134:135], v[74:75], s[28:29]
	v_pk_mul_f32 v[74:75], v[76:77], v[74:75] op_sel_hi:[0,1]
	v_pk_fma_f32 v[76:77], v[76:77], v[134:135], v[74:75] op_sel:[1,1,0] op_sel_hi:[1,0,1]
	s_waitcnt vmcnt(3)
	v_lshlrev_b32_e32 v74, 16, v147
	v_and_b32_e32 v75, 0xffff0000, v147
	v_pk_mul_f32 v[134:135], v[74:75], s[28:29]
	v_pk_mul_f32 v[74:75], v[122:123], v[74:75] op_sel_hi:[0,1]
	v_pk_fma_f32 v[122:123], v[122:123], v[134:135], v[74:75] op_sel:[1,1,0] op_sel_hi:[1,0,1]
	s_waitcnt vmcnt(2)
	v_lshlrev_b32_e32 v74, 16, v148
	v_and_b32_e32 v75, 0xffff0000, v148
	v_pk_mul_f32 v[134:135], v[74:75], s[28:29]
	v_pk_mul_f32 v[74:75], v[96:97], v[74:75] op_sel_hi:[0,1]
	v_pk_fma_f32 v[134:135], v[96:97], v[134:135], v[74:75] op_sel:[1,1,0] op_sel_hi:[1,0,1]
	s_waitcnt vmcnt(1)
	v_lshlrev_b32_e32 v74, 16, v149
	v_and_b32_e32 v75, 0xffff0000, v149
	v_pk_mul_f32 v[96:97], v[74:75], s[28:29]
	v_pk_mul_f32 v[74:75], v[80:81], v[74:75] op_sel_hi:[0,1]
	v_pk_fma_f32 v[80:81], v[80:81], v[96:97], v[74:75] op_sel:[1,1,0] op_sel_hi:[1,0,1]
	s_waitcnt vmcnt(0)
	v_lshlrev_b32_e32 v74, 16, v150
	v_and_b32_e32 v75, 0xffff0000, v150
	v_pk_add_f32 v[138:139], v[132:133], v[128:129]
	v_pk_add_f32 v[128:129], v[132:133], v[128:129] neg_lo:[0,1] neg_hi:[0,1]
	v_pk_add_f32 v[132:133], v[130:131], v[122:123]
	v_pk_add_f32 v[122:123], v[130:131], v[122:123] neg_lo:[0,1] neg_hi:[0,1]
	v_pk_mul_f32 v[96:97], v[74:75], s[28:29]
	v_pk_mul_f32 v[74:75], v[72:73], v[74:75] op_sel_hi:[0,1]
	v_pk_add_f32 v[130:131], v[138:139], v[132:133]
	v_pk_add_f32 v[132:133], v[138:139], v[132:133] neg_lo:[0,1] neg_hi:[0,1]
	v_pk_fma_f32 v[138:139], v[122:123], s[26:27], v[128:129] op_sel:[1,0,0] op_sel_hi:[0,1,1]
	v_pk_fma_f32 v[122:123], v[122:123], s[28:29], v[128:129] op_sel:[1,0,0] op_sel_hi:[0,1,1]
	v_pk_add_f32 v[128:129], v[126:127], v[120:121]
	v_pk_add_f32 v[120:121], v[126:127], v[120:121] neg_lo:[0,1] neg_hi:[0,1]
	v_pk_add_f32 v[126:127], v[124:125], v[134:135]
	v_pk_add_f32 v[124:125], v[124:125], v[134:135] neg_lo:[0,1] neg_hi:[0,1]
	v_pk_fma_f32 v[136:137], v[72:73], v[96:97], v[74:75] op_sel:[1,1,0] op_sel_hi:[1,0,1]
	v_pk_add_f32 v[134:135], v[128:129], v[126:127]
	v_pk_add_f32 v[126:127], v[128:129], v[126:127] neg_lo:[0,1] neg_hi:[0,1]
	v_pk_fma_f32 v[128:129], v[124:125], s[26:27], v[120:121] op_sel:[1,0,0] op_sel_hi:[0,1,1]
	v_pk_fma_f32 v[120:121], v[124:125], s[28:29], v[120:121] op_sel:[1,0,0] op_sel_hi:[0,1,1]
	v_pk_add_f32 v[124:125], v[118:119], v[114:115]
	v_pk_add_f32 v[114:115], v[118:119], v[114:115] neg_lo:[0,1] neg_hi:[0,1]
	v_pk_add_f32 v[118:119], v[116:117], v[80:81]
	v_pk_add_f32 v[80:81], v[116:117], v[80:81] neg_lo:[0,1] neg_hi:[0,1]
	v_pk_add_f32 v[116:117], v[124:125], v[118:119]
	v_pk_add_f32 v[118:119], v[124:125], v[118:119] neg_lo:[0,1] neg_hi:[0,1]
	v_pk_fma_f32 v[124:125], v[80:81], s[26:27], v[114:115] op_sel:[1,0,0] op_sel_hi:[0,1,1]
	v_pk_fma_f32 v[80:81], v[80:81], s[28:29], v[114:115] op_sel:[1,0,0] op_sel_hi:[0,1,1]
	v_pk_add_f32 v[114:115], v[78:79], v[76:77]
	v_pk_add_f32 v[76:77], v[78:79], v[76:77] neg_lo:[0,1] neg_hi:[0,1]
	v_pk_add_f32 v[78:79], v[82:83], v[136:137]
	v_pk_add_f32 v[82:83], v[82:83], v[136:137] neg_lo:[0,1] neg_hi:[0,1]
	v_pk_add_f32 v[136:137], v[114:115], v[78:79]
	v_pk_add_f32 v[78:79], v[114:115], v[78:79] neg_lo:[0,1] neg_hi:[0,1]
	v_pk_fma_f32 v[114:115], v[82:83], s[26:27], v[76:77] op_sel:[1,0,0] op_sel_hi:[0,1,1]
	v_pk_fma_f32 v[76:77], v[82:83], s[28:29], v[76:77] op_sel:[1,0,0] op_sel_hi:[0,1,1]
	v_pk_mul_f32 v[82:83], v[128:129], s[34:35] op_sel_hi:[0,1]
	s_mov_b32 s31, s34
	v_pk_fma_f32 v[82:83], v[128:129], s[30:31], v[82:83] op_sel:[1,0,0]
	v_pk_mul_f32 v[128:129], v[114:115], s[0:1] op_sel_hi:[0,1]
	s_mov_b32 s19, s27
	v_pk_fma_f32 v[114:115], v[114:115], s[38:39], v[128:129] op_sel:[1,0,0]
	v_pk_mul_f32 v[128:129], v[118:119], s[18:19] op_sel_hi:[0,1]
	s_mov_b32 s12, s26
	s_mov_b32 s13, s18
	v_pk_fma_f32 v[118:119], v[118:119], s[12:13], v[128:129] op_sel:[1,0,0]
	v_pk_mul_f32 v[128:129], v[78:79], s[36:37] op_sel_hi:[0,1]
	v_pk_fma_f32 v[78:79], v[78:79], s[36:37], v[128:129] op_sel:[1,0,0] op_sel_hi:[1,0,1]
	v_pk_mul_f32 v[128:129], v[120:121], s[0:1] op_sel_hi:[0,1]
	v_pk_fma_f32 v[120:121], v[120:121], s[38:39], v[128:129] op_sel:[1,0,0]
	v_pk_mul_f32 v[128:129], v[80:81], s[36:37] op_sel_hi:[0,1]
	s_mov_b32 s39, s30
	v_mul_f32_e32 v86, 0x3f3504f3, v124
	v_pk_fma_f32 v[80:81], v[80:81], s[36:37], v[128:129] op_sel:[1,0,0] op_sel_hi:[1,0,1]
	v_pk_mul_f32 v[128:129], v[76:77], s[38:39] op_sel_hi:[0,1]
	v_pk_fma_f32 v[124:125], v[124:125], s[36:37], v[86:87] op_sel:[1,0,0] op_sel_hi:[1,1,0]
	v_mul_f32_e32 v86, 0x3f3504f3, v126
	v_pk_fma_f32 v[76:77], v[76:77], s[8:9], v[128:129] op_sel:[1,0,0]
	v_pk_add_f32 v[128:129], v[130:131], v[116:117]
	v_pk_add_f32 v[116:117], v[130:131], v[116:117] neg_lo:[0,1] neg_hi:[0,1]
	v_pk_add_f32 v[130:131], v[134:135], v[136:137]
	v_pk_add_f32 v[134:135], v[134:135], v[136:137] neg_lo:[0,1] neg_hi:[0,1]
	v_pk_fma_f32 v[126:127], v[126:127], s[36:37], v[86:87] op_sel:[1,0,0] op_sel_hi:[1,1,0]
	v_pk_add_f32 v[136:137], v[128:129], v[130:131]
	v_pk_add_f32 v[128:129], v[128:129], v[130:131] neg_lo:[0,1] neg_hi:[0,1]
	v_pk_fma_f32 v[130:131], v[134:135], s[26:27], v[116:117] op_sel:[1,0,0] op_sel_hi:[0,1,1]
	v_pk_fma_f32 v[116:117], v[134:135], s[28:29], v[116:117] op_sel:[1,0,0] op_sel_hi:[0,1,1]
	v_pk_add_f32 v[134:135], v[138:139], v[124:125]
	v_pk_add_f32 v[124:125], v[138:139], v[124:125] neg_lo:[0,1] neg_hi:[0,1]
	v_pk_add_f32 v[138:139], v[82:83], v[114:115]
	v_pk_add_f32 v[82:83], v[82:83], v[114:115] neg_lo:[0,1] neg_hi:[0,1]
	v_pk_add_f32 v[114:115], v[134:135], v[138:139]
	v_pk_add_f32 v[134:135], v[134:135], v[138:139] neg_lo:[0,1] neg_hi:[0,1]
	v_pk_fma_f32 v[138:139], v[82:83], s[26:27], v[124:125] op_sel:[1,0,0] op_sel_hi:[0,1,1]
	v_pk_fma_f32 v[82:83], v[82:83], s[28:29], v[124:125] op_sel:[1,0,0] op_sel_hi:[0,1,1]
	v_pk_add_f32 v[124:125], v[132:133], v[118:119]
	v_pk_add_f32 v[118:119], v[132:133], v[118:119] neg_lo:[0,1] neg_hi:[0,1]
	v_pk_add_f32 v[132:133], v[126:127], v[78:79]
	v_pk_add_f32 v[78:79], v[126:127], v[78:79] neg_lo:[0,1] neg_hi:[0,1]
	v_mov_b32_e32 v96, v217
	v_mov_b32_e32 v72, v218
	v_mov_b32_e32 v74, v215
	v_mov_b32_e32 v97, v220
	v_mov_b32_e32 v73, v221
	v_pk_add_f32 v[126:127], v[124:125], v[132:133]
	v_pk_add_f32 v[124:125], v[124:125], v[132:133] neg_lo:[0,1] neg_hi:[0,1]
	v_pk_fma_f32 v[132:133], v[78:79], s[26:27], v[118:119] op_sel:[1,0,0] op_sel_hi:[0,1,1]
	v_pk_fma_f32 v[78:79], v[78:79], s[28:29], v[118:119] op_sel:[1,0,0] op_sel_hi:[0,1,1]
	v_pk_add_f32 v[118:119], v[122:123], v[80:81]
	v_pk_add_f32 v[80:81], v[122:123], v[80:81] neg_lo:[0,1] neg_hi:[0,1]
	v_pk_add_f32 v[122:123], v[120:121], v[76:77]
	v_pk_add_f32 v[76:77], v[120:121], v[76:77] neg_lo:[0,1] neg_hi:[0,1]
	v_pk_add_f32 v[120:121], v[118:119], v[122:123]
	v_pk_add_f32 v[118:119], v[118:119], v[122:123] neg_lo:[0,1] neg_hi:[0,1]
	v_pk_fma_f32 v[122:123], v[76:77], s[26:27], v[80:81] op_sel:[1,0,0] op_sel_hi:[0,1,1]
	v_pk_fma_f32 v[76:77], v[76:77], s[28:29], v[80:81] op_sel:[1,0,0] op_sel_hi:[0,1,1]
	v_lshlrev_b32_e32 v75, 3, v74
	v_lshlrev_b32_e32 v80, 7, v74
	v_add3_u32 v80, v219, v75, v80
	ds_write2_b64 v80, v[136:137], v[114:115] offset1:1
	ds_write2_b64 v80, v[126:127], v[120:121] offset0:2 offset1:3
	ds_write2_b64 v80, v[130:131], v[138:139] offset0:4 offset1:5
	ds_write2_b64 v80, v[132:133], v[122:123] offset0:6 offset1:7
	ds_write2_b64 v80, v[128:129], v[134:135] offset0:8 offset1:9
	ds_write2_b64 v80, v[124:125], v[118:119] offset0:10 offset1:11
	ds_write2_b64 v80, v[116:117], v[82:83] offset0:12 offset1:13
	ds_write2_b64 v80, v[78:79], v[76:77] offset0:14 offset1:15
	v_cndmask_b32_e64 v76, v211, v212, s[6:7]
	v_mul_f32_e32 v77, v76, v56
	v_mul_f32_e32 v60, v76, v60
	v_mov_b32_e32 v56, v87
	v_cvt_pk_fp8_f32 v56, v77, v60
	v_mul_f32_e32 v60, v76, v57
	v_mul_f32_e32 v61, v76, v61
	v_mov_b32_e32 v57, v87
	v_cvt_pk_fp8_f32 v57, v60, v61
	v_mul_f32_e32 v60, v76, v65
	v_mul_f32_e32 v61, v76, v69
	v_mul_f32_e32 v44, v76, v44
	v_cvt_pk_fp8_f32 v57, v60, v61 op_sel:[0,0,1]
	v_mul_f32_e32 v60, v76, v58
	v_mul_f32_e32 v61, v76, v62
	v_mov_b32_e32 v58, v87
	v_cvt_pk_fp8_f32 v58, v60, v61
	v_mul_f32_e32 v60, v76, v59
	v_mul_f32_e32 v61, v76, v63
	v_mov_b32_e32 v59, v87
	v_cvt_pk_fp8_f32 v59, v60, v61
	v_mul_f32_e32 v60, v76, v67
	v_mul_f32_e32 v61, v76, v71
	v_mul_f32_e32 v45, v76, v45
	v_cvt_pk_fp8_f32 v59, v60, v61 op_sel:[0,0,1]
	v_mul_f32_e32 v60, v76, v40
	v_mov_b32_e32 v40, v87
	v_cvt_pk_fp8_f32 v40, v60, v44
	v_mul_f32_e32 v44, v76, v41
	v_mov_b32_e32 v41, v87
	v_cvt_pk_fp8_f32 v41, v44, v45
	v_mul_f32_e32 v44, v76, v49
	v_mul_f32_e32 v45, v76, v53
	s_min_i32 s0, s78, s59
	v_cvt_pk_fp8_f32 v41, v44, v45 op_sel:[0,0,1]
	v_mul_f32_e32 v44, v76, v42
	v_mul_f32_e32 v45, v76, v46
	v_mov_b32_e32 v42, v87
	s_mul_i32 s0, s0, s3
	v_cvt_pk_fp8_f32 v42, v44, v45
	v_mul_f32_e32 v44, v76, v43
	v_mul_f32_e32 v45, v76, v47
	v_mov_b32_e32 v43, v87
	s_add_i32 s1, s0, s2
	v_cvt_pk_fp8_f32 v43, v44, v45
	s_mul_hi_i32 s0, s1, 0x2aaaaaab
	v_mul_f32_e32 v64, v76, v64
	v_mul_f32_e32 v68, v76, v68
	s_lshr_b32 s6, s0, 31
	s_ashr_i32 s0, s0, 7
	v_cvt_pk_fp8_f32 v56, v64, v68 op_sel:[0,0,1]
	v_mul_f32_e32 v62, v76, v66
	v_mul_f32_e32 v64, v76, v70
	v_mul_f32_e32 v48, v76, v48
	v_mul_f32_e32 v52, v76, v52
	s_add_i32 s6, s0, s6
	v_cvt_pk_fp8_f32 v58, v62, v64 op_sel:[0,0,1]
	v_cvt_pk_fp8_f32 v40, v48, v52 op_sel:[0,0,1]
	v_mul_f32_e32 v46, v76, v50
	v_mul_f32_e32 v48, v76, v54
	v_mul_f32_e32 v44, v76, v51
	v_mul_f32_e32 v45, v76, v55
	s_add_i32 s0, s6, 18
	s_mulk_i32 s6, 0x300
	v_cvt_pk_fp8_f32 v42, v46, v48 op_sel:[0,0,1]
	v_cvt_pk_fp8_f32 v43, v44, v45 op_sel:[0,0,1]
	s_sub_i32 s19, s1, s6
	s_cmpk_lt_i32 s19, 0x200
	s_cselect_b64 s[6:7], -1, 0
	s_cmpk_gt_i32 s19, 0x1ff
	s_mov_b64 s[56:57], -1
	s_waitcnt lgkmcnt(0)
	s_barrier
	ds_write_b128 v236, v[56:59]
	ds_write_b128 v237, v[40:43]
	s_cbranch_scc0 .LBB0_869
	s_load_dwordx2 s[8:9], s[14:15], 0x110
	s_ashr_i32 s1, s0, 31
	s_lshl_b64 s[56:57], s[0:1], 24
	s_mov_b32 s13, s18
	s_waitcnt lgkmcnt(0)
	s_add_u32 s8, s8, s56
	s_addc_u32 s9, s9, s57
	s_lshl_b32 s1, s19, 3
	s_and_b32 s1, s1, 0x7fffffc0
	s_add_i32 s12, s1, 0xfffff000
	s_mov_b64 s[56:57], 0

.LBB0_871:
	s_lshl_b64 s[12:13], s[12:13], 13
	s_add_u32 s0, s8, s12
	s_addc_u32 s9, s9, s13
	s_lshl_b32 s1, s19, s1
	s_and_b32 s1, s1, 0x700
	s_lshl_b32 s1, s1, 2
	s_add_u32 s8, s0, s1
	s_addc_u32 s9, s9, 0
	s_cmp_gt_i32 s78, s59
	s_cselect_b64 s[0:1], -1, 0
	v_cndmask_b32_e64 v40, v180, 0, s[0:1]
	s_and_b64 s[12:13], s[0:1], exec
	s_cselect_b32 s12, 0, 0x800
	v_lshlrev_b32_e32 v86, 2, v40
	v_lshl_add_u64 v[48:49], s[8:9], 0, v[86:87]
	v_mad_i64_i32 v[40:41], s[8:9], s12, v181, 0
	v_mad_i64_i32 v[42:43], s[8:9], s12, v182, 0
	v_lshl_add_u64 v[40:41], v[40:41], 2, v[48:49]
	v_lshl_add_u64 v[42:43], v[42:43], 2, v[48:49]
	global_load_dwordx4 v[56:59], v[40:41], off nt
	global_load_dwordx4 v[60:63], v[42:43], off nt
	v_mad_i64_i32 v[40:41], s[8:9], s12, v183, 0
	v_mad_i64_i32 v[42:43], s[8:9], s12, v184, 0
	v_lshl_add_u64 v[40:41], v[40:41], 2, v[48:49]
	v_lshl_add_u64 v[42:43], v[42:43], 2, v[48:49]
	global_load_dwordx4 v[64:67], v[40:41], off nt
	global_load_dwordx4 v[68:71], v[42:43], off nt
	v_mad_i64_i32 v[40:41], s[8:9], s12, v185, 0
	v_mad_i64_i32 v[42:43], s[8:9], s12, v186, 0
	v_mad_i64_i32 v[50:51], s[8:9], s12, v187, 0
	v_mad_i64_i32 v[52:53], s[8:9], s12, v188, 0
	v_lshl_add_u64 v[40:41], v[40:41], 2, v[48:49]
	v_lshl_add_u64 v[44:45], v[42:43], 2, v[48:49]
	v_lshl_add_u64 v[50:51], v[50:51], 2, v[48:49]
	v_lshl_add_u64 v[52:53], v[52:53], 2, v[48:49]
	global_load_dwordx4 v[40:43], v[40:41], off nt
	s_nop 0
	global_load_dwordx4 v[44:47], v[44:45], off nt
	s_nop 0
	global_load_dwordx4 v[48:51], v[50:51], off nt
	s_nop 0
	global_load_dwordx4 v[52:55], v[52:53], off nt
	s_cmp_gt_i32 s62, -2
	s_cselect_b32 s8, s76, 0
	s_min_i32 s8, s8, s59
	s_mul_i32 s8, s8, s3
	s_add_i32 s9, s8, s2
	s_mul_hi_i32 s8, s9, 0x2aaaaaab
	s_lshr_b32 s12, s8, 31
	s_ashr_i32 s8, s8, 7
	s_add_i32 s12, s8, s12
	s_add_i32 s8, s12, 18
	s_mulk_i32 s12, 0x300
	s_sub_i32 s19, s9, s12
	s_ashr_i32 s9, s8, 31
	s_cmpk_gt_i32 s19, 0x1ff
	s_mov_b64 s[56:57], -1
	s_cbranch_scc0 .LBB0_873
	s_lshl_b32 s12, s19, 3
	s_and_b32 s31, s12, 0x7fffffc0
	s_lshl_b32 s12, s19, 19
	s_and_b32 s39, s12, 0x380000
	s_lshl_b64 s[12:13], s[8:9], 22
	s_add_u32 s12, s16, s12
	s_addc_u32 s13, s17, s13
	s_add_u32 s12, s12, s39
	s_addc_u32 s13, s13, 0
	s_add_u32 s12, s12, s31
	s_addc_u32 s13, s13, 0
	s_add_u32 s12, s12, 0x24dff000
	s_addc_u32 s13, s13, 0
	s_mov_b64 s[56:57], 0

.LBB0_875:
	s_add_i32 s58, s62, 5
	s_cmp_lt_i32 s62, -1
	s_cselect_b64 s[8:9], -1, 0
	s_or_b64 s[8:9], s[8:9], s[54:55]
	s_and_b64 s[8:9], s[8:9], exec
	s_cselect_b32 s8, s65, s12
	s_cselect_b32 s12, 0x80, s31
	v_mul_i32_i24_e32 v76, s12, v191
	v_or_b32_e32 v76, v76, v189
	v_ashrrev_i32_e32 v77, 31, v76
	s_cselect_b32 s9, s66, s13
	v_lshlrev_b64 v[76:77], 11, v[76:77]
	v_lshl_add_u64 v[76:77], s[8:9], 0, v[76:77]
	v_lshl_add_u64 v[114:115], v[76:77], 0, v[88:89]
	ds_read_b32 v76, v235
	ds_read_b32 v77, v235 offset:1040
	ds_read_b32 v78, v235 offset:2080
	ds_read_b32 v79, v235 offset:3120
	ds_read_b32 v80, v238
	ds_read_b32 v81, v238 offset:1040
	ds_read_b32 v82, v238 offset:2080
	ds_read_b32 v83, v238 offset:3120
	s_waitcnt lgkmcnt(4)
	global_store_dwordx4 v[114:115], v[76:79], off
	v_pk_mul_f32 v[72:73], v[72:73], s[28:29]
	s_mov_b32 s31, s34
	v_mul_i32_i24_e32 v76, s12, v201
	v_or_b32_e32 v76, v76, v189
	v_ashrrev_i32_e32 v77, 31, v76
	v_lshlrev_b64 v[76:77], 11, v[76:77]
	v_lshl_add_u64 v[76:77], s[8:9], 0, v[76:77]
	v_lshl_add_u64 v[76:77], v[76:77], 0, v[88:89]
	s_waitcnt lgkmcnt(0)
	global_store_dwordx4 v[76:77], v[80:83], off
	v_ashrrev_i32_e32 v76, 4, v74
	v_lshlrev_b32_e32 v77, 8, v76
	v_pk_mul_f32 v[140:141], v[72:73], s[28:29]
	v_pk_mul_f32 v[142:143], v[72:73], v[72:73] op_sel_hi:[1,0]
	v_ashrrev_i32_e32 v77, 1, v77
	v_pk_fma_f32 v[142:143], v[72:73], v[140:141], v[142:143] op_sel:[1,1,0] op_sel_hi:[1,0,1]
	v_lshlrev_b32_e32 v79, 11, v76
	v_and_b32_e32 v80, 0x78, v75
	v_add_u32_e32 v77, v219, v77
	v_pk_mul_f32 v[146:147], v[142:143], s[28:29]
	v_pk_mul_f32 v[148:149], v[142:143], v[142:143] op_sel_hi:[1,0]
	v_lshl_add_u32 v78, v76, 7, v219
	v_add3_u32 v77, v77, v79, v80
	v_pk_fma_f32 v[148:149], v[142:143], v[146:147], v[148:149] op_sel:[1,1,0] op_sel_hi:[1,0,1]
	v_add3_u32 v164, v78, v79, v80
	ds_read2_b64 v[78:81], v77 offset0:17 offset1:34
	ds_read2_b64 v[114:117], v77 offset0:51 offset1:68
	ds_read2_b64 v[118:121], v77 offset0:85 offset1:102
	ds_read2_b64 v[122:125], v77 offset0:119 offset1:136
	ds_read2_b64 v[126:129], v77 offset0:153 offset1:170
	ds_read2_b64 v[130:133], v77 offset0:187 offset1:204
	ds_read2_b64 v[134:137], v77 offset0:221 offset1:238
	ds_read_b64 v[82:83], v164
	ds_read_b64 v[138:139], v77 offset:2040
	v_pk_mul_f32 v[144:145], v[72:73], v[142:143] op_sel_hi:[1,0]
	v_pk_mul_f32 v[150:151], v[72:73], v[148:149] op_sel_hi:[1,0]
	s_waitcnt lgkmcnt(8)
	v_pk_mul_f32 v[162:163], v[72:73], v[78:79] op_sel_hi:[1,0]
	v_pk_fma_f32 v[144:145], v[142:143], v[140:141], v[144:145] op_sel:[1,1,0] op_sel_hi:[1,0,1]
	v_pk_fma_f32 v[150:151], v[148:149], v[140:141], v[150:151] op_sel:[1,1,0] op_sel_hi:[1,0,1]
	v_pk_fma_f32 v[78:79], v[78:79], v[140:141], v[162:163] op_sel:[1,1,0] op_sel_hi:[1,0,1]
	v_pk_mul_f32 v[140:141], v[142:143], v[80:81] op_sel_hi:[1,0]
	v_pk_mul_f32 v[154:155], v[144:145], s[28:29]
	v_pk_fma_f32 v[80:81], v[80:81], v[146:147], v[140:141] op_sel:[1,1,0] op_sel_hi:[1,0,1]
	s_waitcnt lgkmcnt(7)
	v_pk_mul_f32 v[140:141], v[144:145], v[114:115] op_sel_hi:[1,0]
	v_pk_mul_f32 v[152:153], v[142:143], v[148:149] op_sel_hi:[1,0]
	v_pk_mul_f32 v[158:159], v[148:149], s[28:29]
	v_pk_fma_f32 v[114:115], v[114:115], v[154:155], v[140:141] op_sel:[1,1,0] op_sel_hi:[1,0,1]
	v_pk_mul_f32 v[140:141], v[148:149], v[116:117] op_sel_hi:[1,0]
	v_pk_fma_f32 v[152:153], v[148:149], v[146:147], v[152:153] op_sel:[1,1,0] op_sel_hi:[1,0,1]
	v_pk_mul_f32 v[156:157], v[144:145], v[148:149] op_sel_hi:[1,0]
	v_pk_fma_f32 v[116:117], v[116:117], v[158:159], v[140:141] op_sel:[1,1,0] op_sel_hi:[1,0,1]
	v_pk_mul_f32 v[140:141], v[150:151], s[28:29]
	s_waitcnt lgkmcnt(6)
	v_pk_mul_f32 v[146:147], v[150:151], v[118:119] op_sel_hi:[1,0]
	v_pk_fma_f32 v[156:157], v[148:149], v[154:155], v[156:157] op_sel:[1,1,0] op_sel_hi:[1,0,1]
	v_pk_mul_f32 v[160:161], v[148:149], v[148:149] op_sel_hi:[1,0]
	v_pk_fma_f32 v[118:119], v[118:119], v[140:141], v[146:147] op_sel:[1,1,0] op_sel_hi:[1,0,1]
	v_pk_mul_f32 v[140:141], v[152:153], s[28:29]
	v_pk_mul_f32 v[146:147], v[152:153], v[120:121] op_sel_hi:[1,0]
	v_pk_fma_f32 v[160:161], v[148:149], v[158:159], v[160:161] op_sel:[1,1,0] op_sel_hi:[1,0,1]
	v_pk_fma_f32 v[120:121], v[120:121], v[140:141], v[146:147] op_sel:[1,1,0] op_sel_hi:[1,0,1]
	v_pk_mul_f32 v[140:141], v[156:157], s[28:29]
	s_waitcnt lgkmcnt(5)
	v_pk_mul_f32 v[146:147], v[156:157], v[122:123] op_sel_hi:[1,0]
	s_mov_b32 s8, s35
	v_pk_fma_f32 v[122:123], v[122:123], v[140:141], v[146:147] op_sel:[1,1,0] op_sel_hi:[1,0,1]
	v_pk_mul_f32 v[140:141], v[160:161], s[28:29]
	v_pk_mul_f32 v[146:147], v[160:161], v[124:125] op_sel_hi:[1,0]
	s_mov_b32 s9, s34
	v_pk_fma_f32 v[124:125], v[124:125], v[140:141], v[146:147] op_sel:[1,1,0] op_sel_hi:[1,0,1]
	v_pk_mul_f32 v[146:147], v[72:73], v[160:161] op_sel_hi:[0,1]
	v_pk_fma_f32 v[72:73], v[72:73], v[140:141], v[146:147] op_sel:[1,1,0] op_sel_hi:[1,0,1]
	s_mov_b32 s39, s35
	v_pk_mul_f32 v[146:147], v[72:73], s[28:29]
	s_waitcnt lgkmcnt(4)
	v_pk_mul_f32 v[72:73], v[72:73], v[126:127] op_sel_hi:[1,0]
	s_mov_b32 s19, s27
	v_pk_fma_f32 v[72:73], v[126:127], v[146:147], v[72:73] op_sel:[1,1,0] op_sel_hi:[1,0,1]
	v_pk_mul_f32 v[126:127], v[142:143], v[160:161] op_sel_hi:[0,1]
	v_pk_fma_f32 v[126:127], v[142:143], v[140:141], v[126:127] op_sel:[1,1,0] op_sel_hi:[1,0,1]
	s_mov_b32 s12, s26
	v_pk_mul_f32 v[142:143], v[126:127], s[28:29]
	v_pk_mul_f32 v[126:127], v[126:127], v[128:129] op_sel_hi:[1,0]
	s_mov_b32 s13, s18
	v_pk_fma_f32 v[126:127], v[128:129], v[142:143], v[126:127] op_sel:[1,1,0] op_sel_hi:[1,0,1]
	v_pk_mul_f32 v[128:129], v[144:145], v[160:161] op_sel_hi:[0,1]
	v_pk_fma_f32 v[128:129], v[144:145], v[140:141], v[128:129] op_sel:[1,1,0] op_sel_hi:[1,0,1]
	s_mov_b64 s[56:57], -1
	v_pk_mul_f32 v[142:143], v[128:129], s[28:29]
	s_waitcnt lgkmcnt(3)
	v_pk_mul_f32 v[128:129], v[128:129], v[130:131] op_sel_hi:[1,0]
	s_nop 0
	v_pk_fma_f32 v[128:129], v[130:131], v[142:143], v[128:129] op_sel:[1,1,0] op_sel_hi:[1,0,1]
	v_pk_mul_f32 v[130:131], v[148:149], v[160:161] op_sel_hi:[0,1]
	v_pk_fma_f32 v[130:131], v[148:149], v[140:141], v[130:131] op_sel:[1,1,0] op_sel_hi:[1,0,1]
	s_nop 0
	v_pk_mul_f32 v[142:143], v[130:131], s[28:29]
	v_pk_mul_f32 v[130:131], v[130:131], v[132:133] op_sel_hi:[1,0]
	s_nop 0
	v_pk_fma_f32 v[130:131], v[132:133], v[142:143], v[130:131] op_sel:[1,1,0] op_sel_hi:[1,0,1]
	v_pk_mul_f32 v[132:133], v[160:161], v[150:151] op_sel_hi:[1,0]
	s_nop 0
	v_pk_fma_f32 v[132:133], v[150:151], v[140:141], v[132:133] op_sel:[1,1,0] op_sel_hi:[1,0,1]
	s_nop 0
	v_pk_mul_f32 v[142:143], v[132:133], s[28:29]
	s_waitcnt lgkmcnt(2)
	v_pk_mul_f32 v[132:133], v[132:133], v[134:135] op_sel_hi:[1,0]
	s_nop 0
	v_pk_fma_f32 v[132:133], v[134:135], v[142:143], v[132:133] op_sel:[1,1,0] op_sel_hi:[1,0,1]
	v_pk_mul_f32 v[134:135], v[160:161], v[152:153] op_sel_hi:[1,0]
	s_nop 0
	v_pk_fma_f32 v[134:135], v[152:153], v[140:141], v[134:135] op_sel:[1,1,0] op_sel_hi:[1,0,1]
	s_nop 0
	v_pk_mul_f32 v[142:143], v[134:135], s[28:29]
	v_pk_mul_f32 v[134:135], v[134:135], v[136:137] op_sel_hi:[1,0]
	s_nop 0
	v_pk_fma_f32 v[134:135], v[136:137], v[142:143], v[134:135] op_sel:[1,1,0] op_sel_hi:[1,0,1]
	v_pk_mul_f32 v[136:137], v[160:161], v[156:157] op_sel_hi:[1,0]
	s_nop 0
	v_pk_fma_f32 v[136:137], v[156:157], v[140:141], v[136:137] op_sel:[1,1,0] op_sel_hi:[1,0,1]
	s_nop 0
	v_pk_mul_f32 v[140:141], v[136:137], s[28:29]
	s_waitcnt lgkmcnt(0)
	v_pk_mul_f32 v[136:137], v[136:137], v[138:139] op_sel_hi:[1,0]
	s_nop 0
	v_pk_fma_f32 v[136:137], v[138:139], v[140:141], v[136:137] op_sel:[1,1,0] op_sel_hi:[1,0,1]
	v_pk_add_f32 v[138:139], v[82:83], v[124:125]
	v_pk_add_f32 v[82:83], v[82:83], v[124:125] neg_lo:[0,1] neg_hi:[0,1]
	v_pk_add_f32 v[124:125], v[116:117], v[130:131]
	v_pk_add_f32 v[116:117], v[116:117], v[130:131] neg_lo:[0,1] neg_hi:[0,1]
	v_pk_add_f32 v[130:131], v[138:139], v[124:125]
	v_pk_add_f32 v[124:125], v[138:139], v[124:125] neg_lo:[0,1] neg_hi:[0,1]
	v_pk_fma_f32 v[138:139], v[116:117], s[26:27], v[82:83] op_sel:[1,0,0] op_sel_hi:[0,1,1]
	v_pk_fma_f32 v[82:83], v[116:117], s[28:29], v[82:83] op_sel:[1,0,0] op_sel_hi:[0,1,1]
	v_pk_add_f32 v[116:117], v[78:79], v[72:73]
	v_pk_add_f32 v[72:73], v[78:79], v[72:73] neg_lo:[0,1] neg_hi:[0,1]
	v_pk_add_f32 v[78:79], v[118:119], v[132:133]
	v_pk_add_f32 v[118:119], v[118:119], v[132:133] neg_lo:[0,1] neg_hi:[0,1]
	v_pk_add_f32 v[132:133], v[116:117], v[78:79]
	v_pk_add_f32 v[78:79], v[116:117], v[78:79] neg_lo:[0,1] neg_hi:[0,1]
	v_pk_fma_f32 v[116:117], v[118:119], s[26:27], v[72:73] op_sel:[1,0,0] op_sel_hi:[0,1,1]
	v_pk_fma_f32 v[72:73], v[118:119], s[28:29], v[72:73] op_sel:[1,0,0] op_sel_hi:[0,1,1]
	v_pk_add_f32 v[118:119], v[80:81], v[126:127]
	v_pk_add_f32 v[80:81], v[80:81], v[126:127] neg_lo:[0,1] neg_hi:[0,1]
	v_pk_add_f32 v[126:127], v[120:121], v[134:135]
	v_pk_add_f32 v[120:121], v[120:121], v[134:135] neg_lo:[0,1] neg_hi:[0,1]
	v_pk_add_f32 v[134:135], v[118:119], v[126:127]
	v_pk_add_f32 v[118:119], v[118:119], v[126:127] neg_lo:[0,1] neg_hi:[0,1]
	v_pk_fma_f32 v[126:127], v[120:121], s[26:27], v[80:81] op_sel:[1,0,0] op_sel_hi:[0,1,1]
	v_pk_fma_f32 v[80:81], v[120:121], s[28:29], v[80:81] op_sel:[1,0,0] op_sel_hi:[0,1,1]
	v_pk_add_f32 v[120:121], v[114:115], v[128:129]
	v_pk_add_f32 v[114:115], v[114:115], v[128:129] neg_lo:[0,1] neg_hi:[0,1]
	v_pk_add_f32 v[128:129], v[122:123], v[136:137]
	v_pk_add_f32 v[122:123], v[122:123], v[136:137] neg_lo:[0,1] neg_hi:[0,1]
	v_pk_add_f32 v[136:137], v[120:121], v[128:129]
	v_pk_add_f32 v[120:121], v[120:121], v[128:129] neg_lo:[0,1] neg_hi:[0,1]
	v_pk_fma_f32 v[128:129], v[122:123], s[26:27], v[114:115] op_sel:[1,0,0] op_sel_hi:[0,1,1]
	v_pk_fma_f32 v[114:115], v[122:123], s[28:29], v[114:115] op_sel:[1,0,0] op_sel_hi:[0,1,1]
	v_pk_mul_f32 v[122:123], v[116:117], s[34:35] op_sel_hi:[0,1]
	v_mul_f32_e32 v86, 0x3f3504f3, v126
	v_pk_fma_f32 v[116:117], v[116:117], s[30:31], v[122:123] op_sel:[1,0,0]
	v_pk_fma_f32 v[122:123], v[126:127], s[36:37], v[86:87] op_sel:[1,0,0] op_sel_hi:[1,1,0]
	v_pk_mul_f32 v[126:127], v[128:129], s[8:9] op_sel_hi:[0,1]
	v_pk_fma_f32 v[126:127], v[128:129], s[38:39], v[126:127] op_sel:[1,0,0]
	v_pk_mul_f32 v[128:129], v[118:119], s[18:19] op_sel_hi:[0,1]
	v_pk_fma_f32 v[118:119], v[118:119], s[12:13], v[128:129] op_sel:[1,0,0]
	v_pk_mul_f32 v[128:129], v[120:121], s[36:37] op_sel_hi:[0,1]
	v_pk_fma_f32 v[120:121], v[120:121], s[36:37], v[128:129] op_sel:[1,0,0] op_sel_hi:[1,0,1]
	v_pk_mul_f32 v[128:129], v[72:73], s[8:9] op_sel_hi:[0,1]
	v_pk_fma_f32 v[72:73], v[72:73], s[38:39], v[128:129] op_sel:[1,0,0]
	v_pk_mul_f32 v[128:129], v[80:81], s[36:37] op_sel_hi:[0,1]
	s_mov_b32 s39, s30
	v_pk_fma_f32 v[80:81], v[80:81], s[36:37], v[128:129] op_sel:[1,0,0] op_sel_hi:[1,0,1]
	v_pk_mul_f32 v[128:129], v[114:115], s[38:39] op_sel_hi:[0,1]
	s_mov_b32 s9, s38
	v_mul_f32_e32 v86, 0x3f3504f3, v78
	v_pk_fma_f32 v[114:115], v[114:115], s[8:9], v[128:129] op_sel:[1,0,0]
	v_pk_add_f32 v[128:129], v[130:131], v[134:135]
	v_pk_add_f32 v[130:131], v[130:131], v[134:135] neg_lo:[0,1] neg_hi:[0,1]
	v_pk_add_f32 v[134:135], v[132:133], v[136:137]
	v_pk_add_f32 v[132:133], v[132:133], v[136:137] neg_lo:[0,1] neg_hi:[0,1]
	v_pk_fma_f32 v[78:79], v[78:79], s[36:37], v[86:87] op_sel:[1,0,0] op_sel_hi:[1,1,0]
	v_pk_add_f32 v[136:137], v[128:129], v[134:135]
	v_pk_add_f32 v[128:129], v[128:129], v[134:135] neg_lo:[0,1] neg_hi:[0,1]
	v_pk_fma_f32 v[134:135], v[132:133], s[26:27], v[130:131] op_sel:[1,0,0] op_sel_hi:[0,1,1]
	v_pk_fma_f32 v[130:131], v[132:133], s[28:29], v[130:131] op_sel:[1,0,0] op_sel_hi:[0,1,1]
	v_pk_add_f32 v[132:133], v[138:139], v[122:123]
	v_pk_add_f32 v[122:123], v[138:139], v[122:123] neg_lo:[0,1] neg_hi:[0,1]
	v_pk_add_f32 v[138:139], v[116:117], v[126:127]
	v_pk_add_f32 v[116:117], v[116:117], v[126:127] neg_lo:[0,1] neg_hi:[0,1]
	v_pk_add_f32 v[126:127], v[132:133], v[138:139]
	v_pk_add_f32 v[132:133], v[132:133], v[138:139] neg_lo:[0,1] neg_hi:[0,1]
	v_pk_fma_f32 v[138:139], v[116:117], s[26:27], v[122:123] op_sel:[1,0,0] op_sel_hi:[0,1,1]
	v_pk_fma_f32 v[116:117], v[116:117], s[28:29], v[122:123] op_sel:[1,0,0] op_sel_hi:[0,1,1]
	v_pk_add_f32 v[122:123], v[124:125], v[118:119]
	v_pk_add_f32 v[118:119], v[124:125], v[118:119] neg_lo:[0,1] neg_hi:[0,1]
	v_pk_add_f32 v[124:125], v[78:79], v[120:121]
	v_pk_add_f32 v[78:79], v[78:79], v[120:121] neg_lo:[0,1] neg_hi:[0,1]
	v_pk_add_f32 v[120:121], v[122:123], v[124:125]
	v_pk_add_f32 v[122:123], v[122:123], v[124:125] neg_lo:[0,1] neg_hi:[0,1]
	v_pk_fma_f32 v[124:125], v[78:79], s[26:27], v[118:119] op_sel:[1,0,0] op_sel_hi:[0,1,1]
	v_pk_fma_f32 v[78:79], v[78:79], s[28:29], v[118:119] op_sel:[1,0,0] op_sel_hi:[0,1,1]
	v_pk_add_f32 v[118:119], v[82:83], v[80:81]
	v_pk_add_f32 v[80:81], v[82:83], v[80:81] neg_lo:[0,1] neg_hi:[0,1]
	v_pk_add_f32 v[82:83], v[72:73], v[114:115]
	v_pk_add_f32 v[72:73], v[72:73], v[114:115] neg_lo:[0,1] neg_hi:[0,1]
	v_pk_add_f32 v[114:115], v[118:119], v[82:83]
	v_pk_add_f32 v[82:83], v[118:119], v[82:83] neg_lo:[0,1] neg_hi:[0,1]
	v_pk_fma_f32 v[118:119], v[72:73], s[26:27], v[80:81] op_sel:[1,0,0] op_sel_hi:[0,1,1]
	v_pk_fma_f32 v[72:73], v[72:73], s[28:29], v[80:81] op_sel:[1,0,0] op_sel_hi:[0,1,1]
	ds_write_b64 v164, v[136:137]
	ds_write2_b64 v77, v[126:127], v[120:121] offset0:17 offset1:34
	ds_write2_b64 v77, v[114:115], v[134:135] offset0:51 offset1:68
	ds_write2_b64 v77, v[138:139], v[124:125] offset0:85 offset1:102
	ds_write2_b64 v77, v[118:119], v[128:129] offset0:119 offset1:136
	ds_write2_b64 v77, v[132:133], v[122:123] offset0:153 offset1:170
	ds_write2_b64 v77, v[82:83], v[130:131] offset0:187 offset1:204
	ds_write2_b64 v77, v[116:117], v[78:79] offset0:221 offset1:238
	ds_write_b64 v77, v[72:73] offset:2040
	v_cndmask_b32_e64 v72, v211, v212, s[4:5]
	v_mul_f32_e32 v73, v72, v24
	v_mul_f32_e32 v28, v72, v28
	v_mov_b32_e32 v24, v87
	v_cvt_pk_fp8_f32 v24, v73, v28
	v_mul_f32_e32 v28, v72, v25
	v_mul_f32_e32 v29, v72, v29
	v_mov_b32_e32 v25, v87
	v_cvt_pk_fp8_f32 v25, v28, v29
	v_mul_f32_e32 v28, v72, v33
	v_mul_f32_e32 v29, v72, v37
	v_mul_f32_e32 v12, v72, v12
	v_cvt_pk_fp8_f32 v25, v28, v29 op_sel:[0,0,1]
	v_mul_f32_e32 v28, v72, v26
	v_mul_f32_e32 v29, v72, v30
	v_mov_b32_e32 v26, v87
	v_cvt_pk_fp8_f32 v26, v28, v29
	v_mul_f32_e32 v28, v72, v27
	v_mul_f32_e32 v29, v72, v31
	v_mov_b32_e32 v27, v87
	v_cvt_pk_fp8_f32 v27, v28, v29
	v_mul_f32_e32 v28, v72, v35
	v_mul_f32_e32 v29, v72, v39
	v_mul_f32_e32 v13, v72, v13
	v_cvt_pk_fp8_f32 v27, v28, v29 op_sel:[0,0,1]
	v_mul_f32_e32 v28, v72, v8
	v_mov_b32_e32 v8, v87
	v_cvt_pk_fp8_f32 v8, v28, v12
	v_mul_f32_e32 v12, v72, v9
	v_mov_b32_e32 v9, v87
	v_cvt_pk_fp8_f32 v9, v12, v13
	v_mul_f32_e32 v12, v72, v17
	v_mul_f32_e32 v13, v72, v21
	s_min_i32 s4, s58, s59
	v_cvt_pk_fp8_f32 v9, v12, v13 op_sel:[0,0,1]
	v_mul_f32_e32 v12, v72, v10
	v_mul_f32_e32 v13, v72, v14
	v_mov_b32_e32 v10, v87
	s_mul_i32 s4, s4, s3
	v_cvt_pk_fp8_f32 v10, v12, v13
	v_mul_f32_e32 v12, v72, v11
	v_mul_f32_e32 v13, v72, v15
	v_mov_b32_e32 v11, v87
	s_add_i32 s4, s4, s2
	v_cvt_pk_fp8_f32 v11, v12, v13
	s_mul_hi_i32 s5, s4, 0x2aaaaaab
	v_mul_f32_e32 v32, v72, v32
	v_mul_f32_e32 v36, v72, v36
	s_lshr_b32 s8, s5, 31
	s_ashr_i32 s5, s5, 7
	v_cvt_pk_fp8_f32 v24, v32, v36 op_sel:[0,0,1]
	v_mul_f32_e32 v30, v72, v34
	v_mul_f32_e32 v32, v72, v38
	v_mul_f32_e32 v16, v72, v16
	v_mul_f32_e32 v20, v72, v20
	s_add_i32 s5, s5, s8
	v_cvt_pk_fp8_f32 v26, v30, v32 op_sel:[0,0,1]
	v_cvt_pk_fp8_f32 v8, v16, v20 op_sel:[0,0,1]
	v_mul_f32_e32 v14, v72, v18
	v_mul_f32_e32 v16, v72, v22
	v_mul_f32_e32 v12, v72, v19
	v_mul_f32_e32 v13, v72, v23
	s_add_i32 s8, s5, 18
	s_mulk_i32 s5, 0x300
	v_cvt_pk_fp8_f32 v10, v14, v16 op_sel:[0,0,1]
	v_cvt_pk_fp8_f32 v11, v12, v13 op_sel:[0,0,1]
	s_sub_i32 s19, s4, s5
	s_cmpk_lt_i32 s19, 0x200
	s_cselect_b64 s[4:5], -1, 0
	s_cmpk_gt_i32 s19, 0x1ff
	s_waitcnt lgkmcnt(0)
	s_barrier
	ds_write_b128 v240, v[24:27]
	ds_write_b128 v241, v[8:11]
	s_cbranch_scc0 .LBB0_877
	s_load_dwordx2 s[12:13], s[14:15], 0x110
	s_ashr_i32 s9, s8, 31
	s_lshl_b64 s[56:57], s[8:9], 24
	s_mov_b32 s55, s18
	s_waitcnt lgkmcnt(0)
	s_add_u32 s12, s12, s56
	s_addc_u32 s13, s13, s57
	s_lshl_b32 s9, s19, 3
	s_and_b32 s9, s9, 0x7fffffc0
	s_add_i32 s54, s9, 0xfffff000
	s_mov_b64 s[56:57], 0

.LBB0_879:
	s_lshl_b64 s[54:55], s[54:55], 13
	s_add_u32 s8, s12, s54
	s_addc_u32 s12, s13, s55
	s_lshl_b32 s9, s19, s9
	s_and_b32 s9, s9, 0x700
	s_lshl_b32 s9, s9, 2
	s_add_u32 s8, s8, s9
	s_addc_u32 s9, s12, 0
	s_cmp_gt_i32 s58, s59
	s_cselect_b64 s[12:13], -1, 0
	v_cndmask_b32_e64 v8, v180, 0, s[12:13]
	s_and_b64 s[12:13], s[12:13], exec
	s_cselect_b32 s12, 0, 0x800
	v_lshlrev_b32_e32 v86, 2, v8
	v_lshl_add_u64 v[16:17], s[8:9], 0, v[86:87]
	v_mad_i64_i32 v[8:9], s[8:9], s12, v181, 0
	v_mad_i64_i32 v[10:11], s[8:9], s12, v182, 0
	v_lshl_add_u64 v[8:9], v[8:9], 2, v[16:17]
	v_lshl_add_u64 v[10:11], v[10:11], 2, v[16:17]
	global_load_dwordx4 v[24:27], v[8:9], off nt
	global_load_dwordx4 v[28:31], v[10:11], off nt
	v_mad_i64_i32 v[8:9], s[8:9], s12, v183, 0
	v_mad_i64_i32 v[10:11], s[8:9], s12, v184, 0
	v_lshl_add_u64 v[8:9], v[8:9], 2, v[16:17]
	v_lshl_add_u64 v[10:11], v[10:11], 2, v[16:17]
	global_load_dwordx4 v[32:35], v[8:9], off nt
	global_load_dwordx4 v[36:39], v[10:11], off nt
	v_mad_i64_i32 v[8:9], s[8:9], s12, v185, 0
	v_mad_i64_i32 v[10:11], s[8:9], s12, v186, 0
	v_mad_i64_i32 v[18:19], s[8:9], s12, v187, 0
	v_mad_i64_i32 v[20:21], s[8:9], s12, v188, 0
	v_lshl_add_u64 v[8:9], v[8:9], 2, v[16:17]
	v_lshl_add_u64 v[12:13], v[10:11], 2, v[16:17]
	v_lshl_add_u64 v[18:19], v[18:19], 2, v[16:17]
	v_lshl_add_u64 v[20:21], v[20:21], 2, v[16:17]
	global_load_dwordx4 v[8:11], v[8:9], off nt
	s_nop 0
	global_load_dwordx4 v[12:15], v[12:13], off nt
	s_nop 0
	global_load_dwordx4 v[16:19], v[18:19], off nt
	s_nop 0
	global_load_dwordx4 v[20:23], v[20:21], off nt
	s_cmp_gt_i32 s62, -3
	s_cselect_b32 s8, s33, 0
	s_min_i32 s8, s8, s59
	s_mul_i32 s8, s8, s3
	s_add_i32 s9, s8, s2
	s_mul_hi_i32 s8, s9, 0x2aaaaaab
	s_lshr_b32 s12, s8, 31
	s_ashr_i32 s8, s8, 7
	s_add_i32 s12, s8, s12
	s_add_i32 s8, s12, 18
	s_mulk_i32 s12, 0x300
	s_sub_i32 s19, s9, s12
	s_ashr_i32 s9, s8, 31
	s_cmpk_gt_i32 s19, 0x1ff
	s_mov_b64 s[54:55], -1
	s_cbranch_scc0 .LBB0_881
	s_lshl_b32 s12, s19, 3
	s_and_b32 s31, s12, 0x7fffffc0
	s_lshl_b32 s12, s19, 19
	s_and_b32 s33, s12, 0x380000
	s_lshl_b64 s[12:13], s[8:9], 22
	s_add_u32 s12, s16, s12
	s_addc_u32 s13, s17, s13
	s_add_u32 s12, s12, s33
	s_addc_u32 s13, s13, 0
	s_add_u32 s12, s12, s31
	s_addc_u32 s13, s13, 0
	s_add_u32 s12, s12, 0x24dff000
	s_addc_u32 s13, s13, 0
	s_mov_b64 s[54:55], 0

.LBB0_883:
	s_add_i32 s19, s62, 6
	s_cmp_lt_i32 s62, -2
	s_cselect_b64 s[8:9], -1, 0
	s_or_b64 s[8:9], s[8:9], s[50:51]
	s_and_b64 s[8:9], s[8:9], exec
	s_cselect_b32 s8, s65, s12
	s_cselect_b32 s12, 0x80, s31
	v_mul_i32_i24_e32 v72, s12, v191
	v_or_b32_e32 v72, v72, v189
	v_ashrrev_i32_e32 v73, 31, v72
	s_cselect_b32 s9, s66, s13
	v_lshlrev_b64 v[72:73], 11, v[72:73]
	v_lshl_add_u64 v[72:73], s[8:9], 0, v[72:73]
	v_lshl_add_u64 v[72:73], v[72:73], 0, v[88:89]
	ds_read_b32 v78, v239
	ds_read_b32 v79, v239 offset:1040
	ds_read_b32 v80, v239 offset:2080
	ds_read_b32 v81, v239 offset:3120
	ds_read_b32 v114, v242
	ds_read_b32 v115, v242 offset:1040
	ds_read_b32 v116, v242 offset:2080
	ds_read_b32 v117, v242 offset:3120
	s_waitcnt lgkmcnt(4)
	global_store_dwordx4 v[72:73], v[78:81], off
	v_mul_i32_i24_e32 v72, s12, v201
	v_or_b32_e32 v72, v72, v189
	v_ashrrev_i32_e32 v73, 31, v72
	v_lshlrev_b64 v[72:73], 11, v[72:73]
	v_lshl_add_u64 v[72:73], s[8:9], 0, v[72:73]
	v_lshl_add_u64 v[72:73], v[72:73], 0, v[88:89]
	s_waitcnt lgkmcnt(0)
	global_store_dwordx4 v[72:73], v[114:117], off
	v_lshlrev_b32_e32 v72, 3, v76
	v_add_u32_e32 v73, 0x100, v74
	v_add_u32_e32 v76, 0x200, v74
	v_add_u32_e32 v77, 0x300, v74
	v_ashrrev_i32_e32 v73, 4, v73
	v_ashrrev_i32_e32 v76, 4, v76
	v_ashrrev_i32_e32 v77, 4, v77
	v_add3_u32 v72, v219, v72, v75
	v_lshlrev_b32_e32 v73, 3, v73
	v_lshlrev_b32_e32 v76, 3, v76
	v_lshlrev_b32_e32 v77, 3, v77
	v_add3_u32 v73, v219, v73, v75
	v_add3_u32 v76, v219, v76, v75
	v_add3_u32 v77, v219, v77, v75
	ds_read_b64 v[114:115], v72
	ds_read_b64 v[128:129], v73 offset:2048
	ds_read_b64 v[120:121], v76 offset:4096
	ds_read_b64 v[130:131], v77 offset:6144
	v_add_u32_e32 v72, 0x400, v74
	v_ashrrev_i32_e32 v72, 4, v72
	v_add_u32_e32 v73, 0x500, v74
	v_add_u32_e32 v76, 0x600, v74
	v_add_u32_e32 v77, 0x700, v74
	v_lshlrev_b32_e32 v72, 3, v72
	v_ashrrev_i32_e32 v73, 4, v73
	v_ashrrev_i32_e32 v76, 4, v76
	v_ashrrev_i32_e32 v77, 4, v77
	v_add3_u32 v72, v219, v72, v75
	v_lshlrev_b32_e32 v73, 3, v73
	v_lshlrev_b32_e32 v76, 3, v76
	v_lshlrev_b32_e32 v77, 3, v77
	v_add3_u32 v73, v219, v73, v75
	v_add3_u32 v76, v219, v76, v75
	v_add3_u32 v77, v219, v77, v75
	ds_read_b64 v[116:117], v72 offset:8192
	ds_read_b64 v[136:137], v73 offset:10240
	ds_read_b64 v[124:125], v76 offset:12288
	ds_read_b64 v[134:135], v77 offset:14336
	v_add_u32_e32 v72, 0x800, v74
	v_ashrrev_i32_e32 v72, 4, v72
	v_add_u32_e32 v73, 0x900, v74
	v_add_u32_e32 v76, 0xa00, v74
	v_add_u32_e32 v77, 0xb00, v74
	v_lshlrev_b32_e32 v72, 3, v72
	v_ashrrev_i32_e32 v73, 4, v73
	v_ashrrev_i32_e32 v76, 4, v76
	v_ashrrev_i32_e32 v77, 4, v77
	v_add3_u32 v72, v219, v72, v75
	v_lshlrev_b32_e32 v73, 3, v73
	v_lshlrev_b32_e32 v76, 3, v76
	v_lshlrev_b32_e32 v77, 3, v77
	v_add3_u32 v73, v219, v73, v75
	v_add3_u32 v76, v219, v76, v75
	v_add3_u32 v77, v219, v77, v75
	ds_read_b64 v[118:119], v72 offset:16384
	ds_read_b64 v[140:141], v73 offset:18432
	ds_read_b64 v[126:127], v76 offset:20480
	ds_read_b64 v[138:139], v77 offset:22528
	v_add_u32_e32 v72, 0xc00, v74
	v_ashrrev_i32_e32 v72, 4, v72
	v_add_u32_e32 v73, 0xd00, v74
	v_add_u32_e32 v76, 0xe00, v74
	v_add_u32_e32 v74, 0xf00, v74
	v_lshlrev_b32_e32 v72, 3, v72
	v_ashrrev_i32_e32 v73, 4, v73
	v_ashrrev_i32_e32 v76, 4, v76
	v_ashrrev_i32_e32 v74, 4, v74
	v_add3_u32 v72, v219, v72, v75
	v_lshlrev_b32_e32 v73, 3, v73
	v_lshlrev_b32_e32 v76, 3, v76
	v_lshlrev_b32_e32 v74, 3, v74
	v_add3_u32 v73, v219, v73, v75
	v_add3_u32 v76, v219, v76, v75
	v_add3_u32 v74, v219, v74, v75
	ds_read_b64 v[122:123], v72 offset:24576
	ds_read_b64 v[144:145], v73 offset:26624
	ds_read_b64 v[132:133], v76 offset:28672
	ds_read_b64 v[142:143], v74 offset:30720
	v_cndmask_b32_e64 v72, v211, v212, s[6:7]
	s_waitcnt vmcnt(19)
	v_mul_f32_e32 v73, v72, v56
	s_waitcnt vmcnt(18)
	v_mul_f32_e32 v60, v72, v60
	v_mov_b32_e32 v56, v87
	v_cvt_pk_fp8_f32 v56, v73, v60
	v_mul_f32_e32 v60, v72, v57
	v_mul_f32_e32 v61, v72, v61
	v_mov_b32_e32 v57, v87
	v_cvt_pk_fp8_f32 v57, v60, v61
	s_waitcnt vmcnt(17)
	v_mul_f32_e32 v60, v72, v65
	s_waitcnt vmcnt(16)
	v_mul_f32_e32 v61, v72, v69
	s_waitcnt vmcnt(14)
	v_mul_f32_e32 v44, v72, v44
	v_cvt_pk_fp8_f32 v57, v60, v61 op_sel:[0,0,1]
	v_mul_f32_e32 v60, v72, v58
	v_mul_f32_e32 v61, v72, v62
	v_mov_b32_e32 v58, v87
	v_cvt_pk_fp8_f32 v58, v60, v61
	v_mul_f32_e32 v60, v72, v59
	v_mul_f32_e32 v61, v72, v63
	v_mov_b32_e32 v59, v87
	v_cvt_pk_fp8_f32 v59, v60, v61
	v_mul_f32_e32 v60, v72, v67
	v_mul_f32_e32 v61, v72, v71
	v_mul_f32_e32 v45, v72, v45
	v_cvt_pk_fp8_f32 v59, v60, v61 op_sel:[0,0,1]
	v_mul_f32_e32 v60, v72, v40
	v_mov_b32_e32 v40, v87
	v_cvt_pk_fp8_f32 v40, v60, v44
	v_mul_f32_e32 v44, v72, v41
	v_mov_b32_e32 v41, v87
	v_cvt_pk_fp8_f32 v41, v44, v45
	s_waitcnt vmcnt(13)
	v_mul_f32_e32 v44, v72, v49
	s_waitcnt vmcnt(12)
	v_mul_f32_e32 v45, v72, v53
	s_min_i32 s6, s19, s59
	v_cvt_pk_fp8_f32 v41, v44, v45 op_sel:[0,0,1]
	v_mul_f32_e32 v44, v72, v42
	v_mul_f32_e32 v45, v72, v46
	v_mov_b32_e32 v42, v87
	v_cvt_pk_fp8_f32 v42, v44, v45
	v_mul_f32_e32 v44, v72, v43
	v_mul_f32_e32 v45, v72, v47
	v_mov_b32_e32 v43, v87
	s_mul_i32 s6, s6, s3
	v_cvt_pk_fp8_f32 v43, v44, v45
	s_add_i32 s7, s6, s2
	v_mul_f32_e32 v64, v72, v64
	v_mul_f32_e32 v68, v72, v68
	s_mul_hi_i32 s6, s7, 0x2aaaaaab
	v_cvt_pk_fp8_f32 v56, v64, v68 op_sel:[0,0,1]
	v_mul_f32_e32 v62, v72, v66
	v_mul_f32_e32 v64, v72, v70
	v_mul_f32_e32 v48, v72, v48
	v_mul_f32_e32 v52, v72, v52
	s_lshr_b32 s8, s6, 31
	s_ashr_i32 s6, s6, 7
	v_cvt_pk_fp8_f32 v58, v62, v64 op_sel:[0,0,1]
	v_cvt_pk_fp8_f32 v40, v48, v52 op_sel:[0,0,1]
	v_mul_f32_e32 v46, v72, v50
	v_mul_f32_e32 v48, v72, v54
	v_mul_f32_e32 v44, v72, v51
	v_mul_f32_e32 v45, v72, v55
	s_add_i32 s8, s6, s8
	v_cvt_pk_fp8_f32 v42, v46, v48 op_sel:[0,0,1]
	v_cvt_pk_fp8_f32 v43, v44, v45 op_sel:[0,0,1]
	s_add_i32 s6, s8, 18
	s_mulk_i32 s8, 0x300
	s_sub_i32 s31, s7, s8
	s_cmpk_gt_i32 s31, 0x1ff
	s_mov_b64 s[50:51], -1
	s_waitcnt lgkmcnt(0)
	s_barrier
	ds_write_b128 v236, v[56:59]
	ds_write_b128 v237, v[40:43]
	s_cbranch_scc0 .LBB0_885
	s_load_dwordx2 s[8:9], s[14:15], 0x110
	s_ashr_i32 s7, s6, 31
	s_lshl_b64 s[50:51], s[6:7], 24
	s_mov_b32 s13, s18
	s_waitcnt lgkmcnt(0)
	s_add_u32 s8, s8, s50
	s_addc_u32 s9, s9, s51
	s_lshl_b32 s7, s31, 3
	s_and_b32 s7, s7, 0x7fffffc0
	s_add_i32 s12, s7, 0xfffff000
	s_mov_b64 s[50:51], 0

.LBB0_887:
	s_lshl_b64 s[12:13], s[12:13], 13
	s_add_u32 s6, s8, s12
	s_addc_u32 s8, s9, s13
	s_lshl_b32 s7, s31, s7
	s_and_b32 s7, s7, 0x700
	s_lshl_b32 s7, s7, 2
	s_add_u32 s6, s6, s7
	s_addc_u32 s7, s8, 0
	s_cmp_gt_i32 s19, s59
	s_cselect_b64 s[8:9], -1, 0
	v_cndmask_b32_e64 v40, v180, 0, s[8:9]
	s_and_b64 s[8:9], s[8:9], exec
	s_cselect_b32 s8, 0, 0x800
	v_lshlrev_b32_e32 v86, 2, v40
	v_lshl_add_u64 v[56:57], s[6:7], 0, v[86:87]
	v_mad_i64_i32 v[40:41], s[6:7], s8, v181, 0
	v_mad_i64_i32 v[42:43], s[6:7], s8, v182, 0
	v_lshl_add_u64 v[40:41], v[40:41], 2, v[56:57]
	v_lshl_add_u64 v[42:43], v[42:43], 2, v[56:57]
	global_load_dwordx4 v[48:51], v[40:41], off nt
	global_load_dwordx4 v[52:55], v[42:43], off nt
	v_mad_i64_i32 v[40:41], s[6:7], s8, v183, 0
	v_mad_i64_i32 v[42:43], s[6:7], s8, v184, 0
	v_lshl_add_u64 v[40:41], v[40:41], 2, v[56:57]
	v_lshl_add_u64 v[42:43], v[42:43], 2, v[56:57]
	global_load_dwordx4 v[64:67], v[40:41], off nt
	global_load_dwordx4 v[68:71], v[42:43], off nt
	v_mad_i64_i32 v[40:41], s[6:7], s8, v185, 0
	v_mad_i64_i32 v[42:43], s[6:7], s8, v186, 0
	v_mad_i64_i32 v[58:59], s[6:7], s8, v187, 0
	v_mad_i64_i32 v[60:61], s[6:7], s8, v188, 0
	v_lshl_add_u64 v[40:41], v[40:41], 2, v[56:57]
	v_lshl_add_u64 v[44:45], v[42:43], 2, v[56:57]
	v_lshl_add_u64 v[58:59], v[58:59], 2, v[56:57]
	v_lshl_add_u64 v[60:61], v[60:61], 2, v[56:57]
	global_load_dwordx4 v[40:43], v[40:41], off nt
	s_nop 0
	global_load_dwordx4 v[44:47], v[44:45], off nt
	s_nop 0
	global_load_dwordx4 v[56:59], v[58:59], off nt
	s_nop 0
	global_load_dwordx4 v[60:63], v[60:61], off nt
	s_cmp_gt_i32 s62, -4
	s_cselect_b32 s6, s77, 0
	s_min_i32 s6, s6, s59
	s_mul_i32 s6, s6, s3
	s_add_i32 s7, s6, s2
	s_mul_hi_i32 s6, s7, 0x2aaaaaab
	s_lshr_b32 s8, s6, 31
	s_ashr_i32 s6, s6, 7
	s_add_i32 s8, s6, s8
	s_add_i32 s6, s8, 18
	s_mulk_i32 s8, 0x300
	s_sub_i32 s19, s7, s8
	s_ashr_i32 s7, s6, 31
	s_cmpk_gt_i32 s19, 0x1ff
	s_mov_b64 s[12:13], -1
	s_cbranch_scc0 .LBB0_889
	s_lshl_b32 s8, s19, 3
	s_and_b32 s12, s8, 0x7fffffc0
	s_lshl_b32 s8, s19, 19
	s_and_b32 s13, s8, 0x380000
	s_lshl_b64 s[8:9], s[6:7], 22
	s_add_u32 s8, s16, s8
	s_addc_u32 s9, s17, s9
	s_add_u32 s8, s8, s13
	s_addc_u32 s9, s9, 0
	s_add_u32 s8, s8, s12
	s_addc_u32 s9, s9, 0
	s_add_u32 s8, s8, 0x24dff000
	s_addc_u32 s9, s9, 0
	s_mov_b64 s[12:13], 0

.LBB0_891:
	s_cmp_lt_i32 s62, -3
	s_cselect_b64 s[6:7], -1, 0
	s_or_b64 s[6:7], s[6:7], s[52:53]
	s_and_b64 s[6:7], s[6:7], exec
	s_cselect_b32 s6, s65, s8
	s_cselect_b32 s8, 0x80, s12
	v_mul_i32_i24_e32 v72, s8, v191
	v_or_b32_e32 v72, v72, v189
	v_ashrrev_i32_e32 v73, 31, v72
	s_cselect_b32 s7, s66, s9
	v_lshlrev_b64 v[72:73], 11, v[72:73]
	v_lshl_add_u64 v[72:73], s[6:7], 0, v[72:73]
	v_lshl_add_u64 v[80:81], v[72:73], 0, v[88:89]
	ds_read_b32 v72, v235
	ds_read_b32 v73, v235 offset:1040
	ds_read_b32 v74, v235 offset:2080
	ds_read_b32 v75, v235 offset:3120
	ds_read_b32 v76, v238
	ds_read_b32 v77, v238 offset:1040
	ds_read_b32 v78, v238 offset:2080
	ds_read_b32 v79, v238 offset:3120
	s_waitcnt lgkmcnt(4)
	global_store_dwordx4 v[80:81], v[72:75], off
	s_andn2_b64 vcc, exec, s[48:49]
	ds_write_b128 v234, v[0:3]
	v_mul_i32_i24_e32 v72, s8, v201
	v_or_b32_e32 v72, v72, v189
	v_ashrrev_i32_e32 v73, 31, v72
	v_lshlrev_b64 v[72:73], 11, v[72:73]
	v_lshl_add_u64 v[72:73], s[6:7], 0, v[72:73]
	v_lshl_add_u64 v[72:73], v[72:73], 0, v[88:89]
	s_waitcnt lgkmcnt(1)
	global_store_dwordx4 v[72:73], v[76:79], off
	ds_write_b128 v234, v[4:7] offset:4096
	s_cbranch_vccnz .LBB0_893
	v_add_co_u32_e32 v0, vcc, 0x45b02000, v84
	s_nop 1
	v_addc_co_u32_e32 v1, vcc, 0, v85, vcc
	v_add_co_u32_e32 v4, vcc, 0x46702000, v84
	s_nop 1
	v_addc_co_u32_e32 v5, vcc, 0, v85, vcc
	global_load_dwordx4 v[0:3], v[0:1], off
	s_nop 0
	global_load_dwordx4 v[4:7], v[4:5], off
.LBB0_893:
	v_cndmask_b32_e64 v72, v211, v212, s[4:5]
	s_waitcnt vmcnt(19)
	v_mul_f32_e32 v73, v72, v24
	s_waitcnt vmcnt(18)
	v_mul_f32_e32 v28, v72, v28
	v_mov_b32_e32 v24, v87
	v_cvt_pk_fp8_f32 v24, v73, v28
	v_mul_f32_e32 v28, v72, v25
	v_mul_f32_e32 v29, v72, v29
	v_mov_b32_e32 v25, v87
	v_cvt_pk_fp8_f32 v25, v28, v29
	s_waitcnt vmcnt(17)
	v_mul_f32_e32 v28, v72, v33
	s_waitcnt vmcnt(16)
	v_mul_f32_e32 v29, v72, v37
	s_waitcnt vmcnt(14)
	v_mul_f32_e32 v12, v72, v12
	v_cvt_pk_fp8_f32 v25, v28, v29 op_sel:[0,0,1]
	v_mul_f32_e32 v28, v72, v26
	v_mul_f32_e32 v29, v72, v30
	v_mov_b32_e32 v26, v87
	v_cvt_pk_fp8_f32 v26, v28, v29
	v_mul_f32_e32 v28, v72, v27
	v_mul_f32_e32 v29, v72, v31
	v_mov_b32_e32 v27, v87
	v_cvt_pk_fp8_f32 v27, v28, v29
	v_mul_f32_e32 v28, v72, v35
	v_mul_f32_e32 v29, v72, v39
	v_mul_f32_e32 v13, v72, v13
	v_cvt_pk_fp8_f32 v27, v28, v29 op_sel:[0,0,1]
	v_mul_f32_e32 v28, v72, v8
	v_mov_b32_e32 v8, v87
	v_cvt_pk_fp8_f32 v8, v28, v12
	v_mul_f32_e32 v12, v72, v9
	v_mov_b32_e32 v9, v87
	v_cvt_pk_fp8_f32 v9, v12, v13
	s_add_i32 s19, s62, 7
	s_waitcnt vmcnt(13)
	v_mul_f32_e32 v12, v72, v17
	s_waitcnt vmcnt(12)
	v_mul_f32_e32 v13, v72, v21
	v_cvt_pk_fp8_f32 v9, v12, v13 op_sel:[0,0,1]
	v_mul_f32_e32 v12, v72, v10
	v_mul_f32_e32 v13, v72, v14
	v_mov_b32_e32 v10, v87
	s_min_i32 s4, s19, s59
	v_cvt_pk_fp8_f32 v10, v12, v13
	v_mul_f32_e32 v12, v72, v11
	v_mul_f32_e32 v13, v72, v15
	v_mov_b32_e32 v11, v87
	s_mul_i32 s4, s4, s3
	v_cvt_pk_fp8_f32 v11, v12, v13
	s_add_i32 s5, s4, s2
	v_mul_f32_e32 v32, v72, v32
	v_mul_f32_e32 v36, v72, v36
	s_mul_hi_i32 s4, s5, 0x2aaaaaab
	v_cvt_pk_fp8_f32 v24, v32, v36 op_sel:[0,0,1]
	v_mul_f32_e32 v30, v72, v34
	v_mul_f32_e32 v32, v72, v38
	v_mul_f32_e32 v16, v72, v16
	v_mul_f32_e32 v20, v72, v20
	s_lshr_b32 s6, s4, 31
	s_ashr_i32 s4, s4, 7
	v_cvt_pk_fp8_f32 v26, v30, v32 op_sel:[0,0,1]
	v_cvt_pk_fp8_f32 v8, v16, v20 op_sel:[0,0,1]
	v_mul_f32_e32 v14, v72, v18
	v_mul_f32_e32 v16, v72, v22
	v_mul_f32_e32 v12, v72, v19
	v_mul_f32_e32 v13, v72, v23
	s_add_i32 s6, s4, s6
	v_cvt_pk_fp8_f32 v10, v14, v16 op_sel:[0,0,1]
	v_cvt_pk_fp8_f32 v11, v12, v13 op_sel:[0,0,1]
	s_add_i32 s4, s6, 18
	s_mulk_i32 s6, 0x300
	s_sub_i32 s31, s5, s6
	s_cmpk_gt_i32 s31, 0x1ff
	s_mov_b64 s[12:13], -1
	s_waitcnt lgkmcnt(0)
	s_barrier
	ds_write_b128 v240, v[24:27]
	ds_write_b128 v241, v[8:11]
	s_cbranch_scc0 .LBB0_895
	s_load_dwordx2 s[6:7], s[14:15], 0x110
	s_ashr_i32 s5, s4, 31
	s_lshl_b64 s[12:13], s[4:5], 24
	s_mov_b32 s9, s18
	s_waitcnt lgkmcnt(0)
	s_add_u32 s6, s6, s12
	s_addc_u32 s7, s7, s13
	s_lshl_b32 s5, s31, 3
	s_and_b32 s5, s5, 0x7fffffc0
	s_add_i32 s8, s5, 0xfffff000
	s_mov_b64 s[12:13], 0

.LBB0_897:
	s_lshl_b64 s[8:9], s[8:9], 13
	s_add_u32 s4, s6, s8
	s_addc_u32 s6, s7, s9
	s_lshl_b32 s5, s31, s5
	s_and_b32 s5, s5, 0x700
	s_lshl_b32 s5, s5, 2
	s_add_u32 s4, s4, s5
	s_addc_u32 s5, s6, 0
	s_cmp_gt_i32 s19, s59
	s_cselect_b64 s[6:7], -1, 0
	v_cndmask_b32_e64 v8, v180, 0, s[6:7]
	s_and_b64 s[6:7], s[6:7], exec
	s_cselect_b32 s6, 0, 0x800
	v_lshlrev_b32_e32 v86, 2, v8
	v_lshl_add_u64 v[24:25], s[4:5], 0, v[86:87]
	v_mad_i64_i32 v[8:9], s[4:5], s6, v181, 0
	v_mad_i64_i32 v[10:11], s[4:5], s6, v182, 0
	v_lshl_add_u64 v[8:9], v[8:9], 2, v[24:25]
	v_lshl_add_u64 v[10:11], v[10:11], 2, v[24:25]
	global_load_dwordx4 v[20:23], v[8:9], off nt
	global_load_dwordx4 v[16:19], v[10:11], off nt
	v_mad_i64_i32 v[8:9], s[4:5], s6, v183, 0
	v_mad_i64_i32 v[10:11], s[4:5], s6, v184, 0
	v_lshl_add_u64 v[8:9], v[8:9], 2, v[24:25]
	v_lshl_add_u64 v[10:11], v[10:11], 2, v[24:25]
	global_load_dwordx4 v[36:39], v[8:9], off nt
	global_load_dwordx4 v[32:35], v[10:11], off nt
	v_mad_i64_i32 v[8:9], s[4:5], s6, v185, 0
	v_mad_i64_i32 v[10:11], s[4:5], s6, v186, 0
	v_mad_i64_i32 v[26:27], s[4:5], s6, v187, 0
	v_mad_i64_i32 v[28:29], s[4:5], s6, v188, 0
	v_lshl_add_u64 v[8:9], v[8:9], 2, v[24:25]
	v_lshl_add_u64 v[10:11], v[10:11], 2, v[24:25]
	v_lshl_add_u64 v[26:27], v[26:27], 2, v[24:25]
	v_lshl_add_u64 v[24:25], v[28:29], 2, v[24:25]
	global_load_dwordx4 v[12:15], v[8:9], off nt
	s_nop 0
	global_load_dwordx4 v[8:11], v[10:11], off nt
	s_nop 0
	global_load_dwordx4 v[28:31], v[26:27], off nt
	s_nop 0
	global_load_dwordx4 v[24:27], v[24:25], off nt
	s_cmp_gt_i32 s62, -5
	s_cselect_b32 s4, s78, 0
	s_min_i32 s4, s4, s59
	s_mul_i32 s4, s4, s3
	s_add_i32 s5, s4, s2
	s_mul_hi_i32 s4, s5, 0x2aaaaaab
	s_lshr_b32 s6, s4, 31
	s_ashr_i32 s4, s4, 7
	s_add_i32 s6, s4, s6
	s_add_i32 s4, s6, 18
	s_mulk_i32 s6, 0x300
	s_sub_i32 s12, s5, s6
	s_ashr_i32 s5, s4, 31
	s_cmpk_gt_i32 s12, 0x1ff
	s_mov_b64 s[8:9], -1
	s_cbranch_scc0 .LBB0_899
	s_lshl_b32 s6, s12, 3
	s_and_b32 s8, s6, 0x7fffffc0
	s_lshl_b32 s6, s12, 19
	s_and_b32 s9, s6, 0x380000
	s_lshl_b64 s[6:7], s[4:5], 22
	s_add_u32 s6, s16, s6
	s_addc_u32 s7, s17, s7
	s_add_u32 s6, s6, s9
	s_addc_u32 s7, s7, 0
	s_add_u32 s6, s6, s8
	s_addc_u32 s7, s7, 0
	s_add_u32 s6, s6, 0x24dff000
	s_addc_u32 s7, s7, 0
	s_mov_b64 s[8:9], 0

.LBB0_901:
	s_cmp_lt_i32 s62, -4
	s_cselect_b64 s[4:5], -1, 0
	s_or_b64 s[0:1], s[4:5], s[0:1]
	s_and_b64 s[0:1], s[0:1], exec
	s_cselect_b32 s4, 0x80, s8
	v_mul_i32_i24_e32 v74, s4, v191
	ds_read_b32 v72, v239
	ds_read_b32 v73, v239 offset:1040
	v_or_b32_e32 v74, v74, v189
	v_ashrrev_i32_e32 v75, 31, v74
	s_cselect_b32 s1, s66, s7
	s_cselect_b32 s0, s65, s6
	v_lshlrev_b64 v[74:75], 11, v[74:75]
	v_lshl_add_u64 v[74:75], s[0:1], 0, v[74:75]
	v_lshl_add_u64 v[80:81], v[74:75], 0, v[88:89]
	ds_read_b32 v74, v239 offset:2080
	ds_read_b32 v75, v239 offset:3120
	ds_read_b32 v76, v242
	ds_read_b32 v77, v242 offset:1040
	ds_read_b32 v78, v242 offset:2080
	ds_read_b32 v79, v242 offset:3120
	ds_read_b96 v[84:86], v233 offset:96
	ds_read_b32 v146, v233 offset:116
	s_waitcnt lgkmcnt(6)
	global_store_dwordx4 v[80:81], v[72:75], off
	v_mov_b32_e32 v176, v215
	s_waitcnt lgkmcnt(0)
	v_mov_b32_e32 v147, v146
	v_mul_i32_i24_e32 v72, s4, v201
	v_or_b32_e32 v72, v72, v189
	v_ashrrev_i32_e32 v73, 31, v72
	v_lshlrev_b64 v[72:73], 11, v[72:73]
	v_lshl_add_u64 v[72:73], s[0:1], 0, v[72:73]
	v_lshl_add_u64 v[72:73], v[72:73], 0, v[88:89]
	global_store_dwordx4 v[72:73], v[76:79], off
	ds_read_b64 v[162:163], v233 offset:72
	ds_read_b128 v[72:75], v233 offset:80
	v_mov_b64_e32 v[156:157], v[146:147]
	v_lshlrev_b32_e32 v177, 3, v176
	v_ashrrev_i32_e32 v179, 3, v176
	v_and_b32_e32 v76, 56, v177
	v_cmp_ne_u32_e64 s[4:5], 0, v76
	v_cmp_ne_u32_e32 vcc, 56, v76
	v_add_u32_e32 v76, -1, v179
	v_lshl_add_u32 v178, v176, 4, v216
	v_cmp_gt_u32_e64 s[6:7], 32, v76
	v_mov_b64_e32 v[158:159], v[146:147]
	v_mov_b64_e32 v[160:161], v[146:147]
	v_mov_b64_e32 v[150:151], v[146:147]
	v_mov_b64_e32 v[148:149], v[146:147]
	v_mov_b64_e32 v[152:153], v[146:147]
	v_mov_b64_e32 v[154:155], v[146:147]
	s_and_saveexec_b64 s[0:1], s[6:7]
	s_cbranch_execz .LBB0_911
	v_add_u32_e32 v76, 0xffffff80, v178
	ds_read_b128 v[80:83], v76
	v_mov_b32_e32 v155, 0
	v_mov_b32_e32 v148, 0
	s_and_saveexec_b64 s[6:7], s[4:5]
	s_cbranch_execz .LBB0_904
	v_add_u32_e32 v76, 0xffffff7e, v178
	ds_read_u16 v76, v76
	s_waitcnt lgkmcnt(0)
	v_lshlrev_b32_e32 v148, 16, v76

.LBB0_936:
	s_or_b32 s9, s62, 1
	s_cmp_lt_i32 s62, 3
	s_cselect_b32 s0, 0x80, s8
	v_mul_i32_i24_e32 v0, s0, v191
	v_or_b32_e32 v0, v0, v189
	v_ashrrev_i32_e32 v1, 31, v0
	s_cselect_b32 s5, s20, s7
	s_cselect_b32 s4, s19, s6
	v_lshlrev_b64 v[4:5], 11, v[0:1]
	v_add_u32_e32 v3, v111, v190
	v_lshl_add_u64 v[4:5], s[4:5], 0, v[4:5]
	v_add_u32_e32 v6, v111, v108
	ds_read_b32 v0, v3
	ds_read_b32 v1, v3 offset:1040
	ds_read_b32 v2, v3 offset:2080
	ds_read_b32 v3, v3 offset:3120
	s_waitcnt lgkmcnt(9)
	ds_read_b32 v96, v6
	s_waitcnt lgkmcnt(9)
	ds_read_b32 v97, v6 offset:1040
	s_waitcnt lgkmcnt(9)
	ds_read_b32 v98, v6 offset:2080
	s_waitcnt lgkmcnt(9)
	ds_read_b32 v99, v6 offset:3120
	v_lshl_add_u64 v[4:5], v[4:5], 0, v[100:101]
	s_mov_b32 s62, s9
	s_waitcnt lgkmcnt(4)
	global_store_dwordx4 v[4:5], v[0:3], off
.LBB0_937:
	s_nop 1
	v_mul_i32_i24_e32 v0, s0, v109
	v_or_b32_e32 v0, v0, v189
	v_ashrrev_i32_e32 v1, 31, v0
	v_lshlrev_b64 v[0:1], 11, v[0:1]
	v_lshl_add_u64 v[0:1], s[4:5], 0, v[0:1]
	v_lshl_add_u64 v[0:1], v[0:1], 0, v[100:101]
	s_cmp_le_i32 s62, s12
	s_waitcnt lgkmcnt(0)
	global_store_dwordx4 v[0:1], v[96:99], off
	s_cbranch_scc0 .LBB0_958
.LBB0_938:
	s_add_i32 s4, s62, -2
	s_min_i32 s4, s4, s59
	s_mul_i32 s4, s4, s3
	s_add_i32 s4, s4, s2
	s_mul_hi_i32 s5, s4, 0x2aaaaaab
	s_lshr_b32 s6, s5, 31
	s_lshr_b32 s5, s5, 7
	s_add_i32 s5, s5, s6
	s_mulk_i32 s5, 0x300
	s_and_b32 s0, s62, 1
	s_sub_i32 s4, s4, s5
	s_cmpk_lt_i32 s4, 0x200
	s_cselect_b64 vcc, -1, 0
	s_cmp_eq_u32 s0, 0
	v_cndmask_b32_e32 v114, v112, v113, vcc
	s_mov_b64 s[6:7], -1
	s_barrier
	s_cbranch_scc1 .LBB0_948
	s_waitcnt vmcnt(7)
	v_mul_f32_e32 v1, v114, v20
	s_waitcnt vmcnt(6)
	v_mul_f32_e32 v2, v114, v16
	v_mov_b32_e32 v0, v103
	v_cvt_pk_fp8_f32 v0, v1, v2
	v_mul_f32_e32 v2, v114, v21
	v_mul_f32_e32 v5, v114, v17
	v_mov_b32_e32 v1, v103
	v_cvt_pk_fp8_f32 v1, v2, v5
	s_waitcnt vmcnt(5)
	v_mul_f32_e32 v3, v114, v36
	s_waitcnt vmcnt(4)
	v_mul_f32_e32 v4, v114, v32
	v_cvt_pk_fp8_f32 v0, v3, v4 op_sel:[0,0,1]
	v_mul_f32_e32 v2, v114, v37
	v_mul_f32_e32 v3, v114, v33
	v_cvt_pk_fp8_f32 v1, v2, v3 op_sel:[0,0,1]
	v_mul_f32_e32 v3, v114, v22
	v_mul_f32_e32 v4, v114, v18
	v_mov_b32_e32 v2, v103
	v_cvt_pk_fp8_f32 v2, v3, v4
	v_mul_f32_e32 v4, v114, v23
	v_mul_f32_e32 v7, v114, v19
	v_mov_b32_e32 v3, v103
	v_cvt_pk_fp8_f32 v3, v4, v7
	v_mul_f32_e32 v5, v114, v38
	v_mul_f32_e32 v6, v114, v34
	v_cvt_pk_fp8_f32 v2, v5, v6 op_sel:[0,0,1]
	v_mul_f32_e32 v4, v114, v39
	v_mul_f32_e32 v5, v114, v35
	v_cvt_pk_fp8_f32 v3, v4, v5 op_sel:[0,0,1]
	s_waitcnt vmcnt(3)
	v_mul_f32_e32 v5, v114, v12
	s_waitcnt vmcnt(2)
	v_mul_f32_e32 v6, v114, v8
	v_mov_b32_e32 v4, v103
	v_cvt_pk_fp8_f32 v4, v5, v6
	v_mul_f32_e32 v6, v114, v13
	v_mul_f32_e32 v73, v114, v9
	v_mov_b32_e32 v5, v103
	v_cvt_pk_fp8_f32 v5, v6, v73
	s_waitcnt vmcnt(1)
	v_mul_f32_e32 v7, v114, v28
	s_waitcnt vmcnt(0)
	v_mul_f32_e32 v72, v114, v24
	v_cvt_pk_fp8_f32 v4, v7, v72 op_sel:[0,0,1]
	v_mul_f32_e32 v6, v114, v29
	v_mul_f32_e32 v7, v114, v25
	v_cvt_pk_fp8_f32 v5, v6, v7 op_sel:[0,0,1]
	v_mul_f32_e32 v7, v114, v14
	v_mul_f32_e32 v72, v114, v10
	v_mov_b32_e32 v6, v103
	v_cvt_pk_fp8_f32 v6, v7, v72
	v_mul_f32_e32 v72, v114, v15
	v_mul_f32_e32 v75, v114, v11
	v_mov_b32_e32 v7, v103
	s_min_i32 s0, s62, s59
	v_cvt_pk_fp8_f32 v7, v72, v75
	s_mul_i32 s0, s0, s3
	s_add_i32 s0, s0, s2
	v_mul_f32_e32 v73, v114, v30
	v_mul_f32_e32 v74, v114, v26
	s_mul_hi_i32 s4, s0, 0x2aaaaaab
	v_cvt_pk_fp8_f32 v6, v73, v74 op_sel:[0,0,1]
	v_mul_f32_e32 v72, v114, v31
	v_mul_f32_e32 v73, v114, v27
	s_lshr_b32 s5, s4, 31
	s_ashr_i32 s4, s4, 7
	v_cvt_pk_fp8_f32 v7, v72, v73 op_sel:[0,0,1]
	s_add_i32 s5, s4, s5
	s_add_i32 s4, s5, 18
	s_mulk_i32 s5, 0x300
	v_add_u32_e32 v72, v104, v105
	s_sub_i32 s22, s0, s5
	ds_write_b128 v72, v[0:3]
	v_add_u32_e32 v0, v104, v106
	s_cmpk_gt_i32 s22, 0x1ff
	s_mov_b64 s[10:11], -1
	ds_write_b128 v0, v[4:7]
	s_cbranch_scc0 .LBB0_941
	s_load_dwordx2 s[6:7], s[14:15], 0x110
	s_ashr_i32 s5, s4, 31
	s_lshl_b64 s[8:9], s[4:5], 24
	s_mov_b64 s[10:11], 0
	s_waitcnt lgkmcnt(0)
	s_add_u32 s6, s6, s8
	s_addc_u32 s7, s7, s9
	s_lshl_b32 s0, s22, 3
	s_and_b32 s0, s0, 0x7fffffc0
	s_addk_i32 s0, 0xf000
	s_mov_b64 s[8:9], s[0:1]

.LBB0_943:
	s_lshl_b64 s[4:5], s[8:9], 13
	s_add_u32 s4, s6, s4
	s_addc_u32 s5, s7, s5
	s_lshl_b32 s0, s22, s0
	s_and_b32 s0, s0, 0x700
	s_lshl_b32 s0, s0, 2
	s_add_u32 s4, s4, s0
	s_addc_u32 s5, s5, 0
	s_cmp_gt_i32 s62, s59
	s_cselect_b64 s[6:7], -1, 0
	v_cndmask_b32_e64 v0, v180, 0, s[6:7]
	s_and_b64 s[6:7], s[6:7], exec
	s_cselect_b32 s0, 0, 0x800
	v_lshlrev_b32_e32 v102, 2, v0
	v_lshl_add_u64 v[88:89], s[4:5], 0, v[102:103]
	v_mad_i64_i32 v[0:1], s[4:5], s0, v181, 0
	v_lshl_add_u64 v[72:73], v[0:1], 2, v[88:89]
	v_mad_i64_i32 v[0:1], s[4:5], s0, v182, 0
	v_lshl_add_u64 v[74:75], v[0:1], 2, v[88:89]
	global_load_dwordx4 v[0:3], v[72:73], off nt
	global_load_dwordx4 v[4:7], v[74:75], off nt
	v_mad_i64_i32 v[72:73], s[4:5], s0, v183, 0
	v_lshl_add_u64 v[80:81], v[72:73], 2, v[88:89]
	v_mad_i64_i32 v[72:73], s[4:5], s0, v184, 0
	v_lshl_add_u64 v[82:83], v[72:73], 2, v[88:89]
	global_load_dwordx4 v[72:75], v[80:81], off nt
	global_load_dwordx4 v[76:79], v[82:83], off nt
	v_mad_i64_i32 v[80:81], s[4:5], s0, v185, 0
	v_lshl_add_u64 v[90:91], v[80:81], 2, v[88:89]
	v_mad_i64_i32 v[80:81], s[4:5], s0, v186, 0
	v_lshl_add_u64 v[92:93], v[80:81], 2, v[88:89]
	global_load_dwordx4 v[80:83], v[90:91], off nt
	global_load_dwordx4 v[84:87], v[92:93], off nt
	v_mad_i64_i32 v[90:91], s[4:5], s0, v187, 0
	v_lshl_add_u64 v[96:97], v[90:91], 2, v[88:89]
	v_mad_i64_i32 v[90:91], s[4:5], s0, v188, 0
	v_lshl_add_u64 v[98:99], v[90:91], 2, v[88:89]
	global_load_dwordx4 v[88:91], v[96:97], off nt
	global_load_dwordx4 v[92:95], v[98:99], off nt
	s_max_i32 s0, s62, 3
	s_add_i32 s0, s0, -3
	s_min_i32 s0, s0, s59
	s_mul_i32 s0, s0, s3
	s_add_i32 s0, s0, s2
	s_mul_hi_i32 s4, s0, 0x2aaaaaab
	s_lshr_b32 s5, s4, 31
	s_ashr_i32 s4, s4, 7
	s_add_i32 s5, s4, s5
	s_add_i32 s4, s5, 18
	s_mulk_i32 s5, 0x300
	s_sub_i32 s0, s0, s5
	s_ashr_i32 s5, s4, 31
	s_cmpk_gt_i32 s0, 0x1ff
	s_mov_b64 s[8:9], -1
	s_cbranch_scc0 .LBB0_945
	s_lshl_b32 s6, s0, 3
	s_and_b32 s8, s6, 0x7fffffc0
	s_lshl_b32 s6, s0, 19
	s_and_b32 s9, s6, 0x380000
	s_lshl_b64 s[6:7], s[4:5], 22
	s_add_u32 s6, s16, s6
	s_addc_u32 s7, s17, s7
	s_add_u32 s6, s6, s9
	s_addc_u32 s7, s7, 0
	s_add_u32 s6, s6, s8
	s_addc_u32 s7, s7, 0
	s_add_u32 s6, s6, 0x24dff000
	s_addc_u32 s7, s7, 0
	s_mov_b64 s[8:9], 0

.LBB0_947:
	s_add_i32 s8, s62, 1
	s_cmp_lt_i32 s62, 3
	s_cselect_b32 s0, 0x80, s9
	v_mul_i32_i24_e32 v96, s0, v191
	v_or_b32_e32 v96, v96, v189
	v_ashrrev_i32_e32 v97, 31, v96
	s_cselect_b32 s5, s20, s7
	s_cselect_b32 s4, s19, s6
	v_lshlrev_b64 v[120:121], 11, v[96:97]
	v_add_u32_e32 v98, v107, v190
	v_add_u32_e32 v99, v107, v108
	v_lshl_add_u64 v[120:121], s[4:5], 0, v[120:121]
	ds_read_b32 v116, v98
	ds_read_b32 v117, v98 offset:1040
	ds_read_b32 v118, v98 offset:2080
	ds_read_b32 v119, v98 offset:3120
	ds_read_b32 v96, v99
	ds_read_b32 v97, v99 offset:1040
	ds_read_b32 v98, v99 offset:2080
	ds_read_b32 v99, v99 offset:3120
	v_lshl_add_u64 v[120:121], v[120:121], 0, v[100:101]
	s_mov_b64 s[6:7], 0
	s_waitcnt lgkmcnt(4)
	global_store_dwordx4 v[120:121], v[116:119], off
.LBB0_948:
	s_and_b64 vcc, exec, s[6:7]
	s_cbranch_vccz .LBB0_957
	s_waitcnt vmcnt(8)
	v_mul_f32_e32 v1, v48, v114
	v_mul_f32_e32 v2, v52, v114
	v_mov_b32_e32 v0, v103
	v_cvt_pk_fp8_f32 v0, v1, v2
	v_mul_f32_e32 v2, v49, v114
	s_waitcnt vmcnt(7)
	v_mul_f32_e32 v5, v53, v114
	v_mov_b32_e32 v1, v103
	v_cvt_pk_fp8_f32 v1, v2, v5
	v_mul_f32_e32 v3, v64, v114
	s_waitcnt vmcnt(6)
	v_mul_f32_e32 v4, v68, v114
	v_cvt_pk_fp8_f32 v0, v3, v4 op_sel:[0,0,1]
	v_mul_f32_e32 v2, v65, v114
	v_mul_f32_e32 v3, v69, v114
	v_cvt_pk_fp8_f32 v1, v2, v3 op_sel:[0,0,1]
	v_mul_f32_e32 v3, v50, v114
	v_mul_f32_e32 v4, v54, v114
	v_mov_b32_e32 v2, v103
	v_cvt_pk_fp8_f32 v2, v3, v4
	v_mul_f32_e32 v4, v51, v114
	v_mul_f32_e32 v7, v55, v114
	v_mov_b32_e32 v3, v103
	v_cvt_pk_fp8_f32 v3, v4, v7
	v_mul_f32_e32 v5, v66, v114
	v_mul_f32_e32 v6, v70, v114
	v_cvt_pk_fp8_f32 v2, v5, v6 op_sel:[0,0,1]
	v_mul_f32_e32 v4, v67, v114
	v_mul_f32_e32 v5, v71, v114
	v_cvt_pk_fp8_f32 v3, v4, v5 op_sel:[0,0,1]
	s_waitcnt vmcnt(5)
	v_mul_f32_e32 v5, v40, v114
	s_waitcnt vmcnt(4)
	v_mul_f32_e32 v6, v114, v44
	v_mov_b32_e32 v4, v103
	v_cvt_pk_fp8_f32 v4, v5, v6
	v_mul_f32_e32 v6, v41, v114
	v_mul_f32_e32 v41, v114, v45
	v_mov_b32_e32 v5, v103
	v_cvt_pk_fp8_f32 v5, v6, v41
	s_waitcnt vmcnt(3)
	v_mul_f32_e32 v7, v114, v56
	s_waitcnt vmcnt(2)
	v_mul_f32_e32 v40, v114, v60
	v_cvt_pk_fp8_f32 v4, v7, v40 op_sel:[0,0,1]
	v_mul_f32_e32 v6, v114, v57
	v_mul_f32_e32 v7, v114, v61
	v_cvt_pk_fp8_f32 v5, v6, v7 op_sel:[0,0,1]
	v_mul_f32_e32 v7, v42, v114
	v_mul_f32_e32 v40, v114, v46
	v_mov_b32_e32 v6, v103
	v_cvt_pk_fp8_f32 v6, v7, v40
	v_mul_f32_e32 v40, v43, v114
	v_mul_f32_e32 v43, v114, v47
	v_mov_b32_e32 v7, v103
	s_min_i32 s0, s62, s59
	v_cvt_pk_fp8_f32 v7, v40, v43
	s_mul_i32 s0, s0, s3
	s_add_i32 s0, s0, s2
	v_mul_f32_e32 v41, v114, v58
	v_mul_f32_e32 v42, v114, v62
	s_mul_hi_i32 s4, s0, 0x2aaaaaab
	v_cvt_pk_fp8_f32 v6, v41, v42 op_sel:[0,0,1]
	v_mul_f32_e32 v40, v114, v59
	v_mul_f32_e32 v41, v114, v63
	s_lshr_b32 s5, s4, 31
	s_ashr_i32 s4, s4, 7
	v_cvt_pk_fp8_f32 v7, v40, v41 op_sel:[0,0,1]
	s_add_i32 s5, s4, s5
	s_add_i32 s4, s5, 18
	s_mulk_i32 s5, 0x300
	v_add_u32_e32 v40, v110, v105
	s_sub_i32 s22, s0, s5
	ds_write_b128 v40, v[0:3]
	v_add_u32_e32 v0, v110, v106
	s_cmpk_gt_i32 s22, 0x1ff
	s_mov_b64 s[10:11], -1
	ds_write_b128 v0, v[4:7]
	s_cbranch_scc0 .LBB0_951
	s_load_dwordx2 s[6:7], s[14:15], 0x110
	s_ashr_i32 s5, s4, 31
	s_lshl_b64 s[8:9], s[4:5], 24
	s_mov_b64 s[10:11], 0
	s_waitcnt lgkmcnt(0)
	s_add_u32 s6, s6, s8
	s_addc_u32 s7, s7, s9
	s_lshl_b32 s0, s22, 3
	s_and_b32 s0, s0, 0x7fffffc0
	s_addk_i32 s0, 0xf000
	s_mov_b64 s[8:9], s[0:1]

.LBB0_953:
	s_lshl_b64 s[4:5], s[8:9], 13
	s_add_u32 s4, s6, s4
	s_addc_u32 s5, s7, s5
	s_lshl_b32 s0, s22, s0
	s_and_b32 s0, s0, 0x700
	s_lshl_b32 s0, s0, 2
	s_add_u32 s4, s4, s0
	s_addc_u32 s5, s5, 0
	s_cmp_gt_i32 s62, s59
	s_cselect_b64 s[6:7], -1, 0
	v_cndmask_b32_e64 v0, v180, 0, s[6:7]
	s_and_b64 s[6:7], s[6:7], exec
	s_cselect_b32 s0, 0, 0x800
	v_lshlrev_b32_e32 v102, 2, v0
	v_lshl_add_u64 v[0:1], s[4:5], 0, v[102:103]
	v_mad_i64_i32 v[2:3], s[4:5], s0, v181, 0
	v_lshl_add_u64 v[2:3], v[2:3], 2, v[0:1]
	v_mad_i64_i32 v[4:5], s[4:5], s0, v182, 0
	v_lshl_add_u64 v[4:5], v[4:5], 2, v[0:1]
	global_load_dwordx4 v[48:51], v[2:3], off nt
	global_load_dwordx4 v[52:55], v[4:5], off nt
	v_mad_i64_i32 v[2:3], s[4:5], s0, v183, 0
	v_lshl_add_u64 v[2:3], v[2:3], 2, v[0:1]
	v_mad_i64_i32 v[4:5], s[4:5], s0, v184, 0
	v_lshl_add_u64 v[4:5], v[4:5], 2, v[0:1]
	global_load_dwordx4 v[64:67], v[2:3], off nt
	global_load_dwordx4 v[68:71], v[4:5], off nt
	v_mad_i64_i32 v[2:3], s[4:5], s0, v185, 0
	v_lshl_add_u64 v[2:3], v[2:3], 2, v[0:1]
	v_mad_i64_i32 v[4:5], s[4:5], s0, v186, 0
	v_lshl_add_u64 v[4:5], v[4:5], 2, v[0:1]
	global_load_dwordx4 v[40:43], v[2:3], off nt
	global_load_dwordx4 v[44:47], v[4:5], off nt
	v_mad_i64_i32 v[2:3], s[4:5], s0, v187, 0
	v_lshl_add_u64 v[2:3], v[2:3], 2, v[0:1]
	v_mad_i64_i32 v[4:5], s[4:5], s0, v188, 0
	v_lshl_add_u64 v[0:1], v[4:5], 2, v[0:1]
	global_load_dwordx4 v[56:59], v[2:3], off nt
	global_load_dwordx4 v[60:63], v[0:1], off nt
	s_max_i32 s0, s62, 3
	s_add_i32 s0, s0, -3
	s_min_i32 s0, s0, s59
	s_mul_i32 s0, s0, s3
	s_add_i32 s0, s0, s2
	s_mul_hi_i32 s4, s0, 0x2aaaaaab
	s_lshr_b32 s5, s4, 31
	s_ashr_i32 s4, s4, 7
	s_add_i32 s5, s4, s5
	s_add_i32 s4, s5, 18
	s_mulk_i32 s5, 0x300
	s_sub_i32 s0, s0, s5
	s_ashr_i32 s5, s4, 31
	s_cmpk_gt_i32 s0, 0x1ff
	s_mov_b64 s[8:9], -1
	s_cbranch_scc0 .LBB0_955
	s_lshl_b32 s6, s0, 3
	s_and_b32 s8, s6, 0x7fffffc0
	s_lshl_b32 s6, s0, 19
	s_and_b32 s9, s6, 0x380000
	s_lshl_b64 s[6:7], s[4:5], 22
	s_add_u32 s6, s16, s6
	s_addc_u32 s7, s17, s7
	s_add_u32 s6, s6, s9
	s_addc_u32 s7, s7, 0
	s_add_u32 s6, s6, s8
	s_addc_u32 s7, s7, 0
	s_add_u32 s6, s6, 0x24dff000
	s_addc_u32 s7, s7, 0
	s_mov_b64 s[8:9], 0

	.amdhsa_kernel _Z6mk_fwd4Args
		.amdhsa_group_segment_fixed_size 0
		.amdhsa_private_segment_fixed_size 0
		.amdhsa_kernarg_size 584
		.amdhsa_user_sgpr_count 2
		.amdhsa_user_sgpr_dispatch_ptr 0
		.amdhsa_user_sgpr_queue_ptr 0
		.amdhsa_user_sgpr_kernarg_segment_ptr 1
		.amdhsa_user_sgpr_dispatch_id 0
		.amdhsa_user_sgpr_kernarg_preload_length 0
		.amdhsa_user_sgpr_kernarg_preload_offset 0
		.amdhsa_user_sgpr_private_segment_size 0
		.amdhsa_uses_dynamic_stack 0
		.amdhsa_enable_private_segment 0
		.amdhsa_system_sgpr_workgroup_id_x 1
		.amdhsa_system_sgpr_workgroup_id_y 0
		.amdhsa_system_sgpr_workgroup_id_z 0
		.amdhsa_system_sgpr_workgroup_info 0
		.amdhsa_system_vgpr_workitem_id 0
		.amdhsa_next_free_vgpr 256
		.amdhsa_next_free_sgpr 102
		.amdhsa_accum_offset 256
		.amdhsa_reserve_vcc 1
		.amdhsa_float_round_mode_32 0
		.amdhsa_float_round_mode_16_64 0
		.amdhsa_float_denorm_mode_32 3
		.amdhsa_float_denorm_mode_16_64 3
		.amdhsa_dx10_clamp 1
		.amdhsa_ieee_mode 1
		.amdhsa_fp16_overflow 0
		.amdhsa_tg_split 0
		.amdhsa_exception_fp_ieee_invalid_op 0
		.amdhsa_exception_fp_denorm_src 0
		.amdhsa_exception_fp_ieee_div_zero 0
		.amdhsa_exception_fp_ieee_overflow 0
		.amdhsa_exception_fp_ieee_underflow 0
		.amdhsa_exception_fp_ieee_inexact 0
		.amdhsa_exception_int_div_zero 0
	.end_amdhsa_kernel

.Lfunc_end0:
	.size	_Z6mk_fwd4Args, .Lfunc_end0-_Z6mk_fwd4Args
	.set _Z6mk_fwd4Args.num_vgpr, 256
	.set _Z6mk_fwd4Args.num_agpr, 0
	.set _Z6mk_fwd4Args.numbered_sgpr, 102
	.set _Z6mk_fwd4Args.num_named_barrier, 0
	.set _Z6mk_fwd4Args.private_seg_size, 0
	.set _Z6mk_fwd4Args.uses_vcc, 1
	.set _Z6mk_fwd4Args.uses_flat_scratch, 0
	.set _Z6mk_fwd4Args.has_dyn_sized_stack, 0
	.set _Z6mk_fwd4Args.has_recursion, 0
	.set _Z6mk_fwd4Args.has_indirect_call, 0

amdhsa.kernels:
  - .agpr_count:     0
    .args:
      - .offset:         0
        .size:           328
        .value_kind:     by_value
      - .offset:         328
        .size:           4
        .value_kind:     hidden_block_count_x
      - .offset:         332
        .size:           4
        .value_kind:     hidden_block_count_y
      - .offset:         336
        .size:           4
        .value_kind:     hidden_block_count_z
      - .offset:         340
        .size:           2
        .value_kind:     hidden_group_size_x
      - .offset:         342
        .size:           2
        .value_kind:     hidden_group_size_y
      - .offset:         344
        .size:           2
        .value_kind:     hidden_group_size_z
      - .offset:         346
        .size:           2
        .value_kind:     hidden_remainder_x
      - .offset:         348
        .size:           2
        .value_kind:     hidden_remainder_y
      - .offset:         350
        .size:           2
        .value_kind:     hidden_remainder_z
      - .offset:         368
        .size:           8
        .value_kind:     hidden_global_offset_x
      - .offset:         376
        .size:           8
        .value_kind:     hidden_global_offset_y
      - .offset:         384
        .size:           8
        .value_kind:     hidden_global_offset_z
      - .offset:         392
        .size:           2
        .value_kind:     hidden_grid_dims
      - .offset:         448
        .size:           4
        .value_kind:     hidden_dynamic_lds_size
    .group_segment_fixed_size: 0
    .kernarg_segment_align: 8
    .kernarg_segment_size: 584
    .language:       OpenCL C
    .language_version:
      - 2
      - 0
    .max_flat_workgroup_size: 512
    .name:           _Z6mk_fwd4Args
    .private_segment_fixed_size: 0
    .sgpr_count:     108
    .sgpr_spill_count: 35
    .symbol:         _Z6mk_fwd4Args.kd
    .uniform_work_group_size: 1
    .uses_dynamic_stack: false
    .vgpr_count:     256
    .vgpr_spill_count: 0
    .wavefront_size: 64
